# v91 + lever 4: one static s_setprio 1 for waves 4-7 at kernel entry, all per-segment s_setprio toggles in the GEMM K-loops removed
# baseline (speedup 1.0000x reference)
.LBB0_15:
	s_or_b64 exec, exec, s[6:7]
	v_readlane_b32 s23, v252, 0
	s_ashr_i32 s6, s23, 31
	v_writelane_b32 v252, s6, 5
	s_lshr_b32 s6, s6, 29
	s_add_i32 s6, s23, s6
	s_ashr_i32 s24, s6, 3
	s_lshr_b32 s10, s8, 6
	s_mul_i32 s7, s24, 0xffffff01
	v_writelane_b32 v252, s10, 6
	s_cmp_lt_u32 s10, 4
	s_cbranch_scc1 .Lprio_skip
	s_setprio 1
.Lprio_skip:
	s_lshl_b32 s10, s23, 5
	s_add_i32 s12, s7, s10
	s_lshl_b32 s7, s12, 3
	s_add_u32 s0, s0, 0x110
	v_writelane_b32 v252, s7, 7
	s_addc_u32 s1, s1, 0
	v_writelane_b32 v252, s0, 8
	s_mov_b32 s38, 0x6dc9c883
	v_mov_b32_e32 v161, 0
	v_writelane_b32 v252, s1, 9
	v_mov_b32_e32 v240, 0x358637bd
	v_readlane_b32 s10, v252, 1
	v_readlane_b32 s11, v252, 2
	s_add_u32 s0, s10, 0x4200
	s_addc_u32 s1, s11, 0
	v_writelane_b32 v252, s0, 10
	s_mov_b32 s39, 0x3fc45f30
	v_mov_b32_e32 v225, 0x3c0881c4
	v_writelane_b32 v252, s1, 11
	s_add_u32 s0, s10, 0x4400
	s_addc_u32 s1, s11, 0
	v_writelane_b32 v252, s0, 12
	v_mov_b32_e32 v226, 0xbab64f3b
	v_mov_b32_e32 v245, 0x3b808081
	v_writelane_b32 v252, s1, 13
	s_add_u32 s0, s10, 0x4500
	s_addc_u32 s1, s11, 0
	v_writelane_b32 v252, s0, 14
	v_mov_b32_e32 v242, 0x7f800000
	v_not_b32_e32 v227, 63
	v_writelane_b32 v252, s1, 15
	s_add_u32 s0, s10, 0x4600
	s_addc_u32 s1, s11, 0
	v_writelane_b32 v252, s0, 16
	v_not_b32_e32 v250, 31
	v_mov_b32_e32 v251, 0x7fc00000
	v_writelane_b32 v252, s1, 17
	s_add_u32 s0, s10, 0x4700
	s_addc_u32 s1, s11, 0
	v_writelane_b32 v252, s0, 18
	v_mov_b32_e32 v243, 0xc2700000
	s_movk_i32 s76, 0x1a00
	v_writelane_b32 v252, s1, 19
	s_add_u32 s0, s10, 0x4800
	s_addc_u32 s1, s11, 0
	v_writelane_b32 v252, s0, 20
	s_mov_b32 s67, 0x6468000
	s_mov_b32 s72, 0
	v_writelane_b32 v252, s1, 21
	s_add_u32 s0, s10, 0x4900
	s_addc_u32 s1, s11, 0
	v_writelane_b32 v252, s0, 22
	s_mov_b32 s97, 0
	v_writelane_b32 v255, s97, 62
	s_mov_b64 s[84:85], -1
	v_writelane_b32 v252, s1, 23
	s_add_u32 s0, s10, 0x4a00
	s_addc_u32 s1, s11, 0
	v_writelane_b32 v252, s0, 24
	s_mov_b64 s[60:61], 0x40000
	s_mov_b64 s[52:53], 0x60000
	v_writelane_b32 v252, s1, 25
	s_add_u32 s0, s10, 0x4b00
	s_addc_u32 s1, s11, 0
	v_writelane_b32 v252, s0, 26
	s_mov_b64 s[56:57], 0x80
	s_mov_b64 s[26:27], 0x60080
	v_writelane_b32 v252, s1, 27
	s_add_u32 s0, s10, 0x4c00
	s_addc_u32 s1, s11, 0
	v_writelane_b32 v252, s0, 28
	s_mov_b32 s30, 0x3b800000
	s_mov_b64 s[28:29], 0x10080
	v_writelane_b32 v252, s1, 29
	s_add_u32 s0, s10, 0x4d00
	s_addc_u32 s1, s11, 0
	v_writelane_b32 v252, s0, 30
	s_mov_b32 s62, 0x3e38aa3b
	s_mov_b32 s66, 0x3e16c740
	v_writelane_b32 v252, s1, 31
	s_add_u32 s0, s10, 0x4e00
	s_addc_u32 s1, s11, 0
	v_writelane_b32 v252, s0, 32
	s_mov_b64 s[68:69], 0x2a400
	s_mov_b64 s[70:71], 0x2be00
	v_writelane_b32 v252, s1, 33
	s_add_u32 s0, s10, 0x4f00
	s_addc_u32 s1, s11, 0
	v_writelane_b32 v252, s0, 34
	s_mov_b32 s82, 0x3b808081
	s_mov_b32 s94, 0x37800000
	v_writelane_b32 v252, s1, 35
	s_add_u32 s0, s10, 0x5000
	s_addc_u32 s1, s11, 0
	v_writelane_b32 v252, s0, 36
	s_waitcnt lgkmcnt(0)
	s_barrier
	v_writelane_b32 v252, s1, 37
	s_add_u32 s0, s10, 0x5100
	s_addc_u32 s1, s11, 0
	v_writelane_b32 v252, s0, 38
	s_nop 1
	v_writelane_b32 v252, s1, 39
	s_add_u32 s0, s10, 0x5200
	s_addc_u32 s1, s11, 0
	v_writelane_b32 v252, s0, 40
	s_nop 1
	v_writelane_b32 v252, s1, 41
	s_add_u32 s0, s10, 0x5300
	s_addc_u32 s1, s11, 0
	v_writelane_b32 v252, s0, 42
	s_cmp_eq_u32 s9, 15
	s_nop 0
	v_writelane_b32 v252, s1, 43
	s_cselect_b64 s[0:1], -1, 0
	v_writelane_b32 v252, s0, 44
	s_cmp_eq_u32 s9, 14
	s_nop 0
	v_writelane_b32 v252, s1, 45
	s_cselect_b64 s[0:1], -1, 0
	v_writelane_b32 v252, s0, 46
	s_cmp_eq_u32 s9, 13
	s_nop 0
	v_writelane_b32 v252, s1, 47
	s_cselect_b64 s[0:1], -1, 0
	v_writelane_b32 v252, s0, 48
	s_cmp_eq_u32 s9, 12
	s_nop 0
	v_writelane_b32 v252, s1, 49
	s_cselect_b64 s[0:1], -1, 0
	v_writelane_b32 v252, s0, 50
	s_cmp_eq_u32 s9, 11
	s_nop 0
	v_writelane_b32 v252, s1, 51
	s_cselect_b64 s[0:1], -1, 0
	v_writelane_b32 v252, s0, 52
	s_cmp_eq_u32 s9, 10
	s_nop 0
	v_writelane_b32 v252, s1, 53
	s_cselect_b64 s[0:1], -1, 0
	v_writelane_b32 v252, s0, 54
	s_cmp_eq_u32 s9, 9
	s_nop 0
	v_writelane_b32 v252, s1, 55
	s_cselect_b64 s[0:1], -1, 0
	v_writelane_b32 v252, s0, 56
	s_cmp_eq_u32 s9, 8
	s_nop 0
	v_writelane_b32 v252, s1, 57
	s_cselect_b64 s[0:1], -1, 0
	v_writelane_b32 v252, s0, 58
	s_cmp_eq_u32 s9, 7
	s_nop 0
	v_writelane_b32 v252, s1, 59
	s_cselect_b64 s[0:1], -1, 0
	v_writelane_b32 v252, s0, 60
	s_cmp_eq_u32 s9, 6
	s_nop 0
	v_writelane_b32 v252, s1, 61
	s_cselect_b64 s[0:1], -1, 0
	v_writelane_b32 v252, s0, 62
	s_cmp_eq_u32 s9, 5
	s_nop 0
	v_writelane_b32 v252, s1, 63
	s_cselect_b64 s[0:1], -1, 0
	v_writelane_b32 v253, s0, 0
	s_cmp_eq_u32 s9, 4
	s_nop 0
	v_writelane_b32 v253, s1, 1
	s_cselect_b64 s[0:1], -1, 0
	v_writelane_b32 v253, s0, 2
	s_cmp_eq_u32 s9, 3
	s_nop 0
	v_writelane_b32 v253, s1, 3
	s_cselect_b64 s[0:1], -1, 0
	v_writelane_b32 v253, s0, 4
	s_cmp_eq_u32 s9, 2
	s_nop 0
	v_writelane_b32 v253, s1, 5
	s_cselect_b64 s[0:1], -1, 0
	v_writelane_b32 v253, s0, 6
	s_cmp_eq_u32 s9, 1
	s_nop 0
	v_writelane_b32 v253, s1, 7
	s_cselect_b64 s[0:1], -1, 0
	v_writelane_b32 v253, s0, 8
	s_cmp_eq_u32 s9, 0
	s_nop 0
	v_writelane_b32 v253, s1, 9
	s_cselect_b64 s[0:1], -1, 0
	v_writelane_b32 v253, s0, 10
	s_nop 1
	v_writelane_b32 v253, s1, 11
	s_lshl_b32 s0, s9, 8
	s_add_u32 s0, s4, s0
	s_addc_u32 s1, s5, 0
	s_add_u32 s4, s0, 0x1400
	s_addc_u32 s5, s1, 0
	v_writelane_b32 v253, s4, 12
	s_add_u32 s0, s0, 0x2400
	s_addc_u32 s1, s1, 0
	v_writelane_b32 v253, s5, 13
	v_writelane_b32 v253, s0, 14
	s_nop 1
	v_writelane_b32 v253, s1, 15
	s_add_u32 s0, s10, 0x7400
	s_addc_u32 s1, s11, 0
	v_writelane_b32 v253, s0, 16
	s_nop 1
	v_writelane_b32 v253, s1, 17
	s_add_u32 s0, s10, 0x7500
	s_addc_u32 s1, s11, 0
	v_writelane_b32 v253, s0, 18
	s_nop 1
	v_writelane_b32 v253, s1, 19
	s_and_b32 s0, s8, 0xffffffc0
	s_cmpk_lt_i32 s23, 0x680
	v_writelane_b32 v253, s0, 20
	s_cselect_b64 s[0:1], -1, 0
	v_writelane_b32 v253, s0, 21
	s_nop 1
	v_writelane_b32 v253, s1, 22
	s_add_i32 s0, s23, 0x80
	s_ashr_i32 s1, s0, 31
	s_lshr_b32 s1, s1, 24
	s_add_i32 s1, s0, s1
	s_and_b32 s1, s1, 0xffffff00
	s_sub_i32 s7, s0, s1
	s_and_b32 s0, s6, -8
	s_sub_i32 s16, s23, s0
	s_cmp_lt_i32 s7, 64
	s_sext_i32_i16 s1, s7
	s_cselect_b64 s[4:5], -1, 0
	s_bfe_u32 s1, s1, 0x3001c
	v_writelane_b32 v253, s4, 23
	s_add_i32 s1, s7, s1
	s_ashr_i32 s6, s7, 31
	v_writelane_b32 v253, s5, 24
	s_sext_i32_i16 s4, s1
	s_and_b32 s1, s1, 0xfff8
	s_sub_i32 s1, s7, s1
	s_ashr_i32 s4, s4, 3
	s_lshl_b32 s5, s1, 3
	v_writelane_b32 v253, s7, 25
	s_cmpk_lt_i32 s23, 0x380
	v_writelane_b32 v253, s6, 26
	s_cselect_b64 s[6:7], -1, 0
	v_writelane_b32 v253, s6, 27
	s_cmpk_lt_i32 s12, 0x200
	s_nop 0
	v_writelane_b32 v253, s7, 28
	s_cselect_b64 s[6:7], -1, 0
	v_writelane_b32 v253, s6, 29
	s_cmpk_gt_u32 s8, 0xff
	s_nop 0
	v_writelane_b32 v253, s7, 30
	s_cselect_b64 s[6:7], -1, 0
	v_writelane_b32 v253, s6, 31
	s_cmpk_lt_i32 s23, 0x800
	s_nop 0
	v_writelane_b32 v253, s7, 32
	s_cselect_b64 s[6:7], -1, 0
	v_writelane_b32 v253, s6, 33
	s_nop 1
	v_writelane_b32 v253, s7, 34
	s_lshl_b32 s6, s16, 8
	s_cmpk_lt_i32 s23, 0x200
	s_cselect_b64 s[8:9], -1, 0
	s_lshl_b32 s7, s16, 6
	v_writelane_b32 v253, s8, 35
	s_cmpk_lt_i32 s23, 0xe00
	s_cselect_b64 s[10:11], -1, 0
	v_writelane_b32 v253, s9, 36
	s_mul_hi_i32 s8, s23, 0x92492493
	v_writelane_b32 v253, s10, 37
	s_add_i32 s8, s8, s23
	s_lshr_b32 s9, s8, 31
	v_writelane_b32 v253, s11, 38
	v_writelane_b32 v253, s8, 39
	s_ashr_i32 s8, s8, 2
	v_writelane_b32 v253, s9, 40
	s_add_i32 s8, s8, s9
	v_writelane_b32 v253, s8, 41
	s_add_i32 s0, s0, 0xffb0
	s_mul_i32 s8, s8, 7
	v_writelane_b32 v253, s0, 42
	s_sub_i32 s8, s23, s8
	v_writelane_b32 v253, s12, 43
	s_lshl_b32 s0, s12, 7
	s_ashr_i32 s9, s8, 31
	v_writelane_b32 v253, s0, 44
	s_mov_b32 s0, s8
	v_writelane_b32 v253, s0, 45
	s_lshl_b64 s[8:9], s[8:9], 9
	s_cmp_lt_i32 s16, 0
	v_writelane_b32 v253, s1, 46
	s_mul_i32 s0, s16, 0x101
	s_cselect_b32 s0, s0, s6
	s_mul_i32 s6, s16, 0x41
	s_cselect_b32 s6, s6, s7
	s_movk_i32 s7, 0xd1
	v_writelane_b32 v253, s8, 47
	s_cselect_b32 s7, s7, 0xd0
	s_mul_i32 s7, s16, s7
	v_writelane_b32 v253, s9, 48
	s_movk_i32 s8, 0x71
	s_movk_i32 s9, 0x1c1
	s_cselect_b32 s8, s8, 0x70
	s_cselect_b32 s9, s9, 0x1c0
	s_add_i32 s7, s7, s24
	s_mul_hi_i32 s10, s7, 0x4ec4ec4f
	s_lshr_b32 s11, s10, 31
	s_ashr_i32 s10, s10, 5
	s_add_i32 s10, s10, s11
	s_mul_i32 s11, s10, 0x68
	s_lshl_b32 s10, s10, 3
	s_sub_i32 s7, s7, s11
	s_sub_i32 s11, 0x80, s10
	s_min_i32 s11, s11, 8
	s_sext_i32_i16 s12, s1
	s_cmp_lt_i32 s12, 0
	s_mul_i32 s1, s1, 9
	s_cselect_b32 s1, s1, s5
	s_add_i32 s1, s1, s4
	s_bfe_i32 s4, s1, 0x80000
	s_bfe_u32 s4, s4, 0x5000a
	s_add_i32 s4, s1, s4
	s_and_b32 s5, s4, 0xffe0
	s_sub_i32 s1, s1, s5
	s_bfe_i32 s5, s1, 0x80000
	s_bfe_u32 s5, s5, 0x3000c
	s_add_i32 s5, s1, s5
	s_mul_i32 s8, s16, s8
	s_and_b32 s12, s5, 0xf8
	s_add_i32 s8, s8, s24
	s_sub_i32 s1, s1, s12
	s_mul_hi_i32 s12, s8, 0x92492493
	s_add_i32 s12, s12, s8
	s_lshr_b32 s13, s12, 31
	s_ashr_i32 s12, s12, 5
	s_add_i32 s12, s12, s13
	s_mul_i32 s13, s12, 56
	s_add_i32 s0, s0, s24
	s_sub_i32 s8, s8, s13
	s_ashr_i32 s13, s0, 31
	s_lshr_b32 s13, s13, 25
	s_add_i32 s13, s0, s13
	s_and_b32 s14, s13, 0xffffff80
	s_add_i32 s6, s6, s24
	s_sub_i32 s0, s0, s14
	s_ashr_i32 s14, s6, 31
	s_lshr_b32 s14, s14, 27
	s_add_i32 s14, s6, s14
	s_mul_i32 s9, s16, s9
	s_and_b32 s15, s14, 0xffffffe0
	s_add_i32 s9, s9, s24
	s_sub_i32 s6, s6, s15
	s_mul_hi_i32 s15, s9, 0x92492493
	s_add_i32 s15, s15, s9
	v_writelane_b32 v253, s16, 49
	s_lshr_b32 s16, s15, 31
	s_ashr_i32 s15, s15, 7
	s_add_i32 s15, s15, s16
	s_mul_i32 s16, s15, 0xe0
	s_sub_i32 s9, s9, s16
	s_abs_i32 s16, s11
	v_cvt_f32_u32_e32 v0, s16
	s_bfe_i32 s4, s4, 0x80000
	s_sub_i32 s17, 0, s16
	s_sext_i32_i16 s4, s4
	v_rcp_iflag_f32_e32 v0, v0
	s_ashr_i32 s4, s4, 5
	s_lshl_b32 s4, s4, 3
	s_bfe_i32 s5, s5, 0x80000
	v_mul_f32_e32 v0, 0x4f7ffffe, v0
	v_cvt_u32_f32_e32 v0, v0
	s_sext_i32_i8 s1, s1
	s_sext_i32_i16 s5, s5
	s_add_i32 s4, s4, s1
	v_readfirstlane_b32 s18, v0
	s_mul_i32 s17, s17, s18
	s_mul_hi_u32 s17, s18, s17
	s_add_i32 s18, s18, s17
	s_abs_i32 s17, s7
	s_mul_hi_u32 s18, s17, s18
	v_writelane_b32 v253, s4, 50
	s_lshl_b32 s1, s12, 3
	s_ashr_i32 s12, s13, 7
	s_ashr_i32 s14, s14, 5
	s_mul_i32 s19, s18, s16
	v_writelane_b32 v253, s5, 51
	s_lshl_b32 s12, s12, 3
	s_lshl_b32 s14, s14, 3
	s_lshl_b32 s15, s15, 3
	s_ashr_i32 s22, s5, 3
	s_sub_i32 s17, s17, s19
	s_sub_i32 s4, 0x80, s1
	s_sub_i32 s13, 0x80, s12
	s_sub_i32 s19, 0x80, s14
	s_sub_i32 s20, 0x80, s15
	s_xor_b32 s21, s7, s11
	v_writelane_b32 v253, s22, 52
	s_min_i32 s4, s4, 8
	s_min_i32 s13, s13, 8
	s_min_i32 s19, s19, 8
	s_min_i32 s20, s20, 8
	s_ashr_i32 s21, s21, 31
	v_writelane_b32 v253, s23, 53
	s_add_i32 s5, s18, 1
	s_sub_i32 s22, s17, s16
	s_cmp_ge_u32 s17, s16
	s_cselect_b32 s5, s5, s18
	s_cselect_b32 s17, s22, s17
	s_add_i32 s18, s5, 1
	s_cmp_ge_u32 s17, s16
	s_cselect_b32 s5, s18, s5
	s_xor_b32 s5, s5, s21
	s_sub_i32 s18, s5, s21
	s_mul_i32 s5, s18, s11
	s_sub_i32 s5, s7, s5
	s_abs_i32 s7, s4
	v_cvt_f32_u32_e32 v0, s7
	s_mov_b32 s16, s18
	v_writelane_b32 v253, s16, 54
	s_sub_i32 s11, 0, s7
	v_rcp_iflag_f32_e32 v0, v0
	v_writelane_b32 v253, s17, 55
	s_add_i32 s10, s10, s5
	s_xor_b32 s5, s8, s4
	v_mul_f32_e32 v0, 0x4f7ffffe, v0
	v_cvt_u32_f32_e32 v0, v0
	s_ashr_i32 s5, s5, 31
	v_readfirstlane_b32 s16, v0
	s_mul_i32 s11, s11, s16
	s_mul_hi_u32 s11, s16, s11
	s_add_i32 s16, s16, s11
	s_abs_i32 s11, s8
	s_mul_hi_u32 s16, s11, s16
	s_mul_i32 s17, s16, s7
	s_sub_i32 s11, s11, s17
	v_writelane_b32 v253, s10, 56
	s_sub_i32 s17, s11, s7
	s_nop 0
	v_writelane_b32 v253, s11, 57
	s_add_i32 s10, s16, 1
	s_cmp_ge_u32 s11, s7
	s_cselect_b32 s10, s10, s16
	s_cselect_b32 s11, s17, s11
	s_add_i32 s16, s10, 1
	s_cmp_ge_u32 s11, s7
	s_cselect_b32 s7, s16, s10
	s_xor_b32 s7, s7, s5
	s_sub_i32 s5, s7, s5
	v_writelane_b32 v253, s5, 58
	s_mul_i32 s4, s5, s4
	s_abs_i32 s5, s13
	v_cvt_f32_u32_e32 v0, s5
	s_sub_i32 s4, s8, s4
	s_sub_i32 s7, 0, s5
	s_add_i32 s4, s1, s4
	v_rcp_iflag_f32_e32 v0, v0
	s_xor_b32 s1, s0, s13
	s_ashr_i32 s1, s1, 31
	s_mov_b64 s[16:17], 0x30000
	v_mul_f32_e32 v0, 0x4f7ffffe, v0
	v_cvt_u32_f32_e32 v0, v0
	s_nop 0
	v_readfirstlane_b32 s8, v0
	s_mul_i32 s7, s7, s8
	s_mul_hi_u32 s7, s8, s7
	s_add_i32 s8, s8, s7
	s_abs_i32 s7, s0
	s_mul_hi_u32 s8, s7, s8
	s_mul_i32 s10, s8, s5
	s_sub_i32 s7, s7, s10
	v_writelane_b32 v253, s4, 59
	s_sub_i32 s10, s7, s5
	s_nop 0
	v_writelane_b32 v253, s5, 60
	s_add_i32 s4, s8, 1
	s_cmp_ge_u32 s7, s5
	s_cselect_b32 s4, s4, s8
	s_cselect_b32 s7, s10, s7
	s_add_i32 s8, s4, 1
	s_cmp_ge_u32 s7, s5
	s_cselect_b32 s4, s8, s4
	s_xor_b32 s4, s4, s1
	s_sub_i32 s8, s4, s1
	s_mul_i32 s1, s8, s13
	s_sub_i32 s0, s0, s1
	s_abs_i32 s1, s19
	v_cvt_f32_u32_e32 v0, s1
	s_mov_b32 s4, s8
	v_writelane_b32 v253, s4, 61
	s_add_i32 s0, s12, s0
	v_rcp_iflag_f32_e32 v0, v0
	v_writelane_b32 v253, s5, 62
	s_sub_i32 s4, 0, s1
	v_mul_f32_e32 v0, 0x4f7ffffe, v0
	v_cvt_u32_f32_e32 v0, v0
	s_nop 0
	v_readfirstlane_b32 s5, v0
	s_mul_i32 s4, s4, s5
	s_mul_hi_u32 s4, s5, s4
	s_add_i32 s5, s5, s4
	s_abs_i32 s4, s6
	s_mul_hi_u32 s5, s4, s5
	s_mul_i32 s7, s5, s1
	v_writelane_b32 v253, s0, 63
	s_sub_i32 s4, s4, s7
	s_add_i32 s7, s5, 1
	v_writelane_b32 v254, s1, 0
	s_xor_b32 s0, s6, s19
	s_ashr_i32 s0, s0, 31
	s_sub_i32 s8, s4, s1
	s_cmp_ge_u32 s4, s1
	s_cselect_b32 s5, s7, s5
	s_cselect_b32 s4, s8, s4
	s_add_i32 s7, s5, 1
	s_cmp_ge_u32 s4, s1
	s_cselect_b32 s1, s7, s5
	s_xor_b32 s1, s1, s0
	s_sub_i32 s4, s1, s0
	s_mov_b32 s0, s4
	v_writelane_b32 v254, s0, 1
	s_nop 1
	v_writelane_b32 v254, s1, 2
	s_abs_i32 s1, s20
	v_cvt_f32_u32_e32 v0, s1
	s_mul_i32 s0, s4, s19
	s_sub_i32 s4, 0, s1
	s_sub_i32 s0, s6, s0
	v_rcp_iflag_f32_e32 v0, v0
	s_add_i32 s0, s14, s0
	v_mul_f32_e32 v0, 0x4f7ffffe, v0
	v_cvt_u32_f32_e32 v0, v0
	s_nop 0
	v_readfirstlane_b32 s5, v0
	s_mul_i32 s4, s4, s5
	s_mul_hi_u32 s4, s5, s4
	s_add_i32 s5, s5, s4
	s_abs_i32 s4, s9
	s_mul_hi_u32 s5, s4, s5
	s_mul_i32 s6, s5, s1
	v_writelane_b32 v254, s0, 3
	s_sub_i32 s4, s4, s6
	s_add_i32 s6, s5, 1
	v_writelane_b32 v254, s1, 4
	s_xor_b32 s0, s9, s20
	s_ashr_i32 s0, s0, 31
	s_sub_i32 s7, s4, s1
	s_cmp_ge_u32 s4, s1
	s_cselect_b32 s5, s6, s5
	s_cselect_b32 s4, s7, s4
	s_add_i32 s6, s5, 1
	s_cmp_ge_u32 s4, s1
	s_cselect_b32 s1, s6, s5
	s_xor_b32 s1, s1, s0
	s_sub_i32 s4, s1, s0
	s_mov_b32 s0, s4
	v_writelane_b32 v254, s0, 5
	s_mul_i32 s5, s24, 0xff0
	s_nop 0
	v_writelane_b32 v254, s1, 6
	s_mul_i32 s0, s4, s20
	s_lshl_b32 s1, s23, 8
	s_mul_i32 s4, s24, 0x7f8
	s_sub_i32 s1, s1, s4
	s_lshl_b32 s4, s23, 9
	s_sub_i32 s4, s4, s5
	v_writelane_b32 v254, s4, 7
	s_lshl_b32 s4, s23, 12
	s_mul_i32 s5, s24, 0x7f80
	s_sub_i32 s0, s9, s0
	v_writelane_b32 v254, s24, 8
	s_sub_i32 s4, s4, s5
	v_writelane_b32 v254, s4, 9
	s_add_i32 s0, s15, s0
	v_writelane_b32 v254, s0, 10
	s_mov_b64 s[8:9], 0x10000
	s_mov_b64 s[14:15], 0x20000
	v_writelane_b32 v254, s1, 11
	s_add_i32 s0, s1, 0xfffff800
	v_writelane_b32 v254, s0, 12
	s_add_u32 s0, s2, 0x800
	v_writelane_b32 v254, s0, 13
	s_addc_u32 s0, s3, 0
	v_writelane_b32 v254, s0, 14
	s_add_i32 s0, 0, 0x20488
	v_writelane_b32 v254, s0, 15
	s_add_i32 s0, 0, 0x2048c
	v_writelane_b32 v254, s0, 16
	s_add_i32 s0, 0, 0x20460
	v_writelane_b32 v254, s0, 17
	s_add_i32 s0, 0, 0x20464
	v_writelane_b32 v254, s0, 18
	s_add_i32 s0, 0, 0x20458
	v_writelane_b32 v254, s0, 19
	s_add_i32 s0, 0, 0x2045c
	v_writelane_b32 v254, s0, 20
	s_add_i32 s0, 0, 0x204b8
	v_writelane_b32 v254, s0, 21
	s_add_i32 s0, 0, 0x204bc
	v_writelane_b32 v254, s0, 22
	s_add_i32 s0, 0, 0x204a0
	v_writelane_b32 v254, s0, 23
	s_add_i32 s0, 0, 0x204a4
	v_writelane_b32 v254, s0, 24
	s_add_i32 s0, 0, 0x204a8
	v_writelane_b32 v254, s0, 25
	s_add_i32 s0, 0, 0x204ac
	v_writelane_b32 v254, s0, 26
	s_add_i32 s0, 0, 0x20420
	v_writelane_b32 v254, s0, 27
	s_add_i32 s0, 0, 0x20424
	v_writelane_b32 v254, s0, 28
	s_add_i32 s0, 0, 0x20410
	v_writelane_b32 v254, s0, 29
	s_add_i32 s0, 0, 0x20414
	v_writelane_b32 v254, s0, 30
	s_add_i32 s0, 0, 0x20400
	v_writelane_b32 v254, s0, 31
	s_add_i32 s0, 0, 0x20404
	v_writelane_b32 v254, s0, 32
	s_add_i32 s0, 0, 0x20408
	v_writelane_b32 v254, s0, 33
	s_add_i32 s0, 0, 0x2040c
	v_writelane_b32 v254, s0, 34
	s_add_i32 s0, 0, 0x20418
	v_writelane_b32 v254, s0, 35
	s_add_i32 s0, 0, 0x2041c
	v_writelane_b32 v254, s0, 36
	s_add_i32 s0, 0, 0x20160
	v_writelane_b32 v254, s0, 37
	s_add_i32 s0, 0, 0x20164
	v_writelane_b32 v254, s0, 38
	s_add_i32 s0, 0, 0x20430
	v_writelane_b32 v254, s0, 39
	s_add_i32 s0, 0, 0x20434
	v_writelane_b32 v254, s0, 40
	s_add_i32 s0, 0, 0x20480
	v_writelane_b32 v254, s0, 41
	s_add_i32 s0, 0, 0x20484
	v_writelane_b32 v254, s0, 42
	s_add_i32 s0, 0, 0x20498
	v_writelane_b32 v254, s0, 43
	s_add_i32 s0, 0, 0x2049c
	v_writelane_b32 v254, s0, 44
	s_add_i32 s0, 0, 0x20448
	v_writelane_b32 v254, s0, 45
	s_add_i32 s0, 0, 0x2044c
	v_writelane_b32 v254, s0, 46
	s_add_i32 s0, 0, 0x20450
	v_writelane_b32 v254, s0, 47
	s_add_i32 s0, 0, 0x20454
	v_writelane_b32 v254, s0, 48
	s_add_i32 s0, 0, 0x20470
	v_writelane_b32 v254, s0, 49
	s_add_i32 s0, 0, 0x20474
	v_writelane_b32 v254, s0, 50
	s_add_i32 s0, 0, 0x20428
	v_writelane_b32 v254, s0, 51
	s_add_i32 s0, 0, 0x2042c
	v_writelane_b32 v254, s0, 52
	s_add_i32 s0, 0, 0x20468
	v_writelane_b32 v254, s0, 53
	s_add_i32 s0, 0, 0x2046c
	v_writelane_b32 v254, s0, 54
	s_add_i32 s0, 0, 0x20478
	v_writelane_b32 v254, s0, 55
	s_add_i32 s0, 0, 0x2047c
	v_writelane_b32 v254, s0, 56
	s_add_i32 s0, 0, 0x20490
	v_writelane_b32 v254, s0, 57
	s_add_i32 s0, 0, 0x20494
	v_writelane_b32 v254, s0, 58
	s_add_i32 s0, 0, 0x20438
	v_writelane_b32 v254, s0, 59
	s_add_i32 s0, 0, 0x2043c
	v_writelane_b32 v254, s0, 60
	s_add_i32 s0, 0, 0x20440
	v_writelane_b32 v254, s0, 61
	s_add_i32 s0, 0, 0x20444
	v_writelane_b32 v254, s0, 62
	s_add_i32 s0, 0, 0x204b0
	v_writelane_b32 v254, s0, 63
	s_add_i32 s0, 0, 0x204b4
	v_writelane_b32 v255, s0, 0
	s_add_i32 s0, 0, 0x204c8
	v_writelane_b32 v255, s0, 1
	s_add_i32 s0, 0, 0x204cc
	v_writelane_b32 v255, s0, 2
	s_add_i32 s0, 0, 0x204d0
	v_writelane_b32 v255, s0, 3
	s_add_i32 s0, 0, 0x204d4
	v_writelane_b32 v255, s0, 4
	s_add_i32 s0, 0, 0x204d8
	v_writelane_b32 v255, s0, 5
	s_add_i32 s0, 0, 0x204dc
	v_writelane_b32 v255, s0, 6
	s_add_i32 s0, 0, 0x204c0
	v_writelane_b32 v255, s0, 7
	s_add_i32 s0, 0, 0x204c4
	v_writelane_b32 v255, s0, 8
	s_add_i32 s0, 0, 0x204e8
	v_writelane_b32 v255, s0, 9
	s_add_i32 s0, 0, 0x204ec
	v_writelane_b32 v255, s0, 10
	s_add_i32 s0, 0, 0x204f0
	v_writelane_b32 v255, s0, 11
	s_add_i32 s0, 0, 0x204f4
	v_writelane_b32 v255, s0, 12
	s_add_i32 s0, 0, 0x204f8
	v_writelane_b32 v255, s0, 13
	s_add_i32 s0, 0, 0x204fc
	v_writelane_b32 v255, s0, 14
	s_add_i32 s0, 0, 0x204e0
	v_writelane_b32 v255, s0, 15
	s_add_i32 s0, 0, 0x204e4
	v_writelane_b32 v255, s0, 16
	s_add_i32 s0, 0, 0x21060
	v_writelane_b32 v255, s0, 17
	s_add_i32 s0, 0, 0x21020
	v_writelane_b32 v255, s0, 18
	s_add_i32 s0, 0, 0x21064
	v_writelane_b32 v255, s0, 19
	s_add_i32 s0, 0, 0x21024
	v_writelane_b32 v255, s0, 20
	s_add_i32 s0, 0, 0x21068
	v_writelane_b32 v255, s0, 21
	s_add_i32 s0, 0, 0x21028
	v_writelane_b32 v255, s0, 22
	s_add_i32 s0, 0, 0x2106c
	v_writelane_b32 v255, s0, 23
	s_add_i32 s0, 0, 0x2102c
	v_writelane_b32 v255, s0, 24
	s_add_i32 s0, 0, 0x21070
	v_writelane_b32 v255, s0, 25
	s_add_i32 s0, 0, 0x21030
	v_writelane_b32 v255, s0, 26
	s_add_i32 s0, 0, 0x21074
	v_writelane_b32 v255, s0, 27
	s_add_i32 s0, 0, 0x21034
	v_writelane_b32 v255, s0, 28
	s_add_i32 s0, 0, 0x21078
	v_writelane_b32 v255, s0, 29
	s_add_i32 s0, 0, 0x21038
	v_writelane_b32 v255, s0, 30
	s_add_i32 s0, 0, 0x2107c
	v_writelane_b32 v255, s0, 31
	s_add_i32 s0, 0, 0x2103c
	v_writelane_b32 v255, s0, 32
	s_add_i32 s0, 0, 0x21080
	v_writelane_b32 v255, s0, 33
	s_mov_b64 s[0:1], 0
	v_writelane_b32 v255, s0, 34
	s_mov_b64 s[20:21], 0x38000
	s_mov_b64 s[24:25], 0x40080
	v_writelane_b32 v255, s1, 35
	s_mov_b64 s[0:1], 0x20080
	s_branch .LBB0_17

.LBB0_189:
	s_add_i32 s38, s2, 2
	s_add_u32 s39, s74, 0xfffc0080
	s_addc_u32 s3, s75, -1
	s_cmp_eq_u32 s80, s2
	s_cselect_b32 s3, s47, s3
	s_cselect_b32 s2, s49, s39
	s_cselect_b32 s91, s86, s23
	s_cselect_b32 s90, s87, s22
	s_add_i32 s39, 0, 0x10000
	s_add_i32 s92, 0, 0x14000
	v_add_u32_e32 v148, s39, v133
	v_add_u32_e32 v166, s92, v133
	ds_read_b128 v[136:139], v148
	ds_read_b128 v[140:143], v148 offset:1024
	ds_read_b128 v[144:147], v148 offset:2048
	ds_read_b128 v[148:151], v148 offset:3072
	ds_read_b128 v[152:155], v166
	ds_read_b128 v[156:159], v166 offset:1024
	ds_read_b128 v[162:165], v166 offset:2048
	ds_read_b128 v[166:169], v166 offset:3072
	v_lshl_add_u64 v[202:203], s[74:75], 0, v[130:131]
	s_add_i32 m0, s33, 0xc000
	ds_read_b128 v[170:173], v135
	ds_read_b128 v[174:177], v135 offset:1024
	ds_read_b128 v[178:181], v135 offset:2048
	ds_read_b128 v[182:185], v135 offset:3072
	ds_read_b128 v[186:189], v135 offset:4096
	ds_read_b128 v[190:193], v135 offset:5120
	ds_read_b128 v[194:197], v135 offset:6144
	ds_read_b128 v[198:201], v135 offset:7168
	global_load_lds_dwordx4 v[202:203], off
	v_lshl_add_u64 v[202:203], v[202:203], 0, s[14:15]
	s_add_i32 m0, s33, 0xe000
	s_nop 0
	global_load_lds_dwordx4 v[202:203], off
	s_waitcnt vmcnt(8)
	s_waitcnt lgkmcnt(0)
	s_barrier
	s_waitcnt lgkmcnt(0)
	v_mfma_f32_16x16x32_bf16 v[124:127], v[136:139], v[170:173], v[124:127]
	v_mfma_f32_16x16x32_bf16 v[120:123], v[144:147], v[170:173], v[120:123]
	v_mfma_f32_16x16x32_bf16 v[108:111], v[136:139], v[178:181], v[108:111]
	v_mfma_f32_16x16x32_bf16 v[104:107], v[144:147], v[178:181], v[104:107]
	v_mfma_f32_16x16x32_bf16 v[92:95], v[136:139], v[186:189], v[92:95]
	v_mfma_f32_16x16x32_bf16 v[88:91], v[144:147], v[186:189], v[88:91]
	v_mfma_f32_16x16x32_bf16 v[76:79], v[136:139], v[194:197], v[76:79]
	v_mfma_f32_16x16x32_bf16 v[72:75], v[144:147], v[194:197], v[72:75]
	v_mfma_f32_16x16x32_bf16 v[124:127], v[140:143], v[174:177], v[124:127]
	v_mfma_f32_16x16x32_bf16 v[120:123], v[148:151], v[174:177], v[120:123]
	v_mfma_f32_16x16x32_bf16 v[108:111], v[140:143], v[182:185], v[108:111]
	v_mfma_f32_16x16x32_bf16 v[104:107], v[148:151], v[182:185], v[104:107]
	v_mfma_f32_16x16x32_bf16 v[92:95], v[140:143], v[190:193], v[92:95]
	v_mfma_f32_16x16x32_bf16 v[88:91], v[148:151], v[190:193], v[88:91]
	v_mfma_f32_16x16x32_bf16 v[76:79], v[140:143], v[198:201], v[76:79]
	v_mfma_f32_16x16x32_bf16 v[72:75], v[148:151], v[198:201], v[72:75]
	v_mfma_f32_16x16x32_bf16 v[116:119], v[152:155], v[170:173], v[116:119]
	v_mfma_f32_16x16x32_bf16 v[112:115], v[162:165], v[170:173], v[112:115]
	v_mfma_f32_16x16x32_bf16 v[100:103], v[152:155], v[178:181], v[100:103]
	v_mfma_f32_16x16x32_bf16 v[96:99], v[162:165], v[178:181], v[96:99]
	v_mfma_f32_16x16x32_bf16 v[84:87], v[152:155], v[186:189], v[84:87]
	v_mfma_f32_16x16x32_bf16 v[80:83], v[162:165], v[186:189], v[80:83]
	v_mfma_f32_16x16x32_bf16 v[68:71], v[152:155], v[194:197], v[68:71]
	v_mfma_f32_16x16x32_bf16 v[64:67], v[162:165], v[194:197], v[64:67]
	v_mfma_f32_16x16x32_bf16 v[116:119], v[156:159], v[174:177], v[116:119]
	v_mfma_f32_16x16x32_bf16 v[112:115], v[166:169], v[174:177], v[112:115]
	v_mfma_f32_16x16x32_bf16 v[100:103], v[156:159], v[182:185], v[100:103]
	v_mfma_f32_16x16x32_bf16 v[96:99], v[166:169], v[182:185], v[96:99]
	v_mfma_f32_16x16x32_bf16 v[84:87], v[156:159], v[190:193], v[84:87]
	v_mfma_f32_16x16x32_bf16 v[80:83], v[166:169], v[190:193], v[80:83]
	v_mfma_f32_16x16x32_bf16 v[68:71], v[156:159], v[198:201], v[68:71]
	v_mfma_f32_16x16x32_bf16 v[64:67], v[166:169], v[198:201], v[64:67]
	s_barrier
	s_add_i32 s39, s39, s31
	v_lshl_add_u64 v[202:203], s[90:91], 0, v[160:161]
	s_mov_b32 m0, s39
	ds_read_b128 v[170:173], v135 offset:16384
	ds_read_b128 v[174:177], v135 offset:17408
	ds_read_b128 v[178:181], v135 offset:18432
	ds_read_b128 v[182:185], v135 offset:19456
	ds_read_b128 v[186:189], v135 offset:20480
	ds_read_b128 v[190:193], v135 offset:21504
	ds_read_b128 v[194:197], v135 offset:22528
	ds_read_b128 v[198:201], v135 offset:23552
	global_load_lds_dwordx4 v[202:203], off
	v_lshl_add_u64 v[204:205], v[202:203], 0, s[14:15]
	s_add_i32 m0, s39, 0x2000
	s_add_i32 s39, s92, s31
	global_load_lds_dwordx4 v[204:205], off
	v_lshl_add_u64 v[204:205], v[202:203], 0, s[60:61]
	s_mov_b32 m0, s39
	s_nop 0
	global_load_lds_dwordx4 v[204:205], off
	v_lshl_add_u64 v[204:205], v[202:203], 0, s[52:53]
	s_add_i32 m0, s39, 0x2000
	s_nop 0
	global_load_lds_dwordx4 v[204:205], off
	v_lshl_add_u64 v[204:205], s[2:3], 0, v[128:129]
	s_mov_b32 m0, s33
	v_lshl_add_u64 v[206:207], v[204:205], 0, s[14:15]
	global_load_lds_dwordx4 v[204:205], off
	s_mov_b32 m0, s58
	s_nop 0
	global_load_lds_dwordx4 v[206:207], off
	s_waitcnt vmcnt(8)
	s_waitcnt lgkmcnt(0)
	s_barrier
	s_waitcnt lgkmcnt(0)
	v_mfma_f32_16x16x32_bf16 v[60:63], v[136:139], v[170:173], v[60:63]
	v_mfma_f32_16x16x32_bf16 v[56:59], v[144:147], v[170:173], v[56:59]
	v_mfma_f32_16x16x32_bf16 v[44:47], v[136:139], v[178:181], v[44:47]
	v_mfma_f32_16x16x32_bf16 v[40:43], v[144:147], v[178:181], v[40:43]
	v_mfma_f32_16x16x32_bf16 v[28:31], v[136:139], v[186:189], v[28:31]
	v_mfma_f32_16x16x32_bf16 v[24:27], v[144:147], v[186:189], v[24:27]
	v_mfma_f32_16x16x32_bf16 v[12:15], v[136:139], v[194:197], v[12:15]
	v_mfma_f32_16x16x32_bf16 v[8:11], v[144:147], v[194:197], v[8:11]
	v_mfma_f32_16x16x32_bf16 v[60:63], v[140:143], v[174:177], v[60:63]
	v_mfma_f32_16x16x32_bf16 v[56:59], v[148:151], v[174:177], v[56:59]
	v_mfma_f32_16x16x32_bf16 v[44:47], v[140:143], v[182:185], v[44:47]
	v_mfma_f32_16x16x32_bf16 v[40:43], v[148:151], v[182:185], v[40:43]
	v_mfma_f32_16x16x32_bf16 v[28:31], v[140:143], v[190:193], v[28:31]
	v_mfma_f32_16x16x32_bf16 v[24:27], v[148:151], v[190:193], v[24:27]
	v_mfma_f32_16x16x32_bf16 v[12:15], v[140:143], v[198:201], v[12:15]
	v_mfma_f32_16x16x32_bf16 v[8:11], v[148:151], v[198:201], v[8:11]
	v_mfma_f32_16x16x32_bf16 v[52:55], v[152:155], v[170:173], v[52:55]
	v_mfma_f32_16x16x32_bf16 v[48:51], v[162:165], v[170:173], v[48:51]
	v_mfma_f32_16x16x32_bf16 v[36:39], v[152:155], v[178:181], v[36:39]
	v_mfma_f32_16x16x32_bf16 v[32:35], v[162:165], v[178:181], v[32:35]
	v_mfma_f32_16x16x32_bf16 v[20:23], v[152:155], v[186:189], v[20:23]
	v_mfma_f32_16x16x32_bf16 v[16:19], v[162:165], v[186:189], v[16:19]
	v_mfma_f32_16x16x32_bf16 v[4:7], v[152:155], v[194:197], v[4:7]
	v_mfma_f32_16x16x32_bf16 v[0:3], v[162:165], v[194:197], v[0:3]
	v_mfma_f32_16x16x32_bf16 v[52:55], v[156:159], v[174:177], v[52:55]
	v_mfma_f32_16x16x32_bf16 v[48:51], v[166:169], v[174:177], v[48:51]
	v_mfma_f32_16x16x32_bf16 v[36:39], v[156:159], v[182:185], v[36:39]
	v_mfma_f32_16x16x32_bf16 v[32:35], v[166:169], v[182:185], v[32:35]
	v_mfma_f32_16x16x32_bf16 v[20:23], v[156:159], v[190:193], v[20:23]
	v_mfma_f32_16x16x32_bf16 v[16:19], v[166:169], v[190:193], v[16:19]
	v_mfma_f32_16x16x32_bf16 v[4:7], v[156:159], v[198:201], v[4:7]
	v_mfma_f32_16x16x32_bf16 v[0:3], v[166:169], v[198:201], v[0:3]
	s_barrier
	s_add_i32 s2, 0, 0x18000
	s_add_i32 s3, 0, 0x1c000
	v_add_u32_e32 v148, s2, v133
	v_add_u32_e32 v166, s3, v133
	ds_read_b128 v[136:139], v148
	ds_read_b128 v[140:143], v148 offset:1024
	ds_read_b128 v[144:147], v148 offset:2048
	ds_read_b128 v[148:151], v148 offset:3072
	ds_read_b128 v[152:155], v166
	ds_read_b128 v[156:159], v166 offset:1024
	ds_read_b128 v[162:165], v166 offset:2048
	ds_read_b128 v[166:169], v166 offset:3072
	s_mov_b32 m0, s59
	v_lshl_add_u64 v[206:207], v[204:205], 0, s[60:61]
	ds_read_b128 v[170:173], v135 offset:32768
	ds_read_b128 v[174:177], v135 offset:33792
	ds_read_b128 v[178:181], v135 offset:34816
	ds_read_b128 v[182:185], v135 offset:35840
	ds_read_b128 v[186:189], v135 offset:36864
	ds_read_b128 v[190:193], v135 offset:37888
	ds_read_b128 v[194:197], v135 offset:38912
	ds_read_b128 v[198:201], v135 offset:39936
	global_load_lds_dwordx4 v[206:207], off
	v_lshl_add_u64 v[206:207], v[204:205], 0, s[52:53]
	s_mov_b32 m0, s63
	s_nop 0
	global_load_lds_dwordx4 v[206:207], off
	s_waitcnt vmcnt(8)
	s_waitcnt lgkmcnt(0)
	s_barrier
	s_waitcnt lgkmcnt(0)
	v_mfma_f32_16x16x32_bf16 v[124:127], v[136:139], v[170:173], v[124:127]
	v_mfma_f32_16x16x32_bf16 v[120:123], v[144:147], v[170:173], v[120:123]
	v_mfma_f32_16x16x32_bf16 v[108:111], v[136:139], v[178:181], v[108:111]
	v_mfma_f32_16x16x32_bf16 v[104:107], v[144:147], v[178:181], v[104:107]
	v_mfma_f32_16x16x32_bf16 v[92:95], v[136:139], v[186:189], v[92:95]
	v_mfma_f32_16x16x32_bf16 v[88:91], v[144:147], v[186:189], v[88:91]
	v_mfma_f32_16x16x32_bf16 v[76:79], v[136:139], v[194:197], v[76:79]
	v_mfma_f32_16x16x32_bf16 v[72:75], v[144:147], v[194:197], v[72:75]
	v_mfma_f32_16x16x32_bf16 v[124:127], v[140:143], v[174:177], v[124:127]
	v_mfma_f32_16x16x32_bf16 v[120:123], v[148:151], v[174:177], v[120:123]
	v_mfma_f32_16x16x32_bf16 v[108:111], v[140:143], v[182:185], v[108:111]
	v_mfma_f32_16x16x32_bf16 v[104:107], v[148:151], v[182:185], v[104:107]
	v_mfma_f32_16x16x32_bf16 v[92:95], v[140:143], v[190:193], v[92:95]
	v_mfma_f32_16x16x32_bf16 v[88:91], v[148:151], v[190:193], v[88:91]
	v_mfma_f32_16x16x32_bf16 v[76:79], v[140:143], v[198:201], v[76:79]
	v_mfma_f32_16x16x32_bf16 v[72:75], v[148:151], v[198:201], v[72:75]
	v_mfma_f32_16x16x32_bf16 v[116:119], v[152:155], v[170:173], v[116:119]
	v_mfma_f32_16x16x32_bf16 v[112:115], v[162:165], v[170:173], v[112:115]
	v_mfma_f32_16x16x32_bf16 v[100:103], v[152:155], v[178:181], v[100:103]
	v_mfma_f32_16x16x32_bf16 v[96:99], v[162:165], v[178:181], v[96:99]
	v_mfma_f32_16x16x32_bf16 v[84:87], v[152:155], v[186:189], v[84:87]
	v_mfma_f32_16x16x32_bf16 v[80:83], v[162:165], v[186:189], v[80:83]
	v_mfma_f32_16x16x32_bf16 v[68:71], v[152:155], v[194:197], v[68:71]
	v_mfma_f32_16x16x32_bf16 v[64:67], v[162:165], v[194:197], v[64:67]
	v_mfma_f32_16x16x32_bf16 v[116:119], v[156:159], v[174:177], v[116:119]
	v_mfma_f32_16x16x32_bf16 v[112:115], v[166:169], v[174:177], v[112:115]
	v_mfma_f32_16x16x32_bf16 v[100:103], v[156:159], v[182:185], v[100:103]
	v_mfma_f32_16x16x32_bf16 v[96:99], v[166:169], v[182:185], v[96:99]
	v_mfma_f32_16x16x32_bf16 v[84:87], v[156:159], v[190:193], v[84:87]
	v_mfma_f32_16x16x32_bf16 v[80:83], v[166:169], v[190:193], v[80:83]
	v_mfma_f32_16x16x32_bf16 v[68:71], v[156:159], v[198:201], v[68:71]
	v_mfma_f32_16x16x32_bf16 v[64:67], v[166:169], v[198:201], v[64:67]
	s_barrier
	s_add_i32 s2, s2, s31
	v_lshl_add_u64 v[206:207], v[202:203], 0, s[56:57]
	s_mov_b32 m0, s2
	ds_read_b128 v[170:173], v135 offset:49152
	ds_read_b128 v[174:177], v135 offset:50176
	ds_read_b128 v[178:181], v135 offset:51200
	ds_read_b128 v[182:185], v135 offset:52224
	ds_read_b128 v[186:189], v135 offset:53248
	ds_read_b128 v[190:193], v135 offset:54272
	ds_read_b128 v[194:197], v135 offset:55296
	ds_read_b128 v[198:201], v135 offset:56320
	global_load_lds_dwordx4 v[206:207], off
	v_lshl_add_u64 v[206:207], v[202:203], 0, s[0:1]
	s_add_i32 m0, s2, 0x2000
	s_add_i32 s2, s3, s31
	global_load_lds_dwordx4 v[206:207], off
	v_lshl_add_u64 v[206:207], v[202:203], 0, s[24:25]
	s_mov_b32 m0, s2
	v_lshl_add_u64 v[202:203], v[202:203], 0, s[26:27]
	global_load_lds_dwordx4 v[206:207], off
	s_add_i32 m0, s2, 0x2000
	s_nop 0
	global_load_lds_dwordx4 v[202:203], off
	v_lshl_add_u64 v[202:203], v[204:205], 0, s[56:57]
	s_mov_b32 m0, s77
	s_nop 0
	global_load_lds_dwordx4 v[202:203], off
	v_lshl_add_u64 v[202:203], v[204:205], 0, s[0:1]
	s_mov_b32 m0, s78
	s_nop 0
	global_load_lds_dwordx4 v[202:203], off
	s_waitcnt vmcnt(8)
	s_waitcnt lgkmcnt(0)
	s_barrier
	s_waitcnt lgkmcnt(0)
	v_mfma_f32_16x16x32_bf16 v[60:63], v[136:139], v[170:173], v[60:63]
	v_mfma_f32_16x16x32_bf16 v[56:59], v[144:147], v[170:173], v[56:59]
	v_mfma_f32_16x16x32_bf16 v[44:47], v[136:139], v[178:181], v[44:47]
	v_mfma_f32_16x16x32_bf16 v[40:43], v[144:147], v[178:181], v[40:43]
	v_mfma_f32_16x16x32_bf16 v[28:31], v[136:139], v[186:189], v[28:31]
	v_mfma_f32_16x16x32_bf16 v[24:27], v[144:147], v[186:189], v[24:27]
	v_mfma_f32_16x16x32_bf16 v[12:15], v[136:139], v[194:197], v[12:15]
	v_mfma_f32_16x16x32_bf16 v[8:11], v[144:147], v[194:197], v[8:11]
	v_mfma_f32_16x16x32_bf16 v[60:63], v[140:143], v[174:177], v[60:63]
	v_mfma_f32_16x16x32_bf16 v[56:59], v[148:151], v[174:177], v[56:59]
	v_mfma_f32_16x16x32_bf16 v[44:47], v[140:143], v[182:185], v[44:47]
	v_mfma_f32_16x16x32_bf16 v[40:43], v[148:151], v[182:185], v[40:43]
	v_mfma_f32_16x16x32_bf16 v[28:31], v[140:143], v[190:193], v[28:31]
	v_mfma_f32_16x16x32_bf16 v[24:27], v[148:151], v[190:193], v[24:27]
	v_mfma_f32_16x16x32_bf16 v[12:15], v[140:143], v[198:201], v[12:15]
	v_mfma_f32_16x16x32_bf16 v[8:11], v[148:151], v[198:201], v[8:11]
	v_mfma_f32_16x16x32_bf16 v[52:55], v[152:155], v[170:173], v[52:55]
	v_mfma_f32_16x16x32_bf16 v[48:51], v[162:165], v[170:173], v[48:51]
	v_mfma_f32_16x16x32_bf16 v[36:39], v[152:155], v[178:181], v[36:39]
	v_mfma_f32_16x16x32_bf16 v[32:35], v[162:165], v[178:181], v[32:35]
	v_mfma_f32_16x16x32_bf16 v[20:23], v[152:155], v[186:189], v[20:23]
	v_mfma_f32_16x16x32_bf16 v[16:19], v[162:165], v[186:189], v[16:19]
	v_mfma_f32_16x16x32_bf16 v[4:7], v[152:155], v[194:197], v[4:7]
	v_mfma_f32_16x16x32_bf16 v[0:3], v[162:165], v[194:197], v[0:3]
	v_mfma_f32_16x16x32_bf16 v[52:55], v[156:159], v[174:177], v[52:55]
	v_mfma_f32_16x16x32_bf16 v[48:51], v[166:169], v[174:177], v[48:51]
	v_mfma_f32_16x16x32_bf16 v[36:39], v[156:159], v[182:185], v[36:39]
	v_mfma_f32_16x16x32_bf16 v[32:35], v[166:169], v[182:185], v[32:35]
	v_mfma_f32_16x16x32_bf16 v[20:23], v[156:159], v[190:193], v[20:23]
	v_mfma_f32_16x16x32_bf16 v[16:19], v[166:169], v[190:193], v[16:19]
	v_mfma_f32_16x16x32_bf16 v[4:7], v[156:159], v[198:201], v[4:7]
	v_mfma_f32_16x16x32_bf16 v[0:3], v[166:169], v[198:201], v[0:3]
	s_barrier
	s_add_u32 s74, s74, 0x100
	s_addc_u32 s75, s75, 0
	s_add_u32 s22, s22, 0x100
	s_addc_u32 s23, s23, 0
	s_cmp_ge_i32 s38, s79
	s_mov_b32 s2, s38
	s_cbranch_scc0 .LBB0_189

.LBB0_206:
	s_add_i32 s38, s2, 2
	s_add_u32 s39, s54, 0xfffc0080
	s_addc_u32 s3, s55, -1
	s_cmp_eq_u32 s78, s2
	s_cselect_b32 s3, s43, s3
	s_cselect_b32 s2, s45, s39
	s_cselect_b32 s87, s81, s23
	s_cselect_b32 s86, s83, s22
	s_add_i32 s39, 0, 0x10000
	s_add_i32 s90, 0, 0x14000
	v_add_u32_e32 v148, s39, v133
	v_add_u32_e32 v166, s90, v133
	ds_read_b128 v[136:139], v148
	ds_read_b128 v[140:143], v148 offset:1024
	ds_read_b128 v[144:147], v148 offset:2048
	ds_read_b128 v[148:151], v148 offset:3072
	ds_read_b128 v[152:155], v166
	ds_read_b128 v[156:159], v166 offset:1024
	ds_read_b128 v[162:165], v166 offset:2048
	ds_read_b128 v[166:169], v166 offset:3072
	v_lshl_add_u64 v[202:203], s[54:55], 0, v[130:131]
	s_add_i32 m0, s33, 0xc000
	ds_read_b128 v[170:173], v135
	ds_read_b128 v[174:177], v135 offset:1024
	ds_read_b128 v[178:181], v135 offset:2048
	ds_read_b128 v[182:185], v135 offset:3072
	ds_read_b128 v[186:189], v135 offset:4096
	ds_read_b128 v[190:193], v135 offset:5120
	ds_read_b128 v[194:197], v135 offset:6144
	ds_read_b128 v[198:201], v135 offset:7168
	global_load_lds_dwordx4 v[202:203], off
	v_lshl_add_u64 v[202:203], v[202:203], 0, s[14:15]
	s_add_i32 m0, s33, 0xe000
	s_nop 0
	global_load_lds_dwordx4 v[202:203], off
	s_waitcnt vmcnt(8)
	s_waitcnt lgkmcnt(0)
	s_barrier
	s_waitcnt lgkmcnt(0)
	v_mfma_f32_16x16x32_bf16 v[124:127], v[136:139], v[170:173], v[124:127]
	v_mfma_f32_16x16x32_bf16 v[120:123], v[144:147], v[170:173], v[120:123]
	v_mfma_f32_16x16x32_bf16 v[108:111], v[136:139], v[178:181], v[108:111]
	v_mfma_f32_16x16x32_bf16 v[104:107], v[144:147], v[178:181], v[104:107]
	v_mfma_f32_16x16x32_bf16 v[92:95], v[136:139], v[186:189], v[92:95]
	v_mfma_f32_16x16x32_bf16 v[88:91], v[144:147], v[186:189], v[88:91]
	v_mfma_f32_16x16x32_bf16 v[76:79], v[136:139], v[194:197], v[76:79]
	v_mfma_f32_16x16x32_bf16 v[72:75], v[144:147], v[194:197], v[72:75]
	v_mfma_f32_16x16x32_bf16 v[124:127], v[140:143], v[174:177], v[124:127]
	v_mfma_f32_16x16x32_bf16 v[120:123], v[148:151], v[174:177], v[120:123]
	v_mfma_f32_16x16x32_bf16 v[108:111], v[140:143], v[182:185], v[108:111]
	v_mfma_f32_16x16x32_bf16 v[104:107], v[148:151], v[182:185], v[104:107]
	v_mfma_f32_16x16x32_bf16 v[92:95], v[140:143], v[190:193], v[92:95]
	v_mfma_f32_16x16x32_bf16 v[88:91], v[148:151], v[190:193], v[88:91]
	v_mfma_f32_16x16x32_bf16 v[76:79], v[140:143], v[198:201], v[76:79]
	v_mfma_f32_16x16x32_bf16 v[72:75], v[148:151], v[198:201], v[72:75]
	v_mfma_f32_16x16x32_bf16 v[116:119], v[152:155], v[170:173], v[116:119]
	v_mfma_f32_16x16x32_bf16 v[112:115], v[162:165], v[170:173], v[112:115]
	v_mfma_f32_16x16x32_bf16 v[100:103], v[152:155], v[178:181], v[100:103]
	v_mfma_f32_16x16x32_bf16 v[96:99], v[162:165], v[178:181], v[96:99]
	v_mfma_f32_16x16x32_bf16 v[84:87], v[152:155], v[186:189], v[84:87]
	v_mfma_f32_16x16x32_bf16 v[80:83], v[162:165], v[186:189], v[80:83]
	v_mfma_f32_16x16x32_bf16 v[68:71], v[152:155], v[194:197], v[68:71]
	v_mfma_f32_16x16x32_bf16 v[64:67], v[162:165], v[194:197], v[64:67]
	v_mfma_f32_16x16x32_bf16 v[116:119], v[156:159], v[174:177], v[116:119]
	v_mfma_f32_16x16x32_bf16 v[112:115], v[166:169], v[174:177], v[112:115]
	v_mfma_f32_16x16x32_bf16 v[100:103], v[156:159], v[182:185], v[100:103]
	v_mfma_f32_16x16x32_bf16 v[96:99], v[166:169], v[182:185], v[96:99]
	v_mfma_f32_16x16x32_bf16 v[84:87], v[156:159], v[190:193], v[84:87]
	v_mfma_f32_16x16x32_bf16 v[80:83], v[166:169], v[190:193], v[80:83]
	v_mfma_f32_16x16x32_bf16 v[68:71], v[156:159], v[198:201], v[68:71]
	v_mfma_f32_16x16x32_bf16 v[64:67], v[166:169], v[198:201], v[64:67]
	s_barrier
	s_add_i32 s39, s39, s10
	v_lshl_add_u64 v[202:203], s[86:87], 0, v[160:161]
	s_mov_b32 m0, s39
	ds_read_b128 v[170:173], v135 offset:16384
	ds_read_b128 v[174:177], v135 offset:17408
	ds_read_b128 v[178:181], v135 offset:18432
	ds_read_b128 v[182:185], v135 offset:19456
	ds_read_b128 v[186:189], v135 offset:20480
	ds_read_b128 v[190:193], v135 offset:21504
	ds_read_b128 v[194:197], v135 offset:22528
	ds_read_b128 v[198:201], v135 offset:23552
	global_load_lds_dwordx4 v[202:203], off
	v_lshl_add_u64 v[204:205], v[202:203], 0, s[14:15]
	s_add_i32 m0, s39, 0x2000
	s_add_i32 s39, s90, s10
	global_load_lds_dwordx4 v[204:205], off
	v_lshl_add_u64 v[204:205], v[202:203], 0, s[60:61]
	s_mov_b32 m0, s39
	s_nop 0
	global_load_lds_dwordx4 v[204:205], off
	v_lshl_add_u64 v[204:205], v[202:203], 0, s[52:53]
	s_add_i32 m0, s39, 0x2000
	s_nop 0
	global_load_lds_dwordx4 v[204:205], off
	v_lshl_add_u64 v[204:205], s[2:3], 0, v[128:129]
	s_mov_b32 m0, s33
	v_lshl_add_u64 v[206:207], v[204:205], 0, s[14:15]
	global_load_lds_dwordx4 v[204:205], off
	s_mov_b32 m0, s58
	s_nop 0
	global_load_lds_dwordx4 v[206:207], off
	s_waitcnt vmcnt(8)
	s_waitcnt lgkmcnt(0)
	s_barrier
	s_waitcnt lgkmcnt(0)
	v_mfma_f32_16x16x32_bf16 v[60:63], v[136:139], v[170:173], v[60:63]
	v_mfma_f32_16x16x32_bf16 v[56:59], v[144:147], v[170:173], v[56:59]
	v_mfma_f32_16x16x32_bf16 v[44:47], v[136:139], v[178:181], v[44:47]
	v_mfma_f32_16x16x32_bf16 v[40:43], v[144:147], v[178:181], v[40:43]
	v_mfma_f32_16x16x32_bf16 v[28:31], v[136:139], v[186:189], v[28:31]
	v_mfma_f32_16x16x32_bf16 v[24:27], v[144:147], v[186:189], v[24:27]
	v_mfma_f32_16x16x32_bf16 v[12:15], v[136:139], v[194:197], v[12:15]
	v_mfma_f32_16x16x32_bf16 v[8:11], v[144:147], v[194:197], v[8:11]
	v_mfma_f32_16x16x32_bf16 v[60:63], v[140:143], v[174:177], v[60:63]
	v_mfma_f32_16x16x32_bf16 v[56:59], v[148:151], v[174:177], v[56:59]
	v_mfma_f32_16x16x32_bf16 v[44:47], v[140:143], v[182:185], v[44:47]
	v_mfma_f32_16x16x32_bf16 v[40:43], v[148:151], v[182:185], v[40:43]
	v_mfma_f32_16x16x32_bf16 v[28:31], v[140:143], v[190:193], v[28:31]
	v_mfma_f32_16x16x32_bf16 v[24:27], v[148:151], v[190:193], v[24:27]
	v_mfma_f32_16x16x32_bf16 v[12:15], v[140:143], v[198:201], v[12:15]
	v_mfma_f32_16x16x32_bf16 v[8:11], v[148:151], v[198:201], v[8:11]
	v_mfma_f32_16x16x32_bf16 v[52:55], v[152:155], v[170:173], v[52:55]
	v_mfma_f32_16x16x32_bf16 v[48:51], v[162:165], v[170:173], v[48:51]
	v_mfma_f32_16x16x32_bf16 v[36:39], v[152:155], v[178:181], v[36:39]
	v_mfma_f32_16x16x32_bf16 v[32:35], v[162:165], v[178:181], v[32:35]
	v_mfma_f32_16x16x32_bf16 v[20:23], v[152:155], v[186:189], v[20:23]
	v_mfma_f32_16x16x32_bf16 v[16:19], v[162:165], v[186:189], v[16:19]
	v_mfma_f32_16x16x32_bf16 v[4:7], v[152:155], v[194:197], v[4:7]
	v_mfma_f32_16x16x32_bf16 v[0:3], v[162:165], v[194:197], v[0:3]
	v_mfma_f32_16x16x32_bf16 v[52:55], v[156:159], v[174:177], v[52:55]
	v_mfma_f32_16x16x32_bf16 v[48:51], v[166:169], v[174:177], v[48:51]
	v_mfma_f32_16x16x32_bf16 v[36:39], v[156:159], v[182:185], v[36:39]
	v_mfma_f32_16x16x32_bf16 v[32:35], v[166:169], v[182:185], v[32:35]
	v_mfma_f32_16x16x32_bf16 v[20:23], v[156:159], v[190:193], v[20:23]
	v_mfma_f32_16x16x32_bf16 v[16:19], v[166:169], v[190:193], v[16:19]
	v_mfma_f32_16x16x32_bf16 v[4:7], v[156:159], v[198:201], v[4:7]
	v_mfma_f32_16x16x32_bf16 v[0:3], v[166:169], v[198:201], v[0:3]
	s_barrier
	s_add_i32 s2, 0, 0x18000
	s_add_i32 s3, 0, 0x1c000
	v_add_u32_e32 v148, s2, v133
	v_add_u32_e32 v166, s3, v133
	ds_read_b128 v[136:139], v148
	ds_read_b128 v[140:143], v148 offset:1024
	ds_read_b128 v[144:147], v148 offset:2048
	ds_read_b128 v[148:151], v148 offset:3072
	ds_read_b128 v[152:155], v166
	ds_read_b128 v[156:159], v166 offset:1024
	ds_read_b128 v[162:165], v166 offset:2048
	ds_read_b128 v[166:169], v166 offset:3072
	s_mov_b32 m0, s59
	v_lshl_add_u64 v[206:207], v[204:205], 0, s[60:61]
	ds_read_b128 v[170:173], v135 offset:32768
	ds_read_b128 v[174:177], v135 offset:33792
	ds_read_b128 v[178:181], v135 offset:34816
	ds_read_b128 v[182:185], v135 offset:35840
	ds_read_b128 v[186:189], v135 offset:36864
	ds_read_b128 v[190:193], v135 offset:37888
	ds_read_b128 v[194:197], v135 offset:38912
	ds_read_b128 v[198:201], v135 offset:39936
	global_load_lds_dwordx4 v[206:207], off
	v_lshl_add_u64 v[206:207], v[204:205], 0, s[52:53]
	s_mov_b32 m0, s63
	s_nop 0
	global_load_lds_dwordx4 v[206:207], off
	s_waitcnt vmcnt(8)
	s_waitcnt lgkmcnt(0)
	s_barrier
	s_waitcnt lgkmcnt(0)
	v_mfma_f32_16x16x32_bf16 v[124:127], v[136:139], v[170:173], v[124:127]
	v_mfma_f32_16x16x32_bf16 v[120:123], v[144:147], v[170:173], v[120:123]
	v_mfma_f32_16x16x32_bf16 v[108:111], v[136:139], v[178:181], v[108:111]
	v_mfma_f32_16x16x32_bf16 v[104:107], v[144:147], v[178:181], v[104:107]
	v_mfma_f32_16x16x32_bf16 v[92:95], v[136:139], v[186:189], v[92:95]
	v_mfma_f32_16x16x32_bf16 v[88:91], v[144:147], v[186:189], v[88:91]
	v_mfma_f32_16x16x32_bf16 v[76:79], v[136:139], v[194:197], v[76:79]
	v_mfma_f32_16x16x32_bf16 v[72:75], v[144:147], v[194:197], v[72:75]
	v_mfma_f32_16x16x32_bf16 v[124:127], v[140:143], v[174:177], v[124:127]
	v_mfma_f32_16x16x32_bf16 v[120:123], v[148:151], v[174:177], v[120:123]
	v_mfma_f32_16x16x32_bf16 v[108:111], v[140:143], v[182:185], v[108:111]
	v_mfma_f32_16x16x32_bf16 v[104:107], v[148:151], v[182:185], v[104:107]
	v_mfma_f32_16x16x32_bf16 v[92:95], v[140:143], v[190:193], v[92:95]
	v_mfma_f32_16x16x32_bf16 v[88:91], v[148:151], v[190:193], v[88:91]
	v_mfma_f32_16x16x32_bf16 v[76:79], v[140:143], v[198:201], v[76:79]
	v_mfma_f32_16x16x32_bf16 v[72:75], v[148:151], v[198:201], v[72:75]
	v_mfma_f32_16x16x32_bf16 v[116:119], v[152:155], v[170:173], v[116:119]
	v_mfma_f32_16x16x32_bf16 v[112:115], v[162:165], v[170:173], v[112:115]
	v_mfma_f32_16x16x32_bf16 v[100:103], v[152:155], v[178:181], v[100:103]
	v_mfma_f32_16x16x32_bf16 v[96:99], v[162:165], v[178:181], v[96:99]
	v_mfma_f32_16x16x32_bf16 v[84:87], v[152:155], v[186:189], v[84:87]
	v_mfma_f32_16x16x32_bf16 v[80:83], v[162:165], v[186:189], v[80:83]
	v_mfma_f32_16x16x32_bf16 v[68:71], v[152:155], v[194:197], v[68:71]
	v_mfma_f32_16x16x32_bf16 v[64:67], v[162:165], v[194:197], v[64:67]
	v_mfma_f32_16x16x32_bf16 v[116:119], v[156:159], v[174:177], v[116:119]
	v_mfma_f32_16x16x32_bf16 v[112:115], v[166:169], v[174:177], v[112:115]
	v_mfma_f32_16x16x32_bf16 v[100:103], v[156:159], v[182:185], v[100:103]
	v_mfma_f32_16x16x32_bf16 v[96:99], v[166:169], v[182:185], v[96:99]
	v_mfma_f32_16x16x32_bf16 v[84:87], v[156:159], v[190:193], v[84:87]
	v_mfma_f32_16x16x32_bf16 v[80:83], v[166:169], v[190:193], v[80:83]
	v_mfma_f32_16x16x32_bf16 v[68:71], v[156:159], v[198:201], v[68:71]
	v_mfma_f32_16x16x32_bf16 v[64:67], v[166:169], v[198:201], v[64:67]
	s_barrier
	s_add_i32 s2, s2, s10
	v_lshl_add_u64 v[206:207], v[202:203], 0, s[56:57]
	s_mov_b32 m0, s2
	ds_read_b128 v[170:173], v135 offset:49152
	ds_read_b128 v[174:177], v135 offset:50176
	ds_read_b128 v[178:181], v135 offset:51200
	ds_read_b128 v[182:185], v135 offset:52224
	ds_read_b128 v[186:189], v135 offset:53248
	ds_read_b128 v[190:193], v135 offset:54272
	ds_read_b128 v[194:197], v135 offset:55296
	ds_read_b128 v[198:201], v135 offset:56320
	global_load_lds_dwordx4 v[206:207], off
	v_lshl_add_u64 v[206:207], v[202:203], 0, s[0:1]
	s_add_i32 m0, s2, 0x2000
	s_add_i32 s2, s3, s10
	global_load_lds_dwordx4 v[206:207], off
	v_lshl_add_u64 v[206:207], v[202:203], 0, s[24:25]
	s_mov_b32 m0, s2
	v_lshl_add_u64 v[202:203], v[202:203], 0, s[26:27]
	global_load_lds_dwordx4 v[206:207], off
	s_add_i32 m0, s2, 0x2000
	s_nop 0
	global_load_lds_dwordx4 v[202:203], off
	v_lshl_add_u64 v[202:203], v[204:205], 0, s[56:57]
	s_mov_b32 m0, s75
	s_nop 0
	global_load_lds_dwordx4 v[202:203], off
	v_lshl_add_u64 v[202:203], v[204:205], 0, s[0:1]
	s_mov_b32 m0, s77
	s_nop 0
	global_load_lds_dwordx4 v[202:203], off
	s_waitcnt vmcnt(8)
	s_waitcnt lgkmcnt(0)
	s_barrier
	s_waitcnt lgkmcnt(0)
	v_mfma_f32_16x16x32_bf16 v[60:63], v[136:139], v[170:173], v[60:63]
	v_mfma_f32_16x16x32_bf16 v[56:59], v[144:147], v[170:173], v[56:59]
	v_mfma_f32_16x16x32_bf16 v[44:47], v[136:139], v[178:181], v[44:47]
	v_mfma_f32_16x16x32_bf16 v[40:43], v[144:147], v[178:181], v[40:43]
	v_mfma_f32_16x16x32_bf16 v[28:31], v[136:139], v[186:189], v[28:31]
	v_mfma_f32_16x16x32_bf16 v[24:27], v[144:147], v[186:189], v[24:27]
	v_mfma_f32_16x16x32_bf16 v[12:15], v[136:139], v[194:197], v[12:15]
	v_mfma_f32_16x16x32_bf16 v[8:11], v[144:147], v[194:197], v[8:11]
	v_mfma_f32_16x16x32_bf16 v[60:63], v[140:143], v[174:177], v[60:63]
	v_mfma_f32_16x16x32_bf16 v[56:59], v[148:151], v[174:177], v[56:59]
	v_mfma_f32_16x16x32_bf16 v[44:47], v[140:143], v[182:185], v[44:47]
	v_mfma_f32_16x16x32_bf16 v[40:43], v[148:151], v[182:185], v[40:43]
	v_mfma_f32_16x16x32_bf16 v[28:31], v[140:143], v[190:193], v[28:31]
	v_mfma_f32_16x16x32_bf16 v[24:27], v[148:151], v[190:193], v[24:27]
	v_mfma_f32_16x16x32_bf16 v[12:15], v[140:143], v[198:201], v[12:15]
	v_mfma_f32_16x16x32_bf16 v[8:11], v[148:151], v[198:201], v[8:11]
	v_mfma_f32_16x16x32_bf16 v[52:55], v[152:155], v[170:173], v[52:55]
	v_mfma_f32_16x16x32_bf16 v[48:51], v[162:165], v[170:173], v[48:51]
	v_mfma_f32_16x16x32_bf16 v[36:39], v[152:155], v[178:181], v[36:39]
	v_mfma_f32_16x16x32_bf16 v[32:35], v[162:165], v[178:181], v[32:35]
	v_mfma_f32_16x16x32_bf16 v[20:23], v[152:155], v[186:189], v[20:23]
	v_mfma_f32_16x16x32_bf16 v[16:19], v[162:165], v[186:189], v[16:19]
	v_mfma_f32_16x16x32_bf16 v[4:7], v[152:155], v[194:197], v[4:7]
	v_mfma_f32_16x16x32_bf16 v[0:3], v[162:165], v[194:197], v[0:3]
	v_mfma_f32_16x16x32_bf16 v[52:55], v[156:159], v[174:177], v[52:55]
	v_mfma_f32_16x16x32_bf16 v[48:51], v[166:169], v[174:177], v[48:51]
	v_mfma_f32_16x16x32_bf16 v[36:39], v[156:159], v[182:185], v[36:39]
	v_mfma_f32_16x16x32_bf16 v[32:35], v[166:169], v[182:185], v[32:35]
	v_mfma_f32_16x16x32_bf16 v[20:23], v[156:159], v[190:193], v[20:23]
	v_mfma_f32_16x16x32_bf16 v[16:19], v[166:169], v[190:193], v[16:19]
	v_mfma_f32_16x16x32_bf16 v[4:7], v[156:159], v[198:201], v[4:7]
	v_mfma_f32_16x16x32_bf16 v[0:3], v[166:169], v[198:201], v[0:3]
	s_barrier
	s_add_u32 s54, s54, 0x100
	s_addc_u32 s55, s55, 0
	s_add_u32 s22, s22, 0x100
	s_addc_u32 s23, s23, 0
	s_cmp_ge_i32 s38, s74
	s_mov_b32 s2, s38
	s_cbranch_scc0 .LBB0_206

.LBB0_339:
	s_add_i32 s22, s2, 2
	s_add_u32 s23, s90, 0xfffe0080
	s_addc_u32 s3, s91, -1
	s_cmp_eq_u32 s83, s2
	s_cselect_b32 s3, s47, s3
	s_cselect_b32 s2, s93, s23
	s_cselect_b32 s35, s95, s38
	s_cselect_b32 s34, vcc_lo, vcc_hi
	s_add_i32 s23, 0, 0x10000
	s_add_i32 s39, 0, 0x14000
	v_add_u32_e32 v148, s23, v133
	v_add_u32_e32 v166, s39, v133
	ds_read_b128 v[136:139], v148
	ds_read_b128 v[140:143], v148 offset:1024
	ds_read_b128 v[144:147], v148 offset:2048
	ds_read_b128 v[148:151], v148 offset:3072
	ds_read_b128 v[152:155], v166
	ds_read_b128 v[156:159], v166 offset:1024
	ds_read_b128 v[162:165], v166 offset:2048
	ds_read_b128 v[166:169], v166 offset:3072
	v_lshl_add_u64 v[202:203], s[90:91], 0, v[130:131]
	s_add_i32 m0, s59, 0xc000
	ds_read_b128 v[170:173], v135
	ds_read_b128 v[174:177], v135 offset:1024
	ds_read_b128 v[178:181], v135 offset:2048
	ds_read_b128 v[182:185], v135 offset:3072
	ds_read_b128 v[186:189], v135 offset:4096
	ds_read_b128 v[190:193], v135 offset:5120
	ds_read_b128 v[194:197], v135 offset:6144
	ds_read_b128 v[198:201], v135 offset:7168
	global_load_lds_dwordx4 v[202:203], off
	v_lshl_add_u64 v[202:203], v[202:203], 0, s[8:9]
	s_add_i32 m0, s59, 0xe000
	s_nop 0
	global_load_lds_dwordx4 v[202:203], off
	s_waitcnt vmcnt(8)
	s_waitcnt lgkmcnt(0)
	s_barrier
	s_waitcnt lgkmcnt(0)
	v_mfma_f32_16x16x32_bf16 v[124:127], v[136:139], v[170:173], v[124:127]
	v_mfma_f32_16x16x32_bf16 v[120:123], v[144:147], v[170:173], v[120:123]
	v_mfma_f32_16x16x32_bf16 v[108:111], v[136:139], v[178:181], v[108:111]
	v_mfma_f32_16x16x32_bf16 v[104:107], v[144:147], v[178:181], v[104:107]
	v_mfma_f32_16x16x32_bf16 v[92:95], v[136:139], v[186:189], v[92:95]
	v_mfma_f32_16x16x32_bf16 v[88:91], v[144:147], v[186:189], v[88:91]
	v_mfma_f32_16x16x32_bf16 v[76:79], v[136:139], v[194:197], v[76:79]
	v_mfma_f32_16x16x32_bf16 v[72:75], v[144:147], v[194:197], v[72:75]
	v_mfma_f32_16x16x32_bf16 v[124:127], v[140:143], v[174:177], v[124:127]
	v_mfma_f32_16x16x32_bf16 v[120:123], v[148:151], v[174:177], v[120:123]
	v_mfma_f32_16x16x32_bf16 v[108:111], v[140:143], v[182:185], v[108:111]
	v_mfma_f32_16x16x32_bf16 v[104:107], v[148:151], v[182:185], v[104:107]
	v_mfma_f32_16x16x32_bf16 v[92:95], v[140:143], v[190:193], v[92:95]
	v_mfma_f32_16x16x32_bf16 v[88:91], v[148:151], v[190:193], v[88:91]
	v_mfma_f32_16x16x32_bf16 v[76:79], v[140:143], v[198:201], v[76:79]
	v_mfma_f32_16x16x32_bf16 v[72:75], v[148:151], v[198:201], v[72:75]
	v_mfma_f32_16x16x32_bf16 v[116:119], v[152:155], v[170:173], v[116:119]
	v_mfma_f32_16x16x32_bf16 v[112:115], v[162:165], v[170:173], v[112:115]
	v_mfma_f32_16x16x32_bf16 v[100:103], v[152:155], v[178:181], v[100:103]
	v_mfma_f32_16x16x32_bf16 v[96:99], v[162:165], v[178:181], v[96:99]
	v_mfma_f32_16x16x32_bf16 v[84:87], v[152:155], v[186:189], v[84:87]
	v_mfma_f32_16x16x32_bf16 v[80:83], v[162:165], v[186:189], v[80:83]
	v_mfma_f32_16x16x32_bf16 v[68:71], v[152:155], v[194:197], v[68:71]
	v_mfma_f32_16x16x32_bf16 v[64:67], v[162:165], v[194:197], v[64:67]
	v_mfma_f32_16x16x32_bf16 v[116:119], v[156:159], v[174:177], v[116:119]
	v_mfma_f32_16x16x32_bf16 v[112:115], v[166:169], v[174:177], v[112:115]
	v_mfma_f32_16x16x32_bf16 v[100:103], v[156:159], v[182:185], v[100:103]
	v_mfma_f32_16x16x32_bf16 v[96:99], v[166:169], v[182:185], v[96:99]
	v_mfma_f32_16x16x32_bf16 v[84:87], v[156:159], v[190:193], v[84:87]
	v_mfma_f32_16x16x32_bf16 v[80:83], v[166:169], v[190:193], v[80:83]
	v_mfma_f32_16x16x32_bf16 v[68:71], v[156:159], v[198:201], v[68:71]
	v_mfma_f32_16x16x32_bf16 v[64:67], v[166:169], v[198:201], v[64:67]
	s_barrier
	s_add_i32 s23, s23, s58
	v_lshl_add_u64 v[202:203], s[34:35], 0, v[160:161]
	s_mov_b32 m0, s23
	ds_read_b128 v[170:173], v135 offset:16384
	ds_read_b128 v[174:177], v135 offset:17408
	ds_read_b128 v[178:181], v135 offset:18432
	ds_read_b128 v[182:185], v135 offset:19456
	ds_read_b128 v[186:189], v135 offset:20480
	ds_read_b128 v[190:193], v135 offset:21504
	ds_read_b128 v[194:197], v135 offset:22528
	ds_read_b128 v[198:201], v135 offset:23552
	global_load_lds_dwordx4 v[202:203], off
	v_lshl_add_u64 v[204:205], v[202:203], 0, s[64:65]
	s_add_i32 m0, s23, 0x2000
	s_add_i32 s23, s39, s58
	global_load_lds_dwordx4 v[204:205], off
	v_lshl_add_u64 v[204:205], v[202:203], 0, s[8:9]
	s_mov_b32 m0, s23
	s_nop 0
	global_load_lds_dwordx4 v[204:205], off
	v_lshl_add_u64 v[204:205], v[202:203], 0, s[4:5]
	s_add_i32 m0, s23, 0x2000
	s_nop 0
	global_load_lds_dwordx4 v[204:205], off
	v_lshl_add_u64 v[204:205], s[2:3], 0, v[128:129]
	s_mov_b32 m0, s59
	v_lshl_add_u64 v[206:207], v[204:205], 0, s[8:9]
	global_load_lds_dwordx4 v[204:205], off
	s_mov_b32 m0, s63
	s_nop 0
	global_load_lds_dwordx4 v[206:207], off
	s_waitcnt vmcnt(8)
	s_waitcnt lgkmcnt(0)
	s_barrier
	s_waitcnt lgkmcnt(0)
	v_mfma_f32_16x16x32_bf16 v[60:63], v[136:139], v[170:173], v[60:63]
	v_mfma_f32_16x16x32_bf16 v[56:59], v[144:147], v[170:173], v[56:59]
	v_mfma_f32_16x16x32_bf16 v[44:47], v[136:139], v[178:181], v[44:47]
	v_mfma_f32_16x16x32_bf16 v[40:43], v[144:147], v[178:181], v[40:43]
	v_mfma_f32_16x16x32_bf16 v[28:31], v[136:139], v[186:189], v[28:31]
	v_mfma_f32_16x16x32_bf16 v[24:27], v[144:147], v[186:189], v[24:27]
	v_mfma_f32_16x16x32_bf16 v[12:15], v[136:139], v[194:197], v[12:15]
	v_mfma_f32_16x16x32_bf16 v[8:11], v[144:147], v[194:197], v[8:11]
	v_mfma_f32_16x16x32_bf16 v[60:63], v[140:143], v[174:177], v[60:63]
	v_mfma_f32_16x16x32_bf16 v[56:59], v[148:151], v[174:177], v[56:59]
	v_mfma_f32_16x16x32_bf16 v[44:47], v[140:143], v[182:185], v[44:47]
	v_mfma_f32_16x16x32_bf16 v[40:43], v[148:151], v[182:185], v[40:43]
	v_mfma_f32_16x16x32_bf16 v[28:31], v[140:143], v[190:193], v[28:31]
	v_mfma_f32_16x16x32_bf16 v[24:27], v[148:151], v[190:193], v[24:27]
	v_mfma_f32_16x16x32_bf16 v[12:15], v[140:143], v[198:201], v[12:15]
	v_mfma_f32_16x16x32_bf16 v[8:11], v[148:151], v[198:201], v[8:11]
	v_mfma_f32_16x16x32_bf16 v[52:55], v[152:155], v[170:173], v[52:55]
	v_mfma_f32_16x16x32_bf16 v[48:51], v[162:165], v[170:173], v[48:51]
	v_mfma_f32_16x16x32_bf16 v[36:39], v[152:155], v[178:181], v[36:39]
	v_mfma_f32_16x16x32_bf16 v[32:35], v[162:165], v[178:181], v[32:35]
	v_mfma_f32_16x16x32_bf16 v[20:23], v[152:155], v[186:189], v[20:23]
	v_mfma_f32_16x16x32_bf16 v[16:19], v[162:165], v[186:189], v[16:19]
	v_mfma_f32_16x16x32_bf16 v[4:7], v[152:155], v[194:197], v[4:7]
	v_mfma_f32_16x16x32_bf16 v[0:3], v[162:165], v[194:197], v[0:3]
	v_mfma_f32_16x16x32_bf16 v[52:55], v[156:159], v[174:177], v[52:55]
	v_mfma_f32_16x16x32_bf16 v[48:51], v[166:169], v[174:177], v[48:51]
	v_mfma_f32_16x16x32_bf16 v[36:39], v[156:159], v[182:185], v[36:39]
	v_mfma_f32_16x16x32_bf16 v[32:35], v[166:169], v[182:185], v[32:35]
	v_mfma_f32_16x16x32_bf16 v[20:23], v[156:159], v[190:193], v[20:23]
	v_mfma_f32_16x16x32_bf16 v[16:19], v[166:169], v[190:193], v[16:19]
	v_mfma_f32_16x16x32_bf16 v[4:7], v[156:159], v[198:201], v[4:7]
	v_mfma_f32_16x16x32_bf16 v[0:3], v[166:169], v[198:201], v[0:3]
	s_barrier
	s_add_i32 s2, 0, 0x18000
	s_add_i32 s3, 0, 0x1c000
	v_add_u32_e32 v148, s2, v133
	v_add_u32_e32 v166, s3, v133
	ds_read_b128 v[136:139], v148
	ds_read_b128 v[140:143], v148 offset:1024
	ds_read_b128 v[144:147], v148 offset:2048
	ds_read_b128 v[148:151], v148 offset:3072
	ds_read_b128 v[152:155], v166
	ds_read_b128 v[156:159], v166 offset:1024
	ds_read_b128 v[162:165], v166 offset:2048
	ds_read_b128 v[166:169], v166 offset:3072
	s_mov_b32 m0, s77
	v_lshl_add_u64 v[206:207], v[204:205], 0, s[14:15]
	ds_read_b128 v[170:173], v135 offset:32768
	ds_read_b128 v[174:177], v135 offset:33792
	ds_read_b128 v[178:181], v135 offset:34816
	ds_read_b128 v[182:185], v135 offset:35840
	ds_read_b128 v[186:189], v135 offset:36864
	ds_read_b128 v[190:193], v135 offset:37888
	ds_read_b128 v[194:197], v135 offset:38912
	ds_read_b128 v[198:201], v135 offset:39936
	global_load_lds_dwordx4 v[206:207], off
	v_lshl_add_u64 v[206:207], v[204:205], 0, s[16:17]
	s_mov_b32 m0, s78
	s_nop 0
	global_load_lds_dwordx4 v[206:207], off
	s_waitcnt vmcnt(8)
	s_waitcnt lgkmcnt(0)
	s_barrier
	s_waitcnt lgkmcnt(0)
	v_mfma_f32_16x16x32_bf16 v[124:127], v[136:139], v[170:173], v[124:127]
	v_mfma_f32_16x16x32_bf16 v[120:123], v[144:147], v[170:173], v[120:123]
	v_mfma_f32_16x16x32_bf16 v[108:111], v[136:139], v[178:181], v[108:111]
	v_mfma_f32_16x16x32_bf16 v[104:107], v[144:147], v[178:181], v[104:107]
	v_mfma_f32_16x16x32_bf16 v[92:95], v[136:139], v[186:189], v[92:95]
	v_mfma_f32_16x16x32_bf16 v[88:91], v[144:147], v[186:189], v[88:91]
	v_mfma_f32_16x16x32_bf16 v[76:79], v[136:139], v[194:197], v[76:79]
	v_mfma_f32_16x16x32_bf16 v[72:75], v[144:147], v[194:197], v[72:75]
	v_mfma_f32_16x16x32_bf16 v[124:127], v[140:143], v[174:177], v[124:127]
	v_mfma_f32_16x16x32_bf16 v[120:123], v[148:151], v[174:177], v[120:123]
	v_mfma_f32_16x16x32_bf16 v[108:111], v[140:143], v[182:185], v[108:111]
	v_mfma_f32_16x16x32_bf16 v[104:107], v[148:151], v[182:185], v[104:107]
	v_mfma_f32_16x16x32_bf16 v[92:95], v[140:143], v[190:193], v[92:95]
	v_mfma_f32_16x16x32_bf16 v[88:91], v[148:151], v[190:193], v[88:91]
	v_mfma_f32_16x16x32_bf16 v[76:79], v[140:143], v[198:201], v[76:79]
	v_mfma_f32_16x16x32_bf16 v[72:75], v[148:151], v[198:201], v[72:75]
	v_mfma_f32_16x16x32_bf16 v[116:119], v[152:155], v[170:173], v[116:119]
	v_mfma_f32_16x16x32_bf16 v[112:115], v[162:165], v[170:173], v[112:115]
	v_mfma_f32_16x16x32_bf16 v[100:103], v[152:155], v[178:181], v[100:103]
	v_mfma_f32_16x16x32_bf16 v[96:99], v[162:165], v[178:181], v[96:99]
	v_mfma_f32_16x16x32_bf16 v[84:87], v[152:155], v[186:189], v[84:87]
	v_mfma_f32_16x16x32_bf16 v[80:83], v[162:165], v[186:189], v[80:83]
	v_mfma_f32_16x16x32_bf16 v[68:71], v[152:155], v[194:197], v[68:71]
	v_mfma_f32_16x16x32_bf16 v[64:67], v[162:165], v[194:197], v[64:67]
	v_mfma_f32_16x16x32_bf16 v[116:119], v[156:159], v[174:177], v[116:119]
	v_mfma_f32_16x16x32_bf16 v[112:115], v[166:169], v[174:177], v[112:115]
	v_mfma_f32_16x16x32_bf16 v[100:103], v[156:159], v[182:185], v[100:103]
	v_mfma_f32_16x16x32_bf16 v[96:99], v[166:169], v[182:185], v[96:99]
	v_mfma_f32_16x16x32_bf16 v[84:87], v[156:159], v[190:193], v[84:87]
	v_mfma_f32_16x16x32_bf16 v[80:83], v[166:169], v[190:193], v[80:83]
	v_mfma_f32_16x16x32_bf16 v[68:71], v[156:159], v[198:201], v[68:71]
	v_mfma_f32_16x16x32_bf16 v[64:67], v[166:169], v[198:201], v[64:67]
	s_barrier
	s_add_i32 s2, s2, s58
	v_lshl_add_u64 v[206:207], v[202:203], 0, s[56:57]
	s_mov_b32 m0, s2
	ds_read_b128 v[170:173], v135 offset:49152
	ds_read_b128 v[174:177], v135 offset:50176
	ds_read_b128 v[178:181], v135 offset:51200
	ds_read_b128 v[182:185], v135 offset:52224
	ds_read_b128 v[186:189], v135 offset:53248
	ds_read_b128 v[190:193], v135 offset:54272
	ds_read_b128 v[194:197], v135 offset:55296
	ds_read_b128 v[198:201], v135 offset:56320
	global_load_lds_dwordx4 v[206:207], off
	v_lshl_add_u64 v[206:207], v[202:203], 0, s[12:13]
	s_add_i32 m0, s2, 0x2000
	s_add_i32 s2, s3, s58
	global_load_lds_dwordx4 v[206:207], off
	v_lshl_add_u64 v[206:207], v[202:203], 0, s[28:29]
	s_mov_b32 m0, s2
	v_lshl_add_u64 v[202:203], v[202:203], 0, s[88:89]
	global_load_lds_dwordx4 v[206:207], off
	s_add_i32 m0, s2, 0x2000
	s_nop 0
	global_load_lds_dwordx4 v[202:203], off
	v_lshl_add_u64 v[202:203], v[204:205], 0, s[56:57]
	s_mov_b32 m0, s79
	s_nop 0
	global_load_lds_dwordx4 v[202:203], off
	v_lshl_add_u64 v[202:203], v[204:205], 0, s[28:29]
	s_mov_b32 m0, s80
	s_nop 0
	global_load_lds_dwordx4 v[202:203], off
	s_waitcnt vmcnt(8)
	s_waitcnt lgkmcnt(0)
	s_barrier
	s_waitcnt lgkmcnt(0)
	v_mfma_f32_16x16x32_bf16 v[60:63], v[136:139], v[170:173], v[60:63]
	v_mfma_f32_16x16x32_bf16 v[56:59], v[144:147], v[170:173], v[56:59]
	v_mfma_f32_16x16x32_bf16 v[44:47], v[136:139], v[178:181], v[44:47]
	v_mfma_f32_16x16x32_bf16 v[40:43], v[144:147], v[178:181], v[40:43]
	v_mfma_f32_16x16x32_bf16 v[28:31], v[136:139], v[186:189], v[28:31]
	v_mfma_f32_16x16x32_bf16 v[24:27], v[144:147], v[186:189], v[24:27]
	v_mfma_f32_16x16x32_bf16 v[12:15], v[136:139], v[194:197], v[12:15]
	v_mfma_f32_16x16x32_bf16 v[8:11], v[144:147], v[194:197], v[8:11]
	v_mfma_f32_16x16x32_bf16 v[60:63], v[140:143], v[174:177], v[60:63]
	v_mfma_f32_16x16x32_bf16 v[56:59], v[148:151], v[174:177], v[56:59]
	v_mfma_f32_16x16x32_bf16 v[44:47], v[140:143], v[182:185], v[44:47]
	v_mfma_f32_16x16x32_bf16 v[40:43], v[148:151], v[182:185], v[40:43]
	v_mfma_f32_16x16x32_bf16 v[28:31], v[140:143], v[190:193], v[28:31]
	v_mfma_f32_16x16x32_bf16 v[24:27], v[148:151], v[190:193], v[24:27]
	v_mfma_f32_16x16x32_bf16 v[12:15], v[140:143], v[198:201], v[12:15]
	v_mfma_f32_16x16x32_bf16 v[8:11], v[148:151], v[198:201], v[8:11]
	v_mfma_f32_16x16x32_bf16 v[52:55], v[152:155], v[170:173], v[52:55]
	v_mfma_f32_16x16x32_bf16 v[48:51], v[162:165], v[170:173], v[48:51]
	v_mfma_f32_16x16x32_bf16 v[36:39], v[152:155], v[178:181], v[36:39]
	v_mfma_f32_16x16x32_bf16 v[32:35], v[162:165], v[178:181], v[32:35]
	v_mfma_f32_16x16x32_bf16 v[20:23], v[152:155], v[186:189], v[20:23]
	v_mfma_f32_16x16x32_bf16 v[16:19], v[162:165], v[186:189], v[16:19]
	v_mfma_f32_16x16x32_bf16 v[4:7], v[152:155], v[194:197], v[4:7]
	v_mfma_f32_16x16x32_bf16 v[0:3], v[162:165], v[194:197], v[0:3]
	v_mfma_f32_16x16x32_bf16 v[52:55], v[156:159], v[174:177], v[52:55]
	v_mfma_f32_16x16x32_bf16 v[48:51], v[166:169], v[174:177], v[48:51]
	v_mfma_f32_16x16x32_bf16 v[36:39], v[156:159], v[182:185], v[36:39]
	v_mfma_f32_16x16x32_bf16 v[32:35], v[166:169], v[182:185], v[32:35]
	v_mfma_f32_16x16x32_bf16 v[20:23], v[156:159], v[190:193], v[20:23]
	v_mfma_f32_16x16x32_bf16 v[16:19], v[166:169], v[190:193], v[16:19]
	v_mfma_f32_16x16x32_bf16 v[4:7], v[156:159], v[198:201], v[4:7]
	v_mfma_f32_16x16x32_bf16 v[0:3], v[166:169], v[198:201], v[0:3]
	s_barrier
	s_add_u32 vcc_hi, vcc_hi, 0x100
	s_addc_u32 s38, s38, 0
	s_add_u32 s90, s90, 0x100
	s_addc_u32 s91, s91, 0
	s_cmp_ge_i32 s22, s81
	s_mov_b32 s2, s22
	s_cbranch_scc0 .LBB0_339

.LBB0_778:
	ds_read_b128 v[20:23], v178
	ds_read_b128 v[24:27], v179
	ds_read_b128 v[16:19], v174
	ds_read_b128 v[0:3], v175
	ds_read_b128 v[28:31], v180
	ds_read_b128 v[4:7], v181
	ds_read_b128 v[8:11], v182
	ds_read_b128 v[12:15], v183
	s_add_i32 vcc_hi, s2, 2
	s_add_u32 s22, s18, 0xfffe0080
	s_addc_u32 s3, s19, -1
	s_cmp_eq_u32 s91, s2
	s_cselect_b32 s2, s47, s22
	s_cselect_b32 s3, s45, s3
	s_cselect_b32 s23, s92, vcc_lo
	s_cselect_b32 s22, s93, s95
	v_add_u32_e32 v224, s90, v173
	v_lshl_add_u64 v[168:169], s[18:19], 0, v[166:167]
	s_add_i32 m0, s54, 0xc000
	ds_read_b128 v[190:193], v224
	ds_read_b128 v[194:197], v224 offset:1024
	ds_read_b128 v[198:201], v224 offset:2048
	ds_read_b128 v[202:205], v224 offset:3072
	ds_read_b128 v[206:209], v224 offset:4096
	ds_read_b128 v[210:213], v224 offset:5120
	ds_read_b128 v[214:217], v224 offset:6144
	ds_read_b128 v[218:221], v224 offset:7168
	global_load_lds_dwordx4 v[168:169], off
	v_lshl_add_u64 v[168:169], v[168:169], 0, s[8:9]
	s_add_i32 m0, s54, 0xe000
	s_nop 0
	global_load_lds_dwordx4 v[168:169], off
	s_waitcnt vmcnt(8)
	s_waitcnt lgkmcnt(0)
	s_barrier
	s_waitcnt lgkmcnt(0)
	v_mfma_f32_16x16x128_f8f6f4 v[156:159], v[16:23], v[190:197], v[156:159]
	v_mfma_f32_16x16x128_f8f6f4 v[152:155], v[24:31], v[190:197], v[152:155]
	v_mfma_f32_16x16x128_f8f6f4 v[140:143], v[16:23], v[198:205], v[140:143]
	v_mfma_f32_16x16x128_f8f6f4 v[136:139], v[24:31], v[198:205], v[136:139]
	v_mfma_f32_16x16x128_f8f6f4 v[124:127], v[16:23], v[206:213], v[124:127]
	v_mfma_f32_16x16x128_f8f6f4 v[120:123], v[24:31], v[206:213], v[120:123]
	v_mfma_f32_16x16x128_f8f6f4 v[108:111], v[16:23], v[214:221], v[108:111]
	v_mfma_f32_16x16x128_f8f6f4 v[104:107], v[24:31], v[214:221], v[104:107]
	v_mfma_f32_16x16x128_f8f6f4 v[148:151], v[0:7], v[190:197], v[148:151]
	v_mfma_f32_16x16x128_f8f6f4 v[144:147], v[8:15], v[190:197], v[144:147]
	v_mfma_f32_16x16x128_f8f6f4 v[132:135], v[0:7], v[198:205], v[132:135]
	v_mfma_f32_16x16x128_f8f6f4 v[128:131], v[8:15], v[198:205], v[128:131]
	v_mfma_f32_16x16x128_f8f6f4 v[116:119], v[0:7], v[206:213], v[116:119]
	v_mfma_f32_16x16x128_f8f6f4 v[112:115], v[8:15], v[206:213], v[112:115]
	v_mfma_f32_16x16x128_f8f6f4 v[100:103], v[0:7], v[214:221], v[100:103]
	v_mfma_f32_16x16x128_f8f6f4 v[96:99], v[8:15], v[214:221], v[96:99]
	s_barrier
	s_mov_b32 m0, s55
	v_lshl_add_u64 v[168:169], s[22:23], 0, v[160:161]
	ds_read_b128 v[190:193], v224 offset:16384
	ds_read_b128 v[194:197], v224 offset:17408
	ds_read_b128 v[198:201], v224 offset:18432
	ds_read_b128 v[202:205], v224 offset:19456
	ds_read_b128 v[206:209], v224 offset:20480
	ds_read_b128 v[210:213], v224 offset:21504
	ds_read_b128 v[214:217], v224 offset:22528
	ds_read_b128 v[218:221], v224 offset:23552
	global_load_lds_dwordx4 v[168:169], off
	v_lshl_add_u64 v[170:171], v[168:169], 0, s[8:9]
	s_mov_b32 m0, s58
	s_nop 0
	global_load_lds_dwordx4 v[170:171], off
	v_lshl_add_u64 v[170:171], v[168:169], 0, s[14:15]
	s_mov_b32 m0, s59
	s_nop 0
	global_load_lds_dwordx4 v[170:171], off
	v_lshl_add_u64 v[170:171], v[168:169], 0, s[16:17]
	s_mov_b32 m0, s63
	s_nop 0
	global_load_lds_dwordx4 v[170:171], off
	v_lshl_add_u64 v[170:171], s[2:3], 0, v[162:163]
	s_mov_b32 m0, s54
	v_lshl_add_u64 v[222:223], v[170:171], 0, s[8:9]
	global_load_lds_dwordx4 v[170:171], off
	s_mov_b32 m0, s74
	s_nop 0
	global_load_lds_dwordx4 v[222:223], off
	s_waitcnt vmcnt(8)
	s_waitcnt lgkmcnt(0)
	s_barrier
	s_waitcnt lgkmcnt(0)
	v_mfma_f32_16x16x128_f8f6f4 v[92:95], v[16:23], v[190:197], v[92:95]
	v_mfma_f32_16x16x128_f8f6f4 v[88:91], v[24:31], v[190:197], v[88:91]
	v_mfma_f32_16x16x128_f8f6f4 v[76:79], v[16:23], v[198:205], v[76:79]
	v_mfma_f32_16x16x128_f8f6f4 v[72:75], v[24:31], v[198:205], v[72:75]
	v_mfma_f32_16x16x128_f8f6f4 v[60:63], v[16:23], v[206:213], v[60:63]
	v_mfma_f32_16x16x128_f8f6f4 v[56:59], v[24:31], v[206:213], v[56:59]
	v_mfma_f32_16x16x128_f8f6f4 v[44:47], v[16:23], v[214:221], v[44:47]
	v_mfma_f32_16x16x128_f8f6f4 v[40:43], v[24:31], v[214:221], v[40:43]
	v_mfma_f32_16x16x128_f8f6f4 v[84:87], v[0:7], v[190:197], v[84:87]
	v_mfma_f32_16x16x128_f8f6f4 v[80:83], v[8:15], v[190:197], v[80:83]
	v_mfma_f32_16x16x128_f8f6f4 v[68:71], v[0:7], v[198:205], v[68:71]
	v_mfma_f32_16x16x128_f8f6f4 v[64:67], v[8:15], v[198:205], v[64:67]
	v_mfma_f32_16x16x128_f8f6f4 v[52:55], v[0:7], v[206:213], v[52:55]
	v_mfma_f32_16x16x128_f8f6f4 v[48:51], v[8:15], v[206:213], v[48:51]
	v_mfma_f32_16x16x128_f8f6f4 v[36:39], v[0:7], v[214:221], v[36:39]
	v_mfma_f32_16x16x128_f8f6f4 v[32:35], v[8:15], v[214:221], v[32:35]
	s_barrier
	ds_read_b128 v[4:7], v184
	ds_read_b128 v[8:11], v185
	ds_read_b128 v[0:3], v176
	ds_read_b128 v[16:19], v177
	ds_read_b128 v[12:15], v186
	ds_read_b128 v[20:23], v187
	ds_read_b128 v[24:27], v188
	ds_read_b128 v[28:31], v189
	s_mov_b32 m0, s75
	v_lshl_add_u64 v[222:223], v[170:171], 0, s[14:15]
	ds_read_b128 v[190:193], v224 offset:32768
	ds_read_b128 v[194:197], v224 offset:33792
	ds_read_b128 v[198:201], v224 offset:34816
	ds_read_b128 v[202:205], v224 offset:35840
	ds_read_b128 v[206:209], v224 offset:36864
	ds_read_b128 v[210:213], v224 offset:37888
	ds_read_b128 v[214:217], v224 offset:38912
	ds_read_b128 v[218:221], v224 offset:39936
	global_load_lds_dwordx4 v[222:223], off
	v_lshl_add_u64 v[222:223], v[170:171], 0, s[16:17]
	s_mov_b32 m0, s77
	s_nop 0
	global_load_lds_dwordx4 v[222:223], off
	s_waitcnt vmcnt(8)
	s_waitcnt lgkmcnt(0)
	s_barrier
	s_waitcnt lgkmcnt(0)
	v_mfma_f32_16x16x128_f8f6f4 v[156:159], v[0:7], v[190:197], v[156:159]
	v_mfma_f32_16x16x128_f8f6f4 v[152:155], v[8:15], v[190:197], v[152:155]
	v_mfma_f32_16x16x128_f8f6f4 v[140:143], v[0:7], v[198:205], v[140:143]
	v_mfma_f32_16x16x128_f8f6f4 v[136:139], v[8:15], v[198:205], v[136:139]
	v_mfma_f32_16x16x128_f8f6f4 v[124:127], v[0:7], v[206:213], v[124:127]
	v_mfma_f32_16x16x128_f8f6f4 v[120:123], v[8:15], v[206:213], v[120:123]
	v_mfma_f32_16x16x128_f8f6f4 v[108:111], v[0:7], v[214:221], v[108:111]
	v_mfma_f32_16x16x128_f8f6f4 v[104:107], v[8:15], v[214:221], v[104:107]
	v_mfma_f32_16x16x128_f8f6f4 v[148:151], v[16:23], v[190:197], v[148:151]
	v_mfma_f32_16x16x128_f8f6f4 v[144:147], v[24:31], v[190:197], v[144:147]
	v_mfma_f32_16x16x128_f8f6f4 v[132:135], v[16:23], v[198:205], v[132:135]
	v_mfma_f32_16x16x128_f8f6f4 v[128:131], v[24:31], v[198:205], v[128:131]
	v_mfma_f32_16x16x128_f8f6f4 v[116:119], v[16:23], v[206:213], v[116:119]
	v_mfma_f32_16x16x128_f8f6f4 v[112:115], v[24:31], v[206:213], v[112:115]
	v_mfma_f32_16x16x128_f8f6f4 v[100:103], v[16:23], v[214:221], v[100:103]
	v_mfma_f32_16x16x128_f8f6f4 v[96:99], v[24:31], v[214:221], v[96:99]
	s_barrier
	s_mov_b32 m0, s78
	v_lshl_add_u64 v[222:223], v[168:169], 0, s[56:57]
	ds_read_b128 v[190:193], v224 offset:49152
	ds_read_b128 v[194:197], v224 offset:50176
	ds_read_b128 v[198:201], v224 offset:51200
	ds_read_b128 v[202:205], v224 offset:52224
	ds_read_b128 v[206:209], v224 offset:53248
	ds_read_b128 v[210:213], v224 offset:54272
	ds_read_b128 v[214:217], v224 offset:55296
	ds_read_b128 v[218:221], v224 offset:56320
	global_load_lds_dwordx4 v[222:223], off
	v_lshl_add_u64 v[222:223], v[168:169], 0, s[28:29]
	s_mov_b32 m0, s79
	s_nop 0
	global_load_lds_dwordx4 v[222:223], off
	v_lshl_add_u64 v[222:223], v[168:169], 0, s[0:1]
	s_mov_b32 m0, s83
	v_lshl_add_u64 v[168:169], v[168:169], 0, s[4:5]
	global_load_lds_dwordx4 v[222:223], off
	s_mov_b32 m0, s86
	s_nop 0
	global_load_lds_dwordx4 v[168:169], off
	v_lshl_add_u64 v[168:169], v[170:171], 0, s[56:57]
	s_mov_b32 m0, s80
	s_nop 0
	global_load_lds_dwordx4 v[168:169], off
	v_lshl_add_u64 v[168:169], v[170:171], 0, s[28:29]
	s_mov_b32 m0, s81
	s_nop 0
	global_load_lds_dwordx4 v[168:169], off
	s_waitcnt vmcnt(8)
	s_waitcnt lgkmcnt(0)
	s_barrier
	s_waitcnt lgkmcnt(0)
	v_mfma_f32_16x16x128_f8f6f4 v[92:95], v[0:7], v[190:197], v[92:95]
	v_mfma_f32_16x16x128_f8f6f4 v[88:91], v[8:15], v[190:197], v[88:91]
	v_mfma_f32_16x16x128_f8f6f4 v[76:79], v[0:7], v[198:205], v[76:79]
	v_mfma_f32_16x16x128_f8f6f4 v[72:75], v[8:15], v[198:205], v[72:75]
	v_mfma_f32_16x16x128_f8f6f4 v[60:63], v[0:7], v[206:213], v[60:63]
	v_mfma_f32_16x16x128_f8f6f4 v[56:59], v[8:15], v[206:213], v[56:59]
	v_mfma_f32_16x16x128_f8f6f4 v[44:47], v[0:7], v[214:221], v[44:47]
	v_mfma_f32_16x16x128_f8f6f4 v[40:43], v[8:15], v[214:221], v[40:43]
	v_mfma_f32_16x16x128_f8f6f4 v[84:87], v[16:23], v[190:197], v[84:87]
	v_mfma_f32_16x16x128_f8f6f4 v[80:83], v[24:31], v[190:197], v[80:83]
	v_mfma_f32_16x16x128_f8f6f4 v[68:71], v[16:23], v[198:205], v[68:71]
	v_mfma_f32_16x16x128_f8f6f4 v[64:67], v[24:31], v[198:205], v[64:67]
	v_mfma_f32_16x16x128_f8f6f4 v[52:55], v[16:23], v[206:213], v[52:55]
	v_mfma_f32_16x16x128_f8f6f4 v[48:51], v[24:31], v[206:213], v[48:51]
	v_mfma_f32_16x16x128_f8f6f4 v[36:39], v[16:23], v[214:221], v[36:39]
	v_mfma_f32_16x16x128_f8f6f4 v[32:35], v[24:31], v[214:221], v[32:35]
	s_barrier
	s_add_u32 s18, s18, 0x100
	s_addc_u32 s19, s19, 0
	s_add_u32 s95, s95, 0x100
	s_addc_u32 vcc_lo, vcc_lo, 0
	s_cmp_ge_i32 vcc_hi, s87
	s_mov_b32 s2, vcc_hi
	s_cbranch_scc0 .LBB0_778

.LBB0_865:
	s_add_i32 s45, s2, 2
	s_add_u32 s46, s22, 0xfff30080
	s_addc_u32 s3, s23, -1
	s_cmp_eq_u32 s80, s2
	s_cselect_b32 s3, s19, s3
	s_cselect_b32 s2, s18, s46
	s_cselect_b32 s47, s39, s44
	s_cselect_b32 s46, s42, s43
	s_add_i32 s55, 0, 0x10000
	s_add_i32 s90, 0, 0x14000
	v_add_u32_e32 v148, s55, v175
	v_add_u32_e32 v160, s90, v175
	ds_read_b128 v[136:139], v148
	ds_read_b128 v[140:143], v148 offset:1024
	ds_read_b128 v[144:147], v148 offset:2048
	ds_read_b128 v[148:151], v148 offset:3072
	ds_read_b128 v[152:155], v160
	ds_read_b128 v[156:159], v160 offset:1024
	ds_read_b128 v[162:165], v160 offset:2048
	ds_read_b128 v[166:169], v160 offset:3072
	v_lshl_add_u64 v[206:207], s[22:23], 0, v[134:135]
	s_add_i32 m0, s59, 0xc000
	ds_read_b128 v[170:173], v177
	ds_read_b128 v[178:181], v177 offset:1024
	ds_read_b128 v[182:185], v177 offset:2048
	ds_read_b128 v[186:189], v177 offset:3072
	ds_read_b128 v[190:193], v177 offset:4096
	ds_read_b128 v[194:197], v177 offset:5120
	ds_read_b128 v[198:201], v177 offset:6144
	ds_read_b128 v[202:205], v177 offset:7168
	global_load_lds_dwordx4 v[206:207], off
	v_lshl_add_u64 v[206:207], v[206:207], 0, s[12:13]
	s_add_i32 m0, s59, 0xe000
	s_nop 0
	global_load_lds_dwordx4 v[206:207], off
	s_waitcnt vmcnt(8)
	s_waitcnt lgkmcnt(0)
	s_barrier
	s_waitcnt lgkmcnt(0)
	v_mfma_f32_16x16x32_bf16 v[108:111], v[136:139], v[170:173], v[108:111]
	v_mfma_f32_16x16x32_bf16 v[104:107], v[144:147], v[170:173], v[104:107]
	v_mfma_f32_16x16x32_bf16 v[100:103], v[136:139], v[182:185], v[100:103]
	v_mfma_f32_16x16x32_bf16 v[96:99], v[144:147], v[182:185], v[96:99]
	v_mfma_f32_16x16x32_bf16 v[92:95], v[136:139], v[190:193], v[92:95]
	v_mfma_f32_16x16x32_bf16 v[88:91], v[144:147], v[190:193], v[88:91]
	v_mfma_f32_16x16x32_bf16 v[84:87], v[136:139], v[198:201], v[84:87]
	v_mfma_f32_16x16x32_bf16 v[80:83], v[144:147], v[198:201], v[80:83]
	v_mfma_f32_16x16x32_bf16 v[108:111], v[140:143], v[178:181], v[108:111]
	v_mfma_f32_16x16x32_bf16 v[104:107], v[148:151], v[178:181], v[104:107]
	v_mfma_f32_16x16x32_bf16 v[100:103], v[140:143], v[186:189], v[100:103]
	v_mfma_f32_16x16x32_bf16 v[96:99], v[148:151], v[186:189], v[96:99]
	v_mfma_f32_16x16x32_bf16 v[92:95], v[140:143], v[194:197], v[92:95]
	v_mfma_f32_16x16x32_bf16 v[88:91], v[148:151], v[194:197], v[88:91]
	v_mfma_f32_16x16x32_bf16 v[84:87], v[140:143], v[202:205], v[84:87]
	v_mfma_f32_16x16x32_bf16 v[80:83], v[148:151], v[202:205], v[80:83]
	v_mfma_f32_16x16x32_bf16 v[76:79], v[152:155], v[170:173], v[76:79]
	v_mfma_f32_16x16x32_bf16 v[72:75], v[162:165], v[170:173], v[72:75]
	v_mfma_f32_16x16x32_bf16 v[68:71], v[152:155], v[182:185], v[68:71]
	v_mfma_f32_16x16x32_bf16 v[64:67], v[162:165], v[182:185], v[64:67]
	v_mfma_f32_16x16x32_bf16 v[60:63], v[152:155], v[190:193], v[60:63]
	v_mfma_f32_16x16x32_bf16 v[56:59], v[162:165], v[190:193], v[56:59]
	v_mfma_f32_16x16x32_bf16 v[52:55], v[152:155], v[198:201], v[52:55]
	v_mfma_f32_16x16x32_bf16 v[48:51], v[162:165], v[198:201], v[48:51]
	v_mfma_f32_16x16x32_bf16 v[76:79], v[156:159], v[178:181], v[76:79]
	v_mfma_f32_16x16x32_bf16 v[72:75], v[166:169], v[178:181], v[72:75]
	v_mfma_f32_16x16x32_bf16 v[68:71], v[156:159], v[186:189], v[68:71]
	v_mfma_f32_16x16x32_bf16 v[64:67], v[166:169], v[186:189], v[64:67]
	v_mfma_f32_16x16x32_bf16 v[60:63], v[156:159], v[194:197], v[60:63]
	v_mfma_f32_16x16x32_bf16 v[56:59], v[166:169], v[194:197], v[56:59]
	v_mfma_f32_16x16x32_bf16 v[52:55], v[156:159], v[202:205], v[52:55]
	v_mfma_f32_16x16x32_bf16 v[48:51], v[166:169], v[202:205], v[48:51]
	s_barrier
	v_lshl_add_u64 v[206:207], s[46:47], 0, v[128:129]
	s_add_i32 s46, s55, s58
	s_mov_b32 m0, s46
	ds_read_b128 v[170:173], v177 offset:16384
	ds_read_b128 v[178:181], v177 offset:17408
	ds_read_b128 v[182:185], v177 offset:18432
	ds_read_b128 v[186:189], v177 offset:19456
	ds_read_b128 v[190:193], v177 offset:20480
	ds_read_b128 v[194:197], v177 offset:21504
	ds_read_b128 v[198:201], v177 offset:22528
	ds_read_b128 v[202:205], v177 offset:23552
	global_load_lds_dwordx4 v[206:207], off
	v_lshl_add_u64 v[208:209], v[206:207], 0, s[8:9]
	s_add_i32 m0, s46, 0x2000
	s_add_i32 s46, s90, s58
	global_load_lds_dwordx4 v[208:209], off
	v_lshl_add_u64 v[208:209], v[206:207], 0, s[14:15]
	s_mov_b32 m0, s46
	s_nop 0
	global_load_lds_dwordx4 v[208:209], off
	v_lshl_add_u64 v[208:209], v[206:207], 0, s[16:17]
	s_add_i32 m0, s46, 0x2000
	s_nop 0
	global_load_lds_dwordx4 v[208:209], off
	v_lshl_add_u64 v[208:209], s[2:3], 0, v[130:131]
	s_mov_b32 m0, s59
	v_lshl_add_u64 v[210:211], v[208:209], 0, s[12:13]
	global_load_lds_dwordx4 v[208:209], off
	s_mov_b32 m0, s63
	s_nop 0
	global_load_lds_dwordx4 v[210:211], off
	s_waitcnt vmcnt(8)
	s_waitcnt lgkmcnt(0)
	s_barrier
	s_waitcnt lgkmcnt(0)
	v_mfma_f32_16x16x32_bf16 v[44:47], v[136:139], v[170:173], v[44:47]
	v_mfma_f32_16x16x32_bf16 v[40:43], v[144:147], v[170:173], v[40:43]
	v_mfma_f32_16x16x32_bf16 v[36:39], v[136:139], v[182:185], v[36:39]
	v_mfma_f32_16x16x32_bf16 v[32:35], v[144:147], v[182:185], v[32:35]
	v_mfma_f32_16x16x32_bf16 v[28:31], v[136:139], v[190:193], v[28:31]
	v_mfma_f32_16x16x32_bf16 v[24:27], v[144:147], v[190:193], v[24:27]
	v_mfma_f32_16x16x32_bf16 v[20:23], v[136:139], v[198:201], v[20:23]
	v_mfma_f32_16x16x32_bf16 v[16:19], v[144:147], v[198:201], v[16:19]
	v_mfma_f32_16x16x32_bf16 v[44:47], v[140:143], v[178:181], v[44:47]
	v_mfma_f32_16x16x32_bf16 v[40:43], v[148:151], v[178:181], v[40:43]
	v_mfma_f32_16x16x32_bf16 v[36:39], v[140:143], v[186:189], v[36:39]
	v_mfma_f32_16x16x32_bf16 v[32:35], v[148:151], v[186:189], v[32:35]
	v_mfma_f32_16x16x32_bf16 v[28:31], v[140:143], v[194:197], v[28:31]
	v_mfma_f32_16x16x32_bf16 v[24:27], v[148:151], v[194:197], v[24:27]
	v_mfma_f32_16x16x32_bf16 v[20:23], v[140:143], v[202:205], v[20:23]
	v_mfma_f32_16x16x32_bf16 v[16:19], v[148:151], v[202:205], v[16:19]
	v_mfma_f32_16x16x32_bf16 v[12:15], v[152:155], v[170:173], v[12:15]
	v_mfma_f32_16x16x32_bf16 v[8:11], v[162:165], v[170:173], v[8:11]
	v_mfma_f32_16x16x32_bf16 v[4:7], v[152:155], v[182:185], v[4:7]
	v_mfma_f32_16x16x32_bf16 v[0:3], v[162:165], v[182:185], v[0:3]
	v_mfma_f32_16x16x32_bf16 v[112:115], v[152:155], v[190:193], v[112:115]
	v_mfma_f32_16x16x32_bf16 v[116:119], v[162:165], v[190:193], v[116:119]
	v_mfma_f32_16x16x32_bf16 v[120:123], v[152:155], v[198:201], v[120:123]
	v_mfma_f32_16x16x32_bf16 v[124:127], v[162:165], v[198:201], v[124:127]
	v_mfma_f32_16x16x32_bf16 v[12:15], v[156:159], v[178:181], v[12:15]
	v_mfma_f32_16x16x32_bf16 v[8:11], v[166:169], v[178:181], v[8:11]
	v_mfma_f32_16x16x32_bf16 v[4:7], v[156:159], v[186:189], v[4:7]
	v_mfma_f32_16x16x32_bf16 v[0:3], v[166:169], v[186:189], v[0:3]
	v_mfma_f32_16x16x32_bf16 v[112:115], v[156:159], v[194:197], v[112:115]
	v_mfma_f32_16x16x32_bf16 v[116:119], v[166:169], v[194:197], v[116:119]
	v_mfma_f32_16x16x32_bf16 v[120:123], v[156:159], v[202:205], v[120:123]
	v_mfma_f32_16x16x32_bf16 v[124:127], v[166:169], v[202:205], v[124:127]
	s_barrier
	s_add_i32 s2, 0, 0x18000
	s_add_i32 s3, 0, 0x1c000
	v_add_u32_e32 v148, s2, v175
	v_add_u32_e32 v160, s3, v175
	ds_read_b128 v[136:139], v148
	ds_read_b128 v[140:143], v148 offset:1024
	ds_read_b128 v[144:147], v148 offset:2048
	ds_read_b128 v[148:151], v148 offset:3072
	ds_read_b128 v[152:155], v160
	ds_read_b128 v[156:159], v160 offset:1024
	ds_read_b128 v[162:165], v160 offset:2048
	ds_read_b128 v[166:169], v160 offset:3072
	s_mov_b32 m0, s77
	v_lshl_add_u64 v[210:211], v[208:209], 0, s[4:5]
	ds_read_b128 v[170:173], v177 offset:32768
	ds_read_b128 v[178:181], v177 offset:33792
	ds_read_b128 v[182:185], v177 offset:34816
	ds_read_b128 v[186:189], v177 offset:35840
	ds_read_b128 v[190:193], v177 offset:36864
	ds_read_b128 v[194:197], v177 offset:37888
	ds_read_b128 v[198:201], v177 offset:38912
	ds_read_b128 v[202:205], v177 offset:39936
	global_load_lds_dwordx4 v[210:211], off
	v_lshl_add_u64 v[210:211], v[208:209], 0, s[72:73]
	s_mov_b32 m0, s78
	s_nop 0
	global_load_lds_dwordx4 v[210:211], off
	s_waitcnt vmcnt(8)
	s_waitcnt lgkmcnt(0)
	s_barrier
	s_waitcnt lgkmcnt(0)
	v_mfma_f32_16x16x32_bf16 v[108:111], v[136:139], v[170:173], v[108:111]
	v_mfma_f32_16x16x32_bf16 v[104:107], v[144:147], v[170:173], v[104:107]
	v_mfma_f32_16x16x32_bf16 v[100:103], v[136:139], v[182:185], v[100:103]
	v_mfma_f32_16x16x32_bf16 v[96:99], v[144:147], v[182:185], v[96:99]
	v_mfma_f32_16x16x32_bf16 v[92:95], v[136:139], v[190:193], v[92:95]
	v_mfma_f32_16x16x32_bf16 v[88:91], v[144:147], v[190:193], v[88:91]
	v_mfma_f32_16x16x32_bf16 v[84:87], v[136:139], v[198:201], v[84:87]
	v_mfma_f32_16x16x32_bf16 v[80:83], v[144:147], v[198:201], v[80:83]
	v_mfma_f32_16x16x32_bf16 v[108:111], v[140:143], v[178:181], v[108:111]
	v_mfma_f32_16x16x32_bf16 v[104:107], v[148:151], v[178:181], v[104:107]
	v_mfma_f32_16x16x32_bf16 v[100:103], v[140:143], v[186:189], v[100:103]
	v_mfma_f32_16x16x32_bf16 v[96:99], v[148:151], v[186:189], v[96:99]
	v_mfma_f32_16x16x32_bf16 v[92:95], v[140:143], v[194:197], v[92:95]
	v_mfma_f32_16x16x32_bf16 v[88:91], v[148:151], v[194:197], v[88:91]
	v_mfma_f32_16x16x32_bf16 v[84:87], v[140:143], v[202:205], v[84:87]
	v_mfma_f32_16x16x32_bf16 v[80:83], v[148:151], v[202:205], v[80:83]
	v_mfma_f32_16x16x32_bf16 v[76:79], v[152:155], v[170:173], v[76:79]
	v_mfma_f32_16x16x32_bf16 v[72:75], v[162:165], v[170:173], v[72:75]
	v_mfma_f32_16x16x32_bf16 v[68:71], v[152:155], v[182:185], v[68:71]
	v_mfma_f32_16x16x32_bf16 v[64:67], v[162:165], v[182:185], v[64:67]
	v_mfma_f32_16x16x32_bf16 v[60:63], v[152:155], v[190:193], v[60:63]
	v_mfma_f32_16x16x32_bf16 v[56:59], v[162:165], v[190:193], v[56:59]
	v_mfma_f32_16x16x32_bf16 v[52:55], v[152:155], v[198:201], v[52:55]
	v_mfma_f32_16x16x32_bf16 v[48:51], v[162:165], v[198:201], v[48:51]
	v_mfma_f32_16x16x32_bf16 v[76:79], v[156:159], v[178:181], v[76:79]
	v_mfma_f32_16x16x32_bf16 v[72:75], v[166:169], v[178:181], v[72:75]
	v_mfma_f32_16x16x32_bf16 v[68:71], v[156:159], v[186:189], v[68:71]
	v_mfma_f32_16x16x32_bf16 v[64:67], v[166:169], v[186:189], v[64:67]
	v_mfma_f32_16x16x32_bf16 v[60:63], v[156:159], v[194:197], v[60:63]
	v_mfma_f32_16x16x32_bf16 v[56:59], v[166:169], v[194:197], v[56:59]
	v_mfma_f32_16x16x32_bf16 v[52:55], v[156:159], v[202:205], v[52:55]
	v_mfma_f32_16x16x32_bf16 v[48:51], v[166:169], v[202:205], v[48:51]
	s_barrier
	s_add_i32 s2, s2, s58
	v_lshl_add_u64 v[210:211], v[206:207], 0, s[56:57]
	s_mov_b32 m0, s2
	ds_read_b128 v[170:173], v177 offset:49152
	ds_read_b128 v[178:181], v177 offset:50176
	ds_read_b128 v[182:185], v177 offset:51200
	ds_read_b128 v[186:189], v177 offset:52224
	ds_read_b128 v[190:193], v177 offset:53248
	ds_read_b128 v[194:197], v177 offset:54272
	ds_read_b128 v[198:201], v177 offset:55296
	ds_read_b128 v[202:205], v177 offset:56320
	global_load_lds_dwordx4 v[210:211], off
	v_lshl_add_u64 v[210:211], v[206:207], 0, s[28:29]
	s_add_i32 m0, s2, 0x2000
	s_add_i32 s2, s3, s58
	global_load_lds_dwordx4 v[210:211], off
	v_lshl_add_u64 v[210:211], v[206:207], 0, s[0:1]
	s_mov_b32 m0, s2
	v_lshl_add_u64 v[206:207], v[206:207], 0, s[64:65]
	global_load_lds_dwordx4 v[210:211], off
	s_add_i32 m0, s2, 0x2000
	s_nop 0
	global_load_lds_dwordx4 v[206:207], off
	v_lshl_add_u64 v[206:207], v[208:209], 0, s[56:57]
	s_mov_b32 m0, s79
	s_nop 0
	global_load_lds_dwordx4 v[206:207], off
	v_lshl_add_u64 v[206:207], v[208:209], 0, s[88:89]
	s_mov_b32 m0, s10
	s_nop 0
	global_load_lds_dwordx4 v[206:207], off
	s_waitcnt vmcnt(8)
	s_waitcnt lgkmcnt(0)
	s_barrier
	s_waitcnt lgkmcnt(0)
	v_mfma_f32_16x16x32_bf16 v[44:47], v[136:139], v[170:173], v[44:47]
	v_mfma_f32_16x16x32_bf16 v[40:43], v[144:147], v[170:173], v[40:43]
	v_mfma_f32_16x16x32_bf16 v[36:39], v[136:139], v[182:185], v[36:39]
	v_mfma_f32_16x16x32_bf16 v[32:35], v[144:147], v[182:185], v[32:35]
	v_mfma_f32_16x16x32_bf16 v[28:31], v[136:139], v[190:193], v[28:31]
	v_mfma_f32_16x16x32_bf16 v[24:27], v[144:147], v[190:193], v[24:27]
	v_mfma_f32_16x16x32_bf16 v[20:23], v[136:139], v[198:201], v[20:23]
	v_mfma_f32_16x16x32_bf16 v[16:19], v[144:147], v[198:201], v[16:19]
	v_mfma_f32_16x16x32_bf16 v[44:47], v[140:143], v[178:181], v[44:47]
	v_mfma_f32_16x16x32_bf16 v[40:43], v[148:151], v[178:181], v[40:43]
	v_mfma_f32_16x16x32_bf16 v[36:39], v[140:143], v[186:189], v[36:39]
	v_mfma_f32_16x16x32_bf16 v[32:35], v[148:151], v[186:189], v[32:35]
	v_mfma_f32_16x16x32_bf16 v[28:31], v[140:143], v[194:197], v[28:31]
	v_mfma_f32_16x16x32_bf16 v[24:27], v[148:151], v[194:197], v[24:27]
	v_mfma_f32_16x16x32_bf16 v[20:23], v[140:143], v[202:205], v[20:23]
	v_mfma_f32_16x16x32_bf16 v[16:19], v[148:151], v[202:205], v[16:19]
	v_mfma_f32_16x16x32_bf16 v[12:15], v[152:155], v[170:173], v[12:15]
	v_mfma_f32_16x16x32_bf16 v[8:11], v[162:165], v[170:173], v[8:11]
	v_mfma_f32_16x16x32_bf16 v[4:7], v[152:155], v[182:185], v[4:7]
	v_mfma_f32_16x16x32_bf16 v[0:3], v[162:165], v[182:185], v[0:3]
	v_mfma_f32_16x16x32_bf16 v[112:115], v[152:155], v[190:193], v[112:115]
	v_mfma_f32_16x16x32_bf16 v[116:119], v[162:165], v[190:193], v[116:119]
	v_mfma_f32_16x16x32_bf16 v[120:123], v[152:155], v[198:201], v[120:123]
	v_mfma_f32_16x16x32_bf16 v[124:127], v[162:165], v[198:201], v[124:127]
	v_mfma_f32_16x16x32_bf16 v[12:15], v[156:159], v[178:181], v[12:15]
	v_mfma_f32_16x16x32_bf16 v[8:11], v[166:169], v[178:181], v[8:11]
	v_mfma_f32_16x16x32_bf16 v[4:7], v[156:159], v[186:189], v[4:7]
	v_mfma_f32_16x16x32_bf16 v[0:3], v[166:169], v[186:189], v[0:3]
	v_mfma_f32_16x16x32_bf16 v[112:115], v[156:159], v[194:197], v[112:115]
	v_mfma_f32_16x16x32_bf16 v[116:119], v[166:169], v[194:197], v[116:119]
	v_mfma_f32_16x16x32_bf16 v[120:123], v[156:159], v[202:205], v[120:123]
	v_mfma_f32_16x16x32_bf16 v[124:127], v[166:169], v[202:205], v[124:127]
	s_barrier
	s_add_u32 s22, s22, 0x100
	s_addc_u32 s23, s23, 0
	s_add_u32 s43, s43, 0x100
	s_addc_u32 s44, s44, 0
	s_cmp_ge_i32 s45, s11
	s_mov_b32 s2, s45
	s_cbranch_scc0 .LBB0_865

.LBB0_1071:
	s_add_i32 s86, s2, 2
	s_add_u32 s87, s74, 0xfffc0080
	s_addc_u32 s3, s75, -1
	s_cmp_eq_u32 s80, s2
	s_cselect_b32 s3, s19, s3
	s_cselect_b32 s2, s38, s87
	s_cselect_b32 s91, s39, s23
	s_cselect_b32 s90, s49, s22
	s_add_i32 s87, 0, 0x10000
	s_add_i32 s92, 0, 0x14000
	v_add_u32_e32 v142, s87, v153
	v_add_u32_e32 v150, s92, v153
	ds_read_b128 v[130:133], v142
	ds_read_b128 v[134:137], v142 offset:1024
	ds_read_b128 v[138:141], v142 offset:2048
	ds_read_b128 v[142:145], v142 offset:3072
	ds_read_b128 v[146:149], v150
	ds_read_b128 v[156:159], v150 offset:1024
	ds_read_b128 v[162:165], v150 offset:2048
	ds_read_b128 v[166:169], v150 offset:3072
	v_lshl_add_u64 v[150:151], s[74:75], 0, v[128:129]
	s_add_i32 m0, s7, 0xc000
	ds_read_b128 v[170:173], v155
	ds_read_b128 v[174:177], v155 offset:1024
	ds_read_b128 v[178:181], v155 offset:2048
	ds_read_b128 v[182:185], v155 offset:3072
	ds_read_b128 v[186:189], v155 offset:4096
	ds_read_b128 v[190:193], v155 offset:5120
	ds_read_b128 v[194:197], v155 offset:6144
	ds_read_b128 v[198:201], v155 offset:7168
	global_load_lds_dwordx4 v[150:151], off
	v_lshl_add_u64 v[150:151], v[150:151], 0, s[14:15]
	s_add_i32 m0, s7, 0xe000
	s_nop 0
	global_load_lds_dwordx4 v[150:151], off
	s_waitcnt vmcnt(8)
	s_waitcnt lgkmcnt(0)
	s_barrier
	s_waitcnt lgkmcnt(0)
	v_mfma_f32_16x16x32_bf16 v[124:127], v[130:133], v[170:173], v[124:127]
	v_mfma_f32_16x16x32_bf16 v[120:123], v[138:141], v[170:173], v[120:123]
	v_mfma_f32_16x16x32_bf16 v[108:111], v[130:133], v[178:181], v[108:111]
	v_mfma_f32_16x16x32_bf16 v[104:107], v[138:141], v[178:181], v[104:107]
	v_mfma_f32_16x16x32_bf16 v[92:95], v[130:133], v[186:189], v[92:95]
	v_mfma_f32_16x16x32_bf16 v[88:91], v[138:141], v[186:189], v[88:91]
	v_mfma_f32_16x16x32_bf16 v[76:79], v[130:133], v[194:197], v[76:79]
	v_mfma_f32_16x16x32_bf16 v[72:75], v[138:141], v[194:197], v[72:75]
	v_mfma_f32_16x16x32_bf16 v[124:127], v[134:137], v[174:177], v[124:127]
	v_mfma_f32_16x16x32_bf16 v[120:123], v[142:145], v[174:177], v[120:123]
	v_mfma_f32_16x16x32_bf16 v[108:111], v[134:137], v[182:185], v[108:111]
	v_mfma_f32_16x16x32_bf16 v[104:107], v[142:145], v[182:185], v[104:107]
	v_mfma_f32_16x16x32_bf16 v[92:95], v[134:137], v[190:193], v[92:95]
	v_mfma_f32_16x16x32_bf16 v[88:91], v[142:145], v[190:193], v[88:91]
	v_mfma_f32_16x16x32_bf16 v[76:79], v[134:137], v[198:201], v[76:79]
	v_mfma_f32_16x16x32_bf16 v[72:75], v[142:145], v[198:201], v[72:75]
	v_mfma_f32_16x16x32_bf16 v[116:119], v[146:149], v[170:173], v[116:119]
	v_mfma_f32_16x16x32_bf16 v[112:115], v[162:165], v[170:173], v[112:115]
	v_mfma_f32_16x16x32_bf16 v[100:103], v[146:149], v[178:181], v[100:103]
	v_mfma_f32_16x16x32_bf16 v[96:99], v[162:165], v[178:181], v[96:99]
	v_mfma_f32_16x16x32_bf16 v[84:87], v[146:149], v[186:189], v[84:87]
	v_mfma_f32_16x16x32_bf16 v[80:83], v[162:165], v[186:189], v[80:83]
	v_mfma_f32_16x16x32_bf16 v[68:71], v[146:149], v[194:197], v[68:71]
	v_mfma_f32_16x16x32_bf16 v[64:67], v[162:165], v[194:197], v[64:67]
	v_mfma_f32_16x16x32_bf16 v[116:119], v[156:159], v[174:177], v[116:119]
	v_mfma_f32_16x16x32_bf16 v[112:115], v[166:169], v[174:177], v[112:115]
	v_mfma_f32_16x16x32_bf16 v[100:103], v[156:159], v[182:185], v[100:103]
	v_mfma_f32_16x16x32_bf16 v[96:99], v[166:169], v[182:185], v[96:99]
	v_mfma_f32_16x16x32_bf16 v[84:87], v[156:159], v[190:193], v[84:87]
	v_mfma_f32_16x16x32_bf16 v[80:83], v[166:169], v[190:193], v[80:83]
	v_mfma_f32_16x16x32_bf16 v[68:71], v[156:159], v[198:201], v[68:71]
	v_mfma_f32_16x16x32_bf16 v[64:67], v[166:169], v[198:201], v[64:67]
	s_barrier
	s_add_i32 s87, s87, s6
	v_lshl_add_u64 v[150:151], s[90:91], 0, v[160:161]
	s_mov_b32 m0, s87
	ds_read_b128 v[170:173], v155 offset:16384
	ds_read_b128 v[174:177], v155 offset:17408
	ds_read_b128 v[178:181], v155 offset:18432
	ds_read_b128 v[182:185], v155 offset:19456
	ds_read_b128 v[186:189], v155 offset:20480
	ds_read_b128 v[190:193], v155 offset:21504
	ds_read_b128 v[194:197], v155 offset:22528
	ds_read_b128 v[198:201], v155 offset:23552
	global_load_lds_dwordx4 v[150:151], off
	v_lshl_add_u64 v[202:203], v[150:151], 0, s[14:15]
	s_add_i32 m0, s87, 0x2000
	s_add_i32 s87, s92, s6
	global_load_lds_dwordx4 v[202:203], off
	v_lshl_add_u64 v[202:203], v[150:151], 0, s[60:61]
	s_mov_b32 m0, s87
	s_nop 0
	global_load_lds_dwordx4 v[202:203], off
	v_lshl_add_u64 v[202:203], v[150:151], 0, s[52:53]
	s_add_i32 m0, s87, 0x2000
	s_nop 0
	global_load_lds_dwordx4 v[202:203], off
	v_lshl_add_u64 v[202:203], s[2:3], 0, v[160:161]
	s_mov_b32 m0, s7
	v_lshl_add_u64 v[204:205], v[202:203], 0, s[14:15]
	global_load_lds_dwordx4 v[202:203], off
	s_mov_b32 m0, s10
	s_nop 0
	global_load_lds_dwordx4 v[204:205], off
	s_waitcnt vmcnt(8)
	s_waitcnt lgkmcnt(0)
	s_barrier
	s_waitcnt lgkmcnt(0)
	v_mfma_f32_16x16x32_bf16 v[60:63], v[130:133], v[170:173], v[60:63]
	v_mfma_f32_16x16x32_bf16 v[56:59], v[138:141], v[170:173], v[56:59]
	v_mfma_f32_16x16x32_bf16 v[44:47], v[130:133], v[178:181], v[44:47]
	v_mfma_f32_16x16x32_bf16 v[40:43], v[138:141], v[178:181], v[40:43]
	v_mfma_f32_16x16x32_bf16 v[28:31], v[130:133], v[186:189], v[28:31]
	v_mfma_f32_16x16x32_bf16 v[24:27], v[138:141], v[186:189], v[24:27]
	v_mfma_f32_16x16x32_bf16 v[12:15], v[130:133], v[194:197], v[12:15]
	v_mfma_f32_16x16x32_bf16 v[8:11], v[138:141], v[194:197], v[8:11]
	v_mfma_f32_16x16x32_bf16 v[60:63], v[134:137], v[174:177], v[60:63]
	v_mfma_f32_16x16x32_bf16 v[56:59], v[142:145], v[174:177], v[56:59]
	v_mfma_f32_16x16x32_bf16 v[44:47], v[134:137], v[182:185], v[44:47]
	v_mfma_f32_16x16x32_bf16 v[40:43], v[142:145], v[182:185], v[40:43]
	v_mfma_f32_16x16x32_bf16 v[28:31], v[134:137], v[190:193], v[28:31]
	v_mfma_f32_16x16x32_bf16 v[24:27], v[142:145], v[190:193], v[24:27]
	v_mfma_f32_16x16x32_bf16 v[12:15], v[134:137], v[198:201], v[12:15]
	v_mfma_f32_16x16x32_bf16 v[8:11], v[142:145], v[198:201], v[8:11]
	v_mfma_f32_16x16x32_bf16 v[52:55], v[146:149], v[170:173], v[52:55]
	v_mfma_f32_16x16x32_bf16 v[48:51], v[162:165], v[170:173], v[48:51]
	v_mfma_f32_16x16x32_bf16 v[36:39], v[146:149], v[178:181], v[36:39]
	v_mfma_f32_16x16x32_bf16 v[32:35], v[162:165], v[178:181], v[32:35]
	v_mfma_f32_16x16x32_bf16 v[20:23], v[146:149], v[186:189], v[20:23]
	v_mfma_f32_16x16x32_bf16 v[16:19], v[162:165], v[186:189], v[16:19]
	v_mfma_f32_16x16x32_bf16 v[4:7], v[146:149], v[194:197], v[4:7]
	v_mfma_f32_16x16x32_bf16 v[0:3], v[162:165], v[194:197], v[0:3]
	v_mfma_f32_16x16x32_bf16 v[52:55], v[156:159], v[174:177], v[52:55]
	v_mfma_f32_16x16x32_bf16 v[48:51], v[166:169], v[174:177], v[48:51]
	v_mfma_f32_16x16x32_bf16 v[36:39], v[156:159], v[182:185], v[36:39]
	v_mfma_f32_16x16x32_bf16 v[32:35], v[166:169], v[182:185], v[32:35]
	v_mfma_f32_16x16x32_bf16 v[20:23], v[156:159], v[190:193], v[20:23]
	v_mfma_f32_16x16x32_bf16 v[16:19], v[166:169], v[190:193], v[16:19]
	v_mfma_f32_16x16x32_bf16 v[4:7], v[156:159], v[198:201], v[4:7]
	v_mfma_f32_16x16x32_bf16 v[0:3], v[166:169], v[198:201], v[0:3]
	s_barrier
	s_add_i32 s2, 0, 0x18000
	s_add_i32 s3, 0, 0x1c000
	v_add_u32_e32 v142, s2, v153
	v_add_u32_e32 v166, s3, v153
	ds_read_b128 v[130:133], v142
	ds_read_b128 v[134:137], v142 offset:1024
	ds_read_b128 v[138:141], v142 offset:2048
	ds_read_b128 v[142:145], v142 offset:3072
	ds_read_b128 v[146:149], v166
	ds_read_b128 v[156:159], v166 offset:1024
	ds_read_b128 v[162:165], v166 offset:2048
	ds_read_b128 v[166:169], v166 offset:3072
	s_mov_b32 m0, s11
	v_lshl_add_u64 v[204:205], v[202:203], 0, s[60:61]
	ds_read_b128 v[170:173], v155 offset:32768
	ds_read_b128 v[174:177], v155 offset:33792
	ds_read_b128 v[178:181], v155 offset:34816
	ds_read_b128 v[182:185], v155 offset:35840
	ds_read_b128 v[186:189], v155 offset:36864
	ds_read_b128 v[190:193], v155 offset:37888
	ds_read_b128 v[194:197], v155 offset:38912
	ds_read_b128 v[198:201], v155 offset:39936
	global_load_lds_dwordx4 v[204:205], off
	v_lshl_add_u64 v[204:205], v[202:203], 0, s[52:53]
	s_mov_b32 m0, s63
	s_nop 0
	global_load_lds_dwordx4 v[204:205], off
	s_waitcnt vmcnt(8)
	s_waitcnt lgkmcnt(0)
	s_barrier
	s_waitcnt lgkmcnt(0)
	v_mfma_f32_16x16x32_bf16 v[124:127], v[130:133], v[170:173], v[124:127]
	v_mfma_f32_16x16x32_bf16 v[120:123], v[138:141], v[170:173], v[120:123]
	v_mfma_f32_16x16x32_bf16 v[108:111], v[130:133], v[178:181], v[108:111]
	v_mfma_f32_16x16x32_bf16 v[104:107], v[138:141], v[178:181], v[104:107]
	v_mfma_f32_16x16x32_bf16 v[92:95], v[130:133], v[186:189], v[92:95]
	v_mfma_f32_16x16x32_bf16 v[88:91], v[138:141], v[186:189], v[88:91]
	v_mfma_f32_16x16x32_bf16 v[76:79], v[130:133], v[194:197], v[76:79]
	v_mfma_f32_16x16x32_bf16 v[72:75], v[138:141], v[194:197], v[72:75]
	v_mfma_f32_16x16x32_bf16 v[124:127], v[134:137], v[174:177], v[124:127]
	v_mfma_f32_16x16x32_bf16 v[120:123], v[142:145], v[174:177], v[120:123]
	v_mfma_f32_16x16x32_bf16 v[108:111], v[134:137], v[182:185], v[108:111]
	v_mfma_f32_16x16x32_bf16 v[104:107], v[142:145], v[182:185], v[104:107]
	v_mfma_f32_16x16x32_bf16 v[92:95], v[134:137], v[190:193], v[92:95]
	v_mfma_f32_16x16x32_bf16 v[88:91], v[142:145], v[190:193], v[88:91]
	v_mfma_f32_16x16x32_bf16 v[76:79], v[134:137], v[198:201], v[76:79]
	v_mfma_f32_16x16x32_bf16 v[72:75], v[142:145], v[198:201], v[72:75]
	v_mfma_f32_16x16x32_bf16 v[116:119], v[146:149], v[170:173], v[116:119]
	v_mfma_f32_16x16x32_bf16 v[112:115], v[162:165], v[170:173], v[112:115]
	v_mfma_f32_16x16x32_bf16 v[100:103], v[146:149], v[178:181], v[100:103]
	v_mfma_f32_16x16x32_bf16 v[96:99], v[162:165], v[178:181], v[96:99]
	v_mfma_f32_16x16x32_bf16 v[84:87], v[146:149], v[186:189], v[84:87]
	v_mfma_f32_16x16x32_bf16 v[80:83], v[162:165], v[186:189], v[80:83]
	v_mfma_f32_16x16x32_bf16 v[68:71], v[146:149], v[194:197], v[68:71]
	v_mfma_f32_16x16x32_bf16 v[64:67], v[162:165], v[194:197], v[64:67]
	v_mfma_f32_16x16x32_bf16 v[116:119], v[156:159], v[174:177], v[116:119]
	v_mfma_f32_16x16x32_bf16 v[112:115], v[166:169], v[174:177], v[112:115]
	v_mfma_f32_16x16x32_bf16 v[100:103], v[156:159], v[182:185], v[100:103]
	v_mfma_f32_16x16x32_bf16 v[96:99], v[166:169], v[182:185], v[96:99]
	v_mfma_f32_16x16x32_bf16 v[84:87], v[156:159], v[190:193], v[84:87]
	v_mfma_f32_16x16x32_bf16 v[80:83], v[166:169], v[190:193], v[80:83]
	v_mfma_f32_16x16x32_bf16 v[68:71], v[156:159], v[198:201], v[68:71]
	v_mfma_f32_16x16x32_bf16 v[64:67], v[166:169], v[198:201], v[64:67]
	s_barrier
	s_add_i32 s2, s2, s6
	v_lshl_add_u64 v[204:205], v[150:151], 0, s[56:57]
	s_mov_b32 m0, s2
	ds_read_b128 v[170:173], v155 offset:49152
	ds_read_b128 v[174:177], v155 offset:50176
	ds_read_b128 v[178:181], v155 offset:51200
	ds_read_b128 v[182:185], v155 offset:52224
	ds_read_b128 v[186:189], v155 offset:53248
	ds_read_b128 v[190:193], v155 offset:54272
	ds_read_b128 v[194:197], v155 offset:55296
	ds_read_b128 v[198:201], v155 offset:56320
	global_load_lds_dwordx4 v[204:205], off
	v_lshl_add_u64 v[204:205], v[150:151], 0, s[0:1]
	s_add_i32 m0, s2, 0x2000
	s_add_i32 s2, s3, s6
	global_load_lds_dwordx4 v[204:205], off
	v_lshl_add_u64 v[204:205], v[150:151], 0, s[24:25]
	s_mov_b32 m0, s2
	v_lshl_add_u64 v[150:151], v[150:151], 0, s[26:27]
	global_load_lds_dwordx4 v[204:205], off
	s_add_i32 m0, s2, 0x2000
	s_nop 0
	global_load_lds_dwordx4 v[150:151], off
	v_lshl_add_u64 v[150:151], v[202:203], 0, s[56:57]
	s_mov_b32 m0, s77
	s_nop 0
	global_load_lds_dwordx4 v[150:151], off
	v_lshl_add_u64 v[150:151], v[202:203], 0, s[0:1]
	s_mov_b32 m0, s78
	s_nop 0
	global_load_lds_dwordx4 v[150:151], off
	s_waitcnt vmcnt(8)
	s_waitcnt lgkmcnt(0)
	s_barrier
	s_waitcnt lgkmcnt(0)
	v_mfma_f32_16x16x32_bf16 v[60:63], v[130:133], v[170:173], v[60:63]
	v_mfma_f32_16x16x32_bf16 v[56:59], v[138:141], v[170:173], v[56:59]
	v_mfma_f32_16x16x32_bf16 v[44:47], v[130:133], v[178:181], v[44:47]
	v_mfma_f32_16x16x32_bf16 v[40:43], v[138:141], v[178:181], v[40:43]
	v_mfma_f32_16x16x32_bf16 v[28:31], v[130:133], v[186:189], v[28:31]
	v_mfma_f32_16x16x32_bf16 v[24:27], v[138:141], v[186:189], v[24:27]
	v_mfma_f32_16x16x32_bf16 v[12:15], v[130:133], v[194:197], v[12:15]
	v_mfma_f32_16x16x32_bf16 v[8:11], v[138:141], v[194:197], v[8:11]
	v_mfma_f32_16x16x32_bf16 v[60:63], v[134:137], v[174:177], v[60:63]
	v_mfma_f32_16x16x32_bf16 v[56:59], v[142:145], v[174:177], v[56:59]
	v_mfma_f32_16x16x32_bf16 v[44:47], v[134:137], v[182:185], v[44:47]
	v_mfma_f32_16x16x32_bf16 v[40:43], v[142:145], v[182:185], v[40:43]
	v_mfma_f32_16x16x32_bf16 v[28:31], v[134:137], v[190:193], v[28:31]
	v_mfma_f32_16x16x32_bf16 v[24:27], v[142:145], v[190:193], v[24:27]
	v_mfma_f32_16x16x32_bf16 v[12:15], v[134:137], v[198:201], v[12:15]
	v_mfma_f32_16x16x32_bf16 v[8:11], v[142:145], v[198:201], v[8:11]
	v_mfma_f32_16x16x32_bf16 v[52:55], v[146:149], v[170:173], v[52:55]
	v_mfma_f32_16x16x32_bf16 v[48:51], v[162:165], v[170:173], v[48:51]
	v_mfma_f32_16x16x32_bf16 v[36:39], v[146:149], v[178:181], v[36:39]
	v_mfma_f32_16x16x32_bf16 v[32:35], v[162:165], v[178:181], v[32:35]
	v_mfma_f32_16x16x32_bf16 v[20:23], v[146:149], v[186:189], v[20:23]
	v_mfma_f32_16x16x32_bf16 v[16:19], v[162:165], v[186:189], v[16:19]
	v_mfma_f32_16x16x32_bf16 v[4:7], v[146:149], v[194:197], v[4:7]
	v_mfma_f32_16x16x32_bf16 v[0:3], v[162:165], v[194:197], v[0:3]
	v_mfma_f32_16x16x32_bf16 v[52:55], v[156:159], v[174:177], v[52:55]
	v_mfma_f32_16x16x32_bf16 v[48:51], v[166:169], v[174:177], v[48:51]
	v_mfma_f32_16x16x32_bf16 v[36:39], v[156:159], v[182:185], v[36:39]
	v_mfma_f32_16x16x32_bf16 v[32:35], v[166:169], v[182:185], v[32:35]
	v_mfma_f32_16x16x32_bf16 v[20:23], v[156:159], v[190:193], v[20:23]
	v_mfma_f32_16x16x32_bf16 v[16:19], v[166:169], v[190:193], v[16:19]
	v_mfma_f32_16x16x32_bf16 v[4:7], v[156:159], v[198:201], v[4:7]
	v_mfma_f32_16x16x32_bf16 v[0:3], v[166:169], v[198:201], v[0:3]
	s_barrier
	s_add_u32 s74, s74, 0x100
	s_addc_u32 s75, s75, 0
	s_add_u32 s22, s22, 0x100
	s_addc_u32 s23, s23, 0
	s_cmp_ge_i32 s86, s79
	s_mov_b32 s2, s86
	s_cbranch_scc0 .LBB0_1071

.LBB0_1094:
	s_add_i32 s86, s2, 2
	s_add_u32 s87, s74, 0xfffc0080
	s_addc_u32 s3, s75, -1
	s_cmp_eq_u32 s80, s2
	s_cselect_b32 s3, s38, s3
	s_cselect_b32 s2, s39, s87
	s_cselect_b32 s91, s47, s23
	s_cselect_b32 s90, s49, s22
	s_add_i32 s87, 0, 0x10000
	s_add_i32 s92, 0, 0x14000
	v_add_u32_e32 v146, s87, v135
	v_add_u32_e32 v158, s92, v135
	ds_read_b128 v[130:133], v146
	ds_read_b128 v[138:141], v146 offset:1024
	ds_read_b128 v[142:145], v146 offset:2048
	ds_read_b128 v[146:149], v146 offset:3072
	ds_read_b128 v[150:153], v158
	ds_read_b128 v[154:157], v158 offset:1024
	ds_read_b128 v[162:165], v158 offset:2048
	ds_read_b128 v[166:169], v158 offset:3072
	v_lshl_add_u64 v[158:159], s[74:75], 0, v[128:129]
	s_add_i32 m0, s7, 0xc000
	ds_read_b128 v[170:173], v137
	ds_read_b128 v[174:177], v137 offset:1024
	ds_read_b128 v[178:181], v137 offset:2048
	ds_read_b128 v[182:185], v137 offset:3072
	ds_read_b128 v[186:189], v137 offset:4096
	ds_read_b128 v[190:193], v137 offset:5120
	ds_read_b128 v[194:197], v137 offset:6144
	ds_read_b128 v[198:201], v137 offset:7168
	global_load_lds_dwordx4 v[158:159], off
	v_lshl_add_u64 v[158:159], v[158:159], 0, s[14:15]
	s_add_i32 m0, s7, 0xe000
	s_nop 0
	global_load_lds_dwordx4 v[158:159], off
	s_waitcnt vmcnt(8)
	s_waitcnt lgkmcnt(0)
	s_barrier
	s_waitcnt lgkmcnt(0)
	v_mfma_f32_16x16x32_bf16 v[124:127], v[130:133], v[170:173], v[124:127]
	v_mfma_f32_16x16x32_bf16 v[120:123], v[142:145], v[170:173], v[120:123]
	v_mfma_f32_16x16x32_bf16 v[108:111], v[130:133], v[178:181], v[108:111]
	v_mfma_f32_16x16x32_bf16 v[104:107], v[142:145], v[178:181], v[104:107]
	v_mfma_f32_16x16x32_bf16 v[92:95], v[130:133], v[186:189], v[92:95]
	v_mfma_f32_16x16x32_bf16 v[88:91], v[142:145], v[186:189], v[88:91]
	v_mfma_f32_16x16x32_bf16 v[76:79], v[130:133], v[194:197], v[76:79]
	v_mfma_f32_16x16x32_bf16 v[72:75], v[142:145], v[194:197], v[72:75]
	v_mfma_f32_16x16x32_bf16 v[124:127], v[138:141], v[174:177], v[124:127]
	v_mfma_f32_16x16x32_bf16 v[120:123], v[146:149], v[174:177], v[120:123]
	v_mfma_f32_16x16x32_bf16 v[108:111], v[138:141], v[182:185], v[108:111]
	v_mfma_f32_16x16x32_bf16 v[104:107], v[146:149], v[182:185], v[104:107]
	v_mfma_f32_16x16x32_bf16 v[92:95], v[138:141], v[190:193], v[92:95]
	v_mfma_f32_16x16x32_bf16 v[88:91], v[146:149], v[190:193], v[88:91]
	v_mfma_f32_16x16x32_bf16 v[76:79], v[138:141], v[198:201], v[76:79]
	v_mfma_f32_16x16x32_bf16 v[72:75], v[146:149], v[198:201], v[72:75]
	v_mfma_f32_16x16x32_bf16 v[116:119], v[150:153], v[170:173], v[116:119]
	v_mfma_f32_16x16x32_bf16 v[112:115], v[162:165], v[170:173], v[112:115]
	v_mfma_f32_16x16x32_bf16 v[100:103], v[150:153], v[178:181], v[100:103]
	v_mfma_f32_16x16x32_bf16 v[96:99], v[162:165], v[178:181], v[96:99]
	v_mfma_f32_16x16x32_bf16 v[84:87], v[150:153], v[186:189], v[84:87]
	v_mfma_f32_16x16x32_bf16 v[80:83], v[162:165], v[186:189], v[80:83]
	v_mfma_f32_16x16x32_bf16 v[68:71], v[150:153], v[194:197], v[68:71]
	v_mfma_f32_16x16x32_bf16 v[64:67], v[162:165], v[194:197], v[64:67]
	v_mfma_f32_16x16x32_bf16 v[116:119], v[154:157], v[174:177], v[116:119]
	v_mfma_f32_16x16x32_bf16 v[112:115], v[166:169], v[174:177], v[112:115]
	v_mfma_f32_16x16x32_bf16 v[100:103], v[154:157], v[182:185], v[100:103]
	v_mfma_f32_16x16x32_bf16 v[96:99], v[166:169], v[182:185], v[96:99]
	v_mfma_f32_16x16x32_bf16 v[84:87], v[154:157], v[190:193], v[84:87]
	v_mfma_f32_16x16x32_bf16 v[80:83], v[166:169], v[190:193], v[80:83]
	v_mfma_f32_16x16x32_bf16 v[68:71], v[154:157], v[198:201], v[68:71]
	v_mfma_f32_16x16x32_bf16 v[64:67], v[166:169], v[198:201], v[64:67]
	s_barrier
	s_add_i32 s87, s87, s6
	v_lshl_add_u64 v[158:159], s[90:91], 0, v[160:161]
	s_mov_b32 m0, s87
	ds_read_b128 v[170:173], v137 offset:16384
	ds_read_b128 v[174:177], v137 offset:17408
	ds_read_b128 v[178:181], v137 offset:18432
	ds_read_b128 v[182:185], v137 offset:19456
	ds_read_b128 v[186:189], v137 offset:20480
	ds_read_b128 v[190:193], v137 offset:21504
	ds_read_b128 v[194:197], v137 offset:22528
	ds_read_b128 v[198:201], v137 offset:23552
	global_load_lds_dwordx4 v[158:159], off
	v_lshl_add_u64 v[202:203], v[158:159], 0, s[14:15]
	s_add_i32 m0, s87, 0x2000
	s_add_i32 s87, s92, s6
	global_load_lds_dwordx4 v[202:203], off
	v_lshl_add_u64 v[202:203], v[158:159], 0, s[60:61]
	s_mov_b32 m0, s87
	s_nop 0
	global_load_lds_dwordx4 v[202:203], off
	v_lshl_add_u64 v[202:203], v[158:159], 0, s[52:53]
	s_add_i32 m0, s87, 0x2000
	s_nop 0
	global_load_lds_dwordx4 v[202:203], off
	v_lshl_add_u64 v[202:203], s[2:3], 0, v[160:161]
	s_mov_b32 m0, s7
	v_lshl_add_u64 v[204:205], v[202:203], 0, s[14:15]
	global_load_lds_dwordx4 v[202:203], off
	s_mov_b32 m0, s10
	s_nop 0
	global_load_lds_dwordx4 v[204:205], off
	s_waitcnt vmcnt(8)
	s_waitcnt lgkmcnt(0)
	s_barrier
	s_waitcnt lgkmcnt(0)
	v_mfma_f32_16x16x32_bf16 v[60:63], v[130:133], v[170:173], v[60:63]
	v_mfma_f32_16x16x32_bf16 v[56:59], v[142:145], v[170:173], v[56:59]
	v_mfma_f32_16x16x32_bf16 v[44:47], v[130:133], v[178:181], v[44:47]
	v_mfma_f32_16x16x32_bf16 v[40:43], v[142:145], v[178:181], v[40:43]
	v_mfma_f32_16x16x32_bf16 v[28:31], v[130:133], v[186:189], v[28:31]
	v_mfma_f32_16x16x32_bf16 v[24:27], v[142:145], v[186:189], v[24:27]
	v_mfma_f32_16x16x32_bf16 v[12:15], v[130:133], v[194:197], v[12:15]
	v_mfma_f32_16x16x32_bf16 v[8:11], v[142:145], v[194:197], v[8:11]
	v_mfma_f32_16x16x32_bf16 v[60:63], v[138:141], v[174:177], v[60:63]
	v_mfma_f32_16x16x32_bf16 v[56:59], v[146:149], v[174:177], v[56:59]
	v_mfma_f32_16x16x32_bf16 v[44:47], v[138:141], v[182:185], v[44:47]
	v_mfma_f32_16x16x32_bf16 v[40:43], v[146:149], v[182:185], v[40:43]
	v_mfma_f32_16x16x32_bf16 v[28:31], v[138:141], v[190:193], v[28:31]
	v_mfma_f32_16x16x32_bf16 v[24:27], v[146:149], v[190:193], v[24:27]
	v_mfma_f32_16x16x32_bf16 v[12:15], v[138:141], v[198:201], v[12:15]
	v_mfma_f32_16x16x32_bf16 v[8:11], v[146:149], v[198:201], v[8:11]
	v_mfma_f32_16x16x32_bf16 v[52:55], v[150:153], v[170:173], v[52:55]
	v_mfma_f32_16x16x32_bf16 v[48:51], v[162:165], v[170:173], v[48:51]
	v_mfma_f32_16x16x32_bf16 v[36:39], v[150:153], v[178:181], v[36:39]
	v_mfma_f32_16x16x32_bf16 v[32:35], v[162:165], v[178:181], v[32:35]
	v_mfma_f32_16x16x32_bf16 v[20:23], v[150:153], v[186:189], v[20:23]
	v_mfma_f32_16x16x32_bf16 v[16:19], v[162:165], v[186:189], v[16:19]
	v_mfma_f32_16x16x32_bf16 v[4:7], v[150:153], v[194:197], v[4:7]
	v_mfma_f32_16x16x32_bf16 v[0:3], v[162:165], v[194:197], v[0:3]
	v_mfma_f32_16x16x32_bf16 v[52:55], v[154:157], v[174:177], v[52:55]
	v_mfma_f32_16x16x32_bf16 v[48:51], v[166:169], v[174:177], v[48:51]
	v_mfma_f32_16x16x32_bf16 v[36:39], v[154:157], v[182:185], v[36:39]
	v_mfma_f32_16x16x32_bf16 v[32:35], v[166:169], v[182:185], v[32:35]
	v_mfma_f32_16x16x32_bf16 v[20:23], v[154:157], v[190:193], v[20:23]
	v_mfma_f32_16x16x32_bf16 v[16:19], v[166:169], v[190:193], v[16:19]
	v_mfma_f32_16x16x32_bf16 v[4:7], v[154:157], v[198:201], v[4:7]
	v_mfma_f32_16x16x32_bf16 v[0:3], v[166:169], v[198:201], v[0:3]
	s_barrier
	s_add_i32 s2, 0, 0x18000
	s_add_i32 s3, 0, 0x1c000
	v_add_u32_e32 v146, s2, v135
	v_add_u32_e32 v166, s3, v135
	ds_read_b128 v[130:133], v146
	ds_read_b128 v[138:141], v146 offset:1024
	ds_read_b128 v[142:145], v146 offset:2048
	ds_read_b128 v[146:149], v146 offset:3072
	ds_read_b128 v[150:153], v166
	ds_read_b128 v[154:157], v166 offset:1024
	ds_read_b128 v[162:165], v166 offset:2048
	ds_read_b128 v[166:169], v166 offset:3072
	s_mov_b32 m0, s11
	v_lshl_add_u64 v[204:205], v[202:203], 0, s[60:61]
	ds_read_b128 v[170:173], v137 offset:32768
	ds_read_b128 v[174:177], v137 offset:33792
	ds_read_b128 v[178:181], v137 offset:34816
	ds_read_b128 v[182:185], v137 offset:35840
	ds_read_b128 v[186:189], v137 offset:36864
	ds_read_b128 v[190:193], v137 offset:37888
	ds_read_b128 v[194:197], v137 offset:38912
	ds_read_b128 v[198:201], v137 offset:39936
	global_load_lds_dwordx4 v[204:205], off
	v_lshl_add_u64 v[204:205], v[202:203], 0, s[52:53]
	s_mov_b32 m0, s63
	s_nop 0
	global_load_lds_dwordx4 v[204:205], off
	s_waitcnt vmcnt(8)
	s_waitcnt lgkmcnt(0)
	s_barrier
	s_waitcnt lgkmcnt(0)
	v_mfma_f32_16x16x32_bf16 v[124:127], v[130:133], v[170:173], v[124:127]
	v_mfma_f32_16x16x32_bf16 v[120:123], v[142:145], v[170:173], v[120:123]
	v_mfma_f32_16x16x32_bf16 v[108:111], v[130:133], v[178:181], v[108:111]
	v_mfma_f32_16x16x32_bf16 v[104:107], v[142:145], v[178:181], v[104:107]
	v_mfma_f32_16x16x32_bf16 v[92:95], v[130:133], v[186:189], v[92:95]
	v_mfma_f32_16x16x32_bf16 v[88:91], v[142:145], v[186:189], v[88:91]
	v_mfma_f32_16x16x32_bf16 v[76:79], v[130:133], v[194:197], v[76:79]
	v_mfma_f32_16x16x32_bf16 v[72:75], v[142:145], v[194:197], v[72:75]
	v_mfma_f32_16x16x32_bf16 v[124:127], v[138:141], v[174:177], v[124:127]
	v_mfma_f32_16x16x32_bf16 v[120:123], v[146:149], v[174:177], v[120:123]
	v_mfma_f32_16x16x32_bf16 v[108:111], v[138:141], v[182:185], v[108:111]
	v_mfma_f32_16x16x32_bf16 v[104:107], v[146:149], v[182:185], v[104:107]
	v_mfma_f32_16x16x32_bf16 v[92:95], v[138:141], v[190:193], v[92:95]
	v_mfma_f32_16x16x32_bf16 v[88:91], v[146:149], v[190:193], v[88:91]
	v_mfma_f32_16x16x32_bf16 v[76:79], v[138:141], v[198:201], v[76:79]
	v_mfma_f32_16x16x32_bf16 v[72:75], v[146:149], v[198:201], v[72:75]
	v_mfma_f32_16x16x32_bf16 v[116:119], v[150:153], v[170:173], v[116:119]
	v_mfma_f32_16x16x32_bf16 v[112:115], v[162:165], v[170:173], v[112:115]
	v_mfma_f32_16x16x32_bf16 v[100:103], v[150:153], v[178:181], v[100:103]
	v_mfma_f32_16x16x32_bf16 v[96:99], v[162:165], v[178:181], v[96:99]
	v_mfma_f32_16x16x32_bf16 v[84:87], v[150:153], v[186:189], v[84:87]
	v_mfma_f32_16x16x32_bf16 v[80:83], v[162:165], v[186:189], v[80:83]
	v_mfma_f32_16x16x32_bf16 v[68:71], v[150:153], v[194:197], v[68:71]
	v_mfma_f32_16x16x32_bf16 v[64:67], v[162:165], v[194:197], v[64:67]
	v_mfma_f32_16x16x32_bf16 v[116:119], v[154:157], v[174:177], v[116:119]
	v_mfma_f32_16x16x32_bf16 v[112:115], v[166:169], v[174:177], v[112:115]
	v_mfma_f32_16x16x32_bf16 v[100:103], v[154:157], v[182:185], v[100:103]
	v_mfma_f32_16x16x32_bf16 v[96:99], v[166:169], v[182:185], v[96:99]
	v_mfma_f32_16x16x32_bf16 v[84:87], v[154:157], v[190:193], v[84:87]
	v_mfma_f32_16x16x32_bf16 v[80:83], v[166:169], v[190:193], v[80:83]
	v_mfma_f32_16x16x32_bf16 v[68:71], v[154:157], v[198:201], v[68:71]
	v_mfma_f32_16x16x32_bf16 v[64:67], v[166:169], v[198:201], v[64:67]
	s_barrier
	s_add_i32 s2, s2, s6
	v_lshl_add_u64 v[204:205], v[158:159], 0, s[56:57]
	s_mov_b32 m0, s2
	ds_read_b128 v[170:173], v137 offset:49152
	ds_read_b128 v[174:177], v137 offset:50176
	ds_read_b128 v[178:181], v137 offset:51200
	ds_read_b128 v[182:185], v137 offset:52224
	ds_read_b128 v[186:189], v137 offset:53248
	ds_read_b128 v[190:193], v137 offset:54272
	ds_read_b128 v[194:197], v137 offset:55296
	ds_read_b128 v[198:201], v137 offset:56320
	global_load_lds_dwordx4 v[204:205], off
	v_lshl_add_u64 v[204:205], v[158:159], 0, s[0:1]
	s_add_i32 m0, s2, 0x2000
	s_add_i32 s2, s3, s6
	global_load_lds_dwordx4 v[204:205], off
	v_lshl_add_u64 v[204:205], v[158:159], 0, s[24:25]
	s_mov_b32 m0, s2
	v_lshl_add_u64 v[158:159], v[158:159], 0, s[26:27]
	global_load_lds_dwordx4 v[204:205], off
	s_add_i32 m0, s2, 0x2000
	s_nop 0
	global_load_lds_dwordx4 v[158:159], off
	v_lshl_add_u64 v[158:159], v[202:203], 0, s[56:57]
	s_mov_b32 m0, s77
	s_nop 0
	global_load_lds_dwordx4 v[158:159], off
	v_lshl_add_u64 v[158:159], v[202:203], 0, s[0:1]
	s_mov_b32 m0, s78
	s_nop 0
	global_load_lds_dwordx4 v[158:159], off
	s_waitcnt vmcnt(8)
	s_waitcnt lgkmcnt(0)
	s_barrier
	s_waitcnt lgkmcnt(0)
	v_mfma_f32_16x16x32_bf16 v[60:63], v[130:133], v[170:173], v[60:63]
	v_mfma_f32_16x16x32_bf16 v[56:59], v[142:145], v[170:173], v[56:59]
	v_mfma_f32_16x16x32_bf16 v[44:47], v[130:133], v[178:181], v[44:47]
	v_mfma_f32_16x16x32_bf16 v[40:43], v[142:145], v[178:181], v[40:43]
	v_mfma_f32_16x16x32_bf16 v[28:31], v[130:133], v[186:189], v[28:31]
	v_mfma_f32_16x16x32_bf16 v[24:27], v[142:145], v[186:189], v[24:27]
	v_mfma_f32_16x16x32_bf16 v[12:15], v[130:133], v[194:197], v[12:15]
	v_mfma_f32_16x16x32_bf16 v[8:11], v[142:145], v[194:197], v[8:11]
	v_mfma_f32_16x16x32_bf16 v[60:63], v[138:141], v[174:177], v[60:63]
	v_mfma_f32_16x16x32_bf16 v[56:59], v[146:149], v[174:177], v[56:59]
	v_mfma_f32_16x16x32_bf16 v[44:47], v[138:141], v[182:185], v[44:47]
	v_mfma_f32_16x16x32_bf16 v[40:43], v[146:149], v[182:185], v[40:43]
	v_mfma_f32_16x16x32_bf16 v[28:31], v[138:141], v[190:193], v[28:31]
	v_mfma_f32_16x16x32_bf16 v[24:27], v[146:149], v[190:193], v[24:27]
	v_mfma_f32_16x16x32_bf16 v[12:15], v[138:141], v[198:201], v[12:15]
	v_mfma_f32_16x16x32_bf16 v[8:11], v[146:149], v[198:201], v[8:11]
	v_mfma_f32_16x16x32_bf16 v[52:55], v[150:153], v[170:173], v[52:55]
	v_mfma_f32_16x16x32_bf16 v[48:51], v[162:165], v[170:173], v[48:51]
	v_mfma_f32_16x16x32_bf16 v[36:39], v[150:153], v[178:181], v[36:39]
	v_mfma_f32_16x16x32_bf16 v[32:35], v[162:165], v[178:181], v[32:35]
	v_mfma_f32_16x16x32_bf16 v[20:23], v[150:153], v[186:189], v[20:23]
	v_mfma_f32_16x16x32_bf16 v[16:19], v[162:165], v[186:189], v[16:19]
	v_mfma_f32_16x16x32_bf16 v[4:7], v[150:153], v[194:197], v[4:7]
	v_mfma_f32_16x16x32_bf16 v[0:3], v[162:165], v[194:197], v[0:3]
	v_mfma_f32_16x16x32_bf16 v[52:55], v[154:157], v[174:177], v[52:55]
	v_mfma_f32_16x16x32_bf16 v[48:51], v[166:169], v[174:177], v[48:51]
	v_mfma_f32_16x16x32_bf16 v[36:39], v[154:157], v[182:185], v[36:39]
	v_mfma_f32_16x16x32_bf16 v[32:35], v[166:169], v[182:185], v[32:35]
	v_mfma_f32_16x16x32_bf16 v[20:23], v[154:157], v[190:193], v[20:23]
	v_mfma_f32_16x16x32_bf16 v[16:19], v[166:169], v[190:193], v[16:19]
	v_mfma_f32_16x16x32_bf16 v[4:7], v[154:157], v[198:201], v[4:7]
	v_mfma_f32_16x16x32_bf16 v[0:3], v[166:169], v[198:201], v[0:3]
	s_barrier
	s_add_u32 s74, s74, 0x100
	s_addc_u32 s75, s75, 0
	s_add_u32 s22, s22, 0x100
	s_addc_u32 s23, s23, 0
	s_cmp_ge_i32 s86, s79
	s_mov_b32 s2, s86
	s_cbranch_scc0 .LBB0_1094

.LBB0_1232:
	s_add_i32 s81, s2, 2
	s_add_u32 s83, s54, 0xfffc0080
	s_addc_u32 s3, s55, -1
	s_cmp_eq_u32 s78, s2
	s_cselect_b32 s3, s38, s3
	s_cselect_b32 s2, s39, s83
	s_cselect_b32 s87, s45, s23
	s_cselect_b32 s86, s47, s22
	s_add_i32 s83, 0, 0x10000
	v_add_u32_e32 v132, s83, v135
	s_add_i32 s90, 0, 0x14000
	ds_read_b128 v[138:141], v132
	ds_read_b128 v[142:145], v132 offset:1024
	ds_read_b128 v[146:149], v132 offset:2048
	ds_read_b128 v[150:153], v132 offset:3072
	v_add_u32_e32 v132, s90, v135
	ds_read_b128 v[154:157], v132
	ds_read_b128 v[162:165], v132 offset:1024
	ds_read_b128 v[166:169], v132 offset:2048
	ds_read_b128 v[170:173], v132 offset:3072
	v_lshl_add_u64 v[132:133], s[54:55], 0, v[130:131]
	s_add_i32 m0, s33, 0xc000
	ds_read_b128 v[174:177], v137
	ds_read_b128 v[178:181], v137 offset:1024
	ds_read_b128 v[182:185], v137 offset:2048
	ds_read_b128 v[186:189], v137 offset:3072
	ds_read_b128 v[190:193], v137 offset:4096
	ds_read_b128 v[194:197], v137 offset:5120
	ds_read_b128 v[198:201], v137 offset:6144
	ds_read_b128 v[202:205], v137 offset:7168
	global_load_lds_dwordx4 v[132:133], off
	v_lshl_add_u64 v[132:133], v[132:133], 0, s[14:15]
	s_add_i32 m0, s33, 0xe000
	s_nop 0
	global_load_lds_dwordx4 v[132:133], off
	s_waitcnt vmcnt(8)
	s_waitcnt lgkmcnt(0)
	s_barrier
	s_waitcnt lgkmcnt(0)
	v_mfma_f32_16x16x32_bf16 v[124:127], v[138:141], v[174:177], v[124:127]
	v_mfma_f32_16x16x32_bf16 v[116:119], v[146:149], v[174:177], v[116:119]
	v_mfma_f32_16x16x32_bf16 v[108:111], v[138:141], v[182:185], v[108:111]
	v_mfma_f32_16x16x32_bf16 v[100:103], v[146:149], v[182:185], v[100:103]
	v_mfma_f32_16x16x32_bf16 v[92:95], v[138:141], v[190:193], v[92:95]
	v_mfma_f32_16x16x32_bf16 v[84:87], v[146:149], v[190:193], v[84:87]
	v_mfma_f32_16x16x32_bf16 v[76:79], v[138:141], v[198:201], v[76:79]
	v_mfma_f32_16x16x32_bf16 v[68:71], v[146:149], v[198:201], v[68:71]
	v_mfma_f32_16x16x32_bf16 v[124:127], v[142:145], v[178:181], v[124:127]
	v_mfma_f32_16x16x32_bf16 v[116:119], v[150:153], v[178:181], v[116:119]
	v_mfma_f32_16x16x32_bf16 v[108:111], v[142:145], v[186:189], v[108:111]
	v_mfma_f32_16x16x32_bf16 v[100:103], v[150:153], v[186:189], v[100:103]
	v_mfma_f32_16x16x32_bf16 v[92:95], v[142:145], v[194:197], v[92:95]
	v_mfma_f32_16x16x32_bf16 v[84:87], v[150:153], v[194:197], v[84:87]
	v_mfma_f32_16x16x32_bf16 v[76:79], v[142:145], v[202:205], v[76:79]
	v_mfma_f32_16x16x32_bf16 v[68:71], v[150:153], v[202:205], v[68:71]
	v_mfma_f32_16x16x32_bf16 v[120:123], v[154:157], v[174:177], v[120:123]
	v_mfma_f32_16x16x32_bf16 v[112:115], v[166:169], v[174:177], v[112:115]
	v_mfma_f32_16x16x32_bf16 v[104:107], v[154:157], v[182:185], v[104:107]
	v_mfma_f32_16x16x32_bf16 v[96:99], v[166:169], v[182:185], v[96:99]
	v_mfma_f32_16x16x32_bf16 v[88:91], v[154:157], v[190:193], v[88:91]
	v_mfma_f32_16x16x32_bf16 v[80:83], v[166:169], v[190:193], v[80:83]
	v_mfma_f32_16x16x32_bf16 v[72:75], v[154:157], v[198:201], v[72:75]
	v_mfma_f32_16x16x32_bf16 v[64:67], v[166:169], v[198:201], v[64:67]
	v_mfma_f32_16x16x32_bf16 v[120:123], v[162:165], v[178:181], v[120:123]
	v_mfma_f32_16x16x32_bf16 v[112:115], v[170:173], v[178:181], v[112:115]
	v_mfma_f32_16x16x32_bf16 v[104:107], v[162:165], v[186:189], v[104:107]
	v_mfma_f32_16x16x32_bf16 v[96:99], v[170:173], v[186:189], v[96:99]
	v_mfma_f32_16x16x32_bf16 v[88:91], v[162:165], v[194:197], v[88:91]
	v_mfma_f32_16x16x32_bf16 v[80:83], v[170:173], v[194:197], v[80:83]
	v_mfma_f32_16x16x32_bf16 v[72:75], v[162:165], v[202:205], v[72:75]
	v_mfma_f32_16x16x32_bf16 v[64:67], v[170:173], v[202:205], v[64:67]
	s_barrier
	s_add_i32 s83, s83, s31
	v_lshl_add_u64 v[132:133], s[86:87], 0, v[160:161]
	s_mov_b32 m0, s83
	ds_read_b128 v[174:177], v137 offset:16384
	ds_read_b128 v[178:181], v137 offset:17408
	ds_read_b128 v[182:185], v137 offset:18432
	ds_read_b128 v[186:189], v137 offset:19456
	ds_read_b128 v[190:193], v137 offset:20480
	ds_read_b128 v[194:197], v137 offset:21504
	ds_read_b128 v[198:201], v137 offset:22528
	ds_read_b128 v[202:205], v137 offset:23552
	global_load_lds_dwordx4 v[132:133], off
	v_lshl_add_u64 v[158:159], v[132:133], 0, s[14:15]
	s_add_i32 m0, s83, 0x2000
	s_add_i32 s83, s90, s31
	global_load_lds_dwordx4 v[158:159], off
	v_lshl_add_u64 v[158:159], v[132:133], 0, s[60:61]
	s_mov_b32 m0, s83
	s_nop 0
	global_load_lds_dwordx4 v[158:159], off
	v_lshl_add_u64 v[158:159], v[132:133], 0, s[52:53]
	s_add_i32 m0, s83, 0x2000
	s_nop 0
	global_load_lds_dwordx4 v[158:159], off
	v_lshl_add_u64 v[158:159], s[2:3], 0, v[128:129]
	s_mov_b32 m0, s33
	v_lshl_add_u64 v[206:207], v[158:159], 0, s[14:15]
	global_load_lds_dwordx4 v[158:159], off
	s_mov_b32 m0, s58
	s_nop 0
	global_load_lds_dwordx4 v[206:207], off
	s_waitcnt vmcnt(8)
	s_waitcnt lgkmcnt(0)
	s_barrier
	s_waitcnt lgkmcnt(0)
	v_mfma_f32_16x16x32_bf16 v[60:63], v[138:141], v[174:177], v[60:63]
	v_mfma_f32_16x16x32_bf16 v[52:55], v[146:149], v[174:177], v[52:55]
	v_mfma_f32_16x16x32_bf16 v[44:47], v[138:141], v[182:185], v[44:47]
	v_mfma_f32_16x16x32_bf16 v[36:39], v[146:149], v[182:185], v[36:39]
	v_mfma_f32_16x16x32_bf16 v[28:31], v[138:141], v[190:193], v[28:31]
	v_mfma_f32_16x16x32_bf16 v[20:23], v[146:149], v[190:193], v[20:23]
	v_mfma_f32_16x16x32_bf16 v[12:15], v[138:141], v[198:201], v[12:15]
	v_mfma_f32_16x16x32_bf16 v[4:7], v[146:149], v[198:201], v[4:7]
	v_mfma_f32_16x16x32_bf16 v[60:63], v[142:145], v[178:181], v[60:63]
	v_mfma_f32_16x16x32_bf16 v[52:55], v[150:153], v[178:181], v[52:55]
	v_mfma_f32_16x16x32_bf16 v[44:47], v[142:145], v[186:189], v[44:47]
	v_mfma_f32_16x16x32_bf16 v[36:39], v[150:153], v[186:189], v[36:39]
	v_mfma_f32_16x16x32_bf16 v[28:31], v[142:145], v[194:197], v[28:31]
	v_mfma_f32_16x16x32_bf16 v[20:23], v[150:153], v[194:197], v[20:23]
	v_mfma_f32_16x16x32_bf16 v[12:15], v[142:145], v[202:205], v[12:15]
	v_mfma_f32_16x16x32_bf16 v[4:7], v[150:153], v[202:205], v[4:7]
	v_mfma_f32_16x16x32_bf16 v[56:59], v[154:157], v[174:177], v[56:59]
	v_mfma_f32_16x16x32_bf16 v[48:51], v[166:169], v[174:177], v[48:51]
	v_mfma_f32_16x16x32_bf16 v[40:43], v[154:157], v[182:185], v[40:43]
	v_mfma_f32_16x16x32_bf16 v[32:35], v[166:169], v[182:185], v[32:35]
	v_mfma_f32_16x16x32_bf16 v[24:27], v[154:157], v[190:193], v[24:27]
	v_mfma_f32_16x16x32_bf16 v[16:19], v[166:169], v[190:193], v[16:19]
	v_mfma_f32_16x16x32_bf16 v[8:11], v[154:157], v[198:201], v[8:11]
	v_mfma_f32_16x16x32_bf16 v[0:3], v[166:169], v[198:201], v[0:3]
	v_mfma_f32_16x16x32_bf16 v[56:59], v[162:165], v[178:181], v[56:59]
	v_mfma_f32_16x16x32_bf16 v[48:51], v[170:173], v[178:181], v[48:51]
	v_mfma_f32_16x16x32_bf16 v[40:43], v[162:165], v[186:189], v[40:43]
	v_mfma_f32_16x16x32_bf16 v[32:35], v[170:173], v[186:189], v[32:35]
	v_mfma_f32_16x16x32_bf16 v[24:27], v[162:165], v[194:197], v[24:27]
	v_mfma_f32_16x16x32_bf16 v[16:19], v[170:173], v[194:197], v[16:19]
	v_mfma_f32_16x16x32_bf16 v[8:11], v[162:165], v[202:205], v[8:11]
	v_mfma_f32_16x16x32_bf16 v[0:3], v[170:173], v[202:205], v[0:3]
	s_barrier
	s_add_i32 s2, 0, 0x18000
	s_add_i32 s3, 0, 0x1c000
	v_add_u32_e32 v150, s2, v135
	v_add_u32_e32 v170, s3, v135
	ds_read_b128 v[138:141], v150
	ds_read_b128 v[142:145], v150 offset:1024
	ds_read_b128 v[146:149], v150 offset:2048
	ds_read_b128 v[150:153], v150 offset:3072
	ds_read_b128 v[154:157], v170
	ds_read_b128 v[162:165], v170 offset:1024
	ds_read_b128 v[166:169], v170 offset:2048
	ds_read_b128 v[170:173], v170 offset:3072
	s_mov_b32 m0, s59
	v_lshl_add_u64 v[206:207], v[158:159], 0, s[60:61]
	ds_read_b128 v[174:177], v137 offset:32768
	ds_read_b128 v[178:181], v137 offset:33792
	ds_read_b128 v[182:185], v137 offset:34816
	ds_read_b128 v[186:189], v137 offset:35840
	ds_read_b128 v[190:193], v137 offset:36864
	ds_read_b128 v[194:197], v137 offset:37888
	ds_read_b128 v[198:201], v137 offset:38912
	ds_read_b128 v[202:205], v137 offset:39936
	global_load_lds_dwordx4 v[206:207], off
	v_lshl_add_u64 v[206:207], v[158:159], 0, s[52:53]
	s_mov_b32 m0, s63
	s_nop 0
	global_load_lds_dwordx4 v[206:207], off
	s_waitcnt vmcnt(8)
	s_waitcnt lgkmcnt(0)
	s_barrier
	s_waitcnt lgkmcnt(0)
	v_mfma_f32_16x16x32_bf16 v[124:127], v[138:141], v[174:177], v[124:127]
	v_mfma_f32_16x16x32_bf16 v[116:119], v[146:149], v[174:177], v[116:119]
	v_mfma_f32_16x16x32_bf16 v[108:111], v[138:141], v[182:185], v[108:111]
	v_mfma_f32_16x16x32_bf16 v[100:103], v[146:149], v[182:185], v[100:103]
	v_mfma_f32_16x16x32_bf16 v[92:95], v[138:141], v[190:193], v[92:95]
	v_mfma_f32_16x16x32_bf16 v[84:87], v[146:149], v[190:193], v[84:87]
	v_mfma_f32_16x16x32_bf16 v[76:79], v[138:141], v[198:201], v[76:79]
	v_mfma_f32_16x16x32_bf16 v[68:71], v[146:149], v[198:201], v[68:71]
	v_mfma_f32_16x16x32_bf16 v[124:127], v[142:145], v[178:181], v[124:127]
	v_mfma_f32_16x16x32_bf16 v[116:119], v[150:153], v[178:181], v[116:119]
	v_mfma_f32_16x16x32_bf16 v[108:111], v[142:145], v[186:189], v[108:111]
	v_mfma_f32_16x16x32_bf16 v[100:103], v[150:153], v[186:189], v[100:103]
	v_mfma_f32_16x16x32_bf16 v[92:95], v[142:145], v[194:197], v[92:95]
	v_mfma_f32_16x16x32_bf16 v[84:87], v[150:153], v[194:197], v[84:87]
	v_mfma_f32_16x16x32_bf16 v[76:79], v[142:145], v[202:205], v[76:79]
	v_mfma_f32_16x16x32_bf16 v[68:71], v[150:153], v[202:205], v[68:71]
	v_mfma_f32_16x16x32_bf16 v[120:123], v[154:157], v[174:177], v[120:123]
	v_mfma_f32_16x16x32_bf16 v[112:115], v[166:169], v[174:177], v[112:115]
	v_mfma_f32_16x16x32_bf16 v[104:107], v[154:157], v[182:185], v[104:107]
	v_mfma_f32_16x16x32_bf16 v[96:99], v[166:169], v[182:185], v[96:99]
	v_mfma_f32_16x16x32_bf16 v[88:91], v[154:157], v[190:193], v[88:91]
	v_mfma_f32_16x16x32_bf16 v[80:83], v[166:169], v[190:193], v[80:83]
	v_mfma_f32_16x16x32_bf16 v[72:75], v[154:157], v[198:201], v[72:75]
	v_mfma_f32_16x16x32_bf16 v[64:67], v[166:169], v[198:201], v[64:67]
	v_mfma_f32_16x16x32_bf16 v[120:123], v[162:165], v[178:181], v[120:123]
	v_mfma_f32_16x16x32_bf16 v[112:115], v[170:173], v[178:181], v[112:115]
	v_mfma_f32_16x16x32_bf16 v[104:107], v[162:165], v[186:189], v[104:107]
	v_mfma_f32_16x16x32_bf16 v[96:99], v[170:173], v[186:189], v[96:99]
	v_mfma_f32_16x16x32_bf16 v[88:91], v[162:165], v[194:197], v[88:91]
	v_mfma_f32_16x16x32_bf16 v[80:83], v[170:173], v[194:197], v[80:83]
	v_mfma_f32_16x16x32_bf16 v[72:75], v[162:165], v[202:205], v[72:75]
	v_mfma_f32_16x16x32_bf16 v[64:67], v[170:173], v[202:205], v[64:67]
	s_barrier
	s_add_i32 s2, s2, s31
	v_lshl_add_u64 v[206:207], v[132:133], 0, s[56:57]
	s_mov_b32 m0, s2
	ds_read_b128 v[174:177], v137 offset:49152
	ds_read_b128 v[178:181], v137 offset:50176
	ds_read_b128 v[182:185], v137 offset:51200
	ds_read_b128 v[186:189], v137 offset:52224
	ds_read_b128 v[190:193], v137 offset:53248
	ds_read_b128 v[194:197], v137 offset:54272
	ds_read_b128 v[198:201], v137 offset:55296
	ds_read_b128 v[202:205], v137 offset:56320
	global_load_lds_dwordx4 v[206:207], off
	v_lshl_add_u64 v[206:207], v[132:133], 0, s[0:1]
	s_add_i32 m0, s2, 0x2000
	s_add_i32 s2, s3, s31
	global_load_lds_dwordx4 v[206:207], off
	v_lshl_add_u64 v[206:207], v[132:133], 0, s[24:25]
	s_mov_b32 m0, s2
	v_lshl_add_u64 v[132:133], v[132:133], 0, s[26:27]
	global_load_lds_dwordx4 v[206:207], off
	s_add_i32 m0, s2, 0x2000
	s_nop 0
	global_load_lds_dwordx4 v[132:133], off
	v_lshl_add_u64 v[132:133], v[158:159], 0, s[56:57]
	s_mov_b32 m0, s74
	s_nop 0
	global_load_lds_dwordx4 v[132:133], off
	v_lshl_add_u64 v[132:133], v[158:159], 0, s[0:1]
	s_mov_b32 m0, s75
	s_nop 0
	global_load_lds_dwordx4 v[132:133], off
	s_waitcnt vmcnt(8)
	s_waitcnt lgkmcnt(0)
	s_barrier
	s_waitcnt lgkmcnt(0)
	v_mfma_f32_16x16x32_bf16 v[60:63], v[138:141], v[174:177], v[60:63]
	v_mfma_f32_16x16x32_bf16 v[52:55], v[146:149], v[174:177], v[52:55]
	v_mfma_f32_16x16x32_bf16 v[44:47], v[138:141], v[182:185], v[44:47]
	v_mfma_f32_16x16x32_bf16 v[36:39], v[146:149], v[182:185], v[36:39]
	v_mfma_f32_16x16x32_bf16 v[28:31], v[138:141], v[190:193], v[28:31]
	v_mfma_f32_16x16x32_bf16 v[20:23], v[146:149], v[190:193], v[20:23]
	v_mfma_f32_16x16x32_bf16 v[12:15], v[138:141], v[198:201], v[12:15]
	v_mfma_f32_16x16x32_bf16 v[4:7], v[146:149], v[198:201], v[4:7]
	v_mfma_f32_16x16x32_bf16 v[60:63], v[142:145], v[178:181], v[60:63]
	v_mfma_f32_16x16x32_bf16 v[52:55], v[150:153], v[178:181], v[52:55]
	v_mfma_f32_16x16x32_bf16 v[44:47], v[142:145], v[186:189], v[44:47]
	v_mfma_f32_16x16x32_bf16 v[36:39], v[150:153], v[186:189], v[36:39]
	v_mfma_f32_16x16x32_bf16 v[28:31], v[142:145], v[194:197], v[28:31]
	v_mfma_f32_16x16x32_bf16 v[20:23], v[150:153], v[194:197], v[20:23]
	v_mfma_f32_16x16x32_bf16 v[12:15], v[142:145], v[202:205], v[12:15]
	v_mfma_f32_16x16x32_bf16 v[4:7], v[150:153], v[202:205], v[4:7]
	v_mfma_f32_16x16x32_bf16 v[56:59], v[154:157], v[174:177], v[56:59]
	v_mfma_f32_16x16x32_bf16 v[48:51], v[166:169], v[174:177], v[48:51]
	v_mfma_f32_16x16x32_bf16 v[40:43], v[154:157], v[182:185], v[40:43]
	v_mfma_f32_16x16x32_bf16 v[32:35], v[166:169], v[182:185], v[32:35]
	v_mfma_f32_16x16x32_bf16 v[24:27], v[154:157], v[190:193], v[24:27]
	v_mfma_f32_16x16x32_bf16 v[16:19], v[166:169], v[190:193], v[16:19]
	v_mfma_f32_16x16x32_bf16 v[8:11], v[154:157], v[198:201], v[8:11]
	v_mfma_f32_16x16x32_bf16 v[0:3], v[166:169], v[198:201], v[0:3]
	v_mfma_f32_16x16x32_bf16 v[56:59], v[162:165], v[178:181], v[56:59]
	v_mfma_f32_16x16x32_bf16 v[48:51], v[170:173], v[178:181], v[48:51]
	v_mfma_f32_16x16x32_bf16 v[40:43], v[162:165], v[186:189], v[40:43]
	v_mfma_f32_16x16x32_bf16 v[32:35], v[170:173], v[186:189], v[32:35]
	v_mfma_f32_16x16x32_bf16 v[24:27], v[162:165], v[194:197], v[24:27]
	v_mfma_f32_16x16x32_bf16 v[16:19], v[170:173], v[194:197], v[16:19]
	v_mfma_f32_16x16x32_bf16 v[8:11], v[162:165], v[202:205], v[8:11]
	v_mfma_f32_16x16x32_bf16 v[0:3], v[170:173], v[202:205], v[0:3]
	s_barrier
	s_add_u32 s54, s54, 0x100
	s_addc_u32 s55, s55, 0
	s_add_u32 s22, s22, 0x100
	s_addc_u32 s23, s23, 0
	s_cmp_ge_i32 s81, s77
	s_mov_b32 s2, s81
	s_cbranch_scc0 .LBB0_1232

.LBB0_1311:
	s_add_i32 s77, s2, 2
	s_add_u32 s78, s46, 0xfff20080
	s_addc_u32 s3, s47, -1
	s_cmp_eq_u32 s58, s2
	s_cselect_b32 s3, s19, s3
	s_cselect_b32 s2, s18, s78
	s_cselect_b32 s79, s39, s23
	s_cselect_b32 s78, s38, s22
	s_add_i32 s80, 0, 0x10000
	s_add_i32 s81, 0, 0x14000
	v_add_u32_e32 v142, s80, v153
	v_add_u32_e32 v150, s81, v153
	ds_read_b128 v[130:133], v142
	ds_read_b128 v[134:137], v142 offset:1024
	ds_read_b128 v[138:141], v142 offset:2048
	ds_read_b128 v[142:145], v142 offset:3072
	ds_read_b128 v[146:149], v150
	ds_read_b128 v[156:159], v150 offset:1024
	ds_read_b128 v[162:165], v150 offset:2048
	ds_read_b128 v[166:169], v150 offset:3072
	v_lshl_add_u64 v[150:151], s[46:47], 0, v[128:129]
	s_add_i32 m0, s33, 0xc000
	ds_read_b128 v[170:173], v155
	ds_read_b128 v[174:177], v155 offset:1024
	ds_read_b128 v[178:181], v155 offset:2048
	ds_read_b128 v[182:185], v155 offset:3072
	ds_read_b128 v[186:189], v155 offset:4096
	ds_read_b128 v[190:193], v155 offset:5120
	ds_read_b128 v[194:197], v155 offset:6144
	ds_read_b128 v[198:201], v155 offset:7168
	global_load_lds_dwordx4 v[150:151], off
	v_lshl_add_u64 v[150:151], v[150:151], 0, s[84:85]
	s_add_i32 m0, s33, 0xe000
	s_nop 0
	global_load_lds_dwordx4 v[150:151], off
	s_waitcnt vmcnt(8)
	s_waitcnt lgkmcnt(0)
	s_barrier
	s_waitcnt lgkmcnt(0)
	v_mfma_f32_16x16x32_bf16 v[124:127], v[130:133], v[170:173], v[124:127]
	v_mfma_f32_16x16x32_bf16 v[120:123], v[138:141], v[170:173], v[120:123]
	v_mfma_f32_16x16x32_bf16 v[108:111], v[130:133], v[178:181], v[108:111]
	v_mfma_f32_16x16x32_bf16 v[104:107], v[138:141], v[178:181], v[104:107]
	v_mfma_f32_16x16x32_bf16 v[92:95], v[130:133], v[186:189], v[92:95]
	v_mfma_f32_16x16x32_bf16 v[88:91], v[138:141], v[186:189], v[88:91]
	v_mfma_f32_16x16x32_bf16 v[76:79], v[130:133], v[194:197], v[76:79]
	v_mfma_f32_16x16x32_bf16 v[72:75], v[138:141], v[194:197], v[72:75]
	v_mfma_f32_16x16x32_bf16 v[124:127], v[134:137], v[174:177], v[124:127]
	v_mfma_f32_16x16x32_bf16 v[120:123], v[142:145], v[174:177], v[120:123]
	v_mfma_f32_16x16x32_bf16 v[108:111], v[134:137], v[182:185], v[108:111]
	v_mfma_f32_16x16x32_bf16 v[104:107], v[142:145], v[182:185], v[104:107]
	v_mfma_f32_16x16x32_bf16 v[92:95], v[134:137], v[190:193], v[92:95]
	v_mfma_f32_16x16x32_bf16 v[88:91], v[142:145], v[190:193], v[88:91]
	v_mfma_f32_16x16x32_bf16 v[76:79], v[134:137], v[198:201], v[76:79]
	v_mfma_f32_16x16x32_bf16 v[72:75], v[142:145], v[198:201], v[72:75]
	v_mfma_f32_16x16x32_bf16 v[116:119], v[146:149], v[170:173], v[116:119]
	v_mfma_f32_16x16x32_bf16 v[112:115], v[162:165], v[170:173], v[112:115]
	v_mfma_f32_16x16x32_bf16 v[100:103], v[146:149], v[178:181], v[100:103]
	v_mfma_f32_16x16x32_bf16 v[96:99], v[162:165], v[178:181], v[96:99]
	v_mfma_f32_16x16x32_bf16 v[84:87], v[146:149], v[186:189], v[84:87]
	v_mfma_f32_16x16x32_bf16 v[80:83], v[162:165], v[186:189], v[80:83]
	v_mfma_f32_16x16x32_bf16 v[68:71], v[146:149], v[194:197], v[68:71]
	v_mfma_f32_16x16x32_bf16 v[64:67], v[162:165], v[194:197], v[64:67]
	v_mfma_f32_16x16x32_bf16 v[116:119], v[156:159], v[174:177], v[116:119]
	v_mfma_f32_16x16x32_bf16 v[112:115], v[166:169], v[174:177], v[112:115]
	v_mfma_f32_16x16x32_bf16 v[100:103], v[156:159], v[182:185], v[100:103]
	v_mfma_f32_16x16x32_bf16 v[96:99], v[166:169], v[182:185], v[96:99]
	v_mfma_f32_16x16x32_bf16 v[84:87], v[156:159], v[190:193], v[84:87]
	v_mfma_f32_16x16x32_bf16 v[80:83], v[166:169], v[190:193], v[80:83]
	v_mfma_f32_16x16x32_bf16 v[68:71], v[156:159], v[198:201], v[68:71]
	v_mfma_f32_16x16x32_bf16 v[64:67], v[166:169], v[198:201], v[64:67]
	s_barrier
	v_lshl_add_u64 v[150:151], s[78:79], 0, v[160:161]
	s_add_i32 s78, s80, s31
	s_mov_b32 m0, s78
	ds_read_b128 v[170:173], v155 offset:16384
	ds_read_b128 v[174:177], v155 offset:17408
	ds_read_b128 v[178:181], v155 offset:18432
	ds_read_b128 v[182:185], v155 offset:19456
	ds_read_b128 v[186:189], v155 offset:20480
	ds_read_b128 v[190:193], v155 offset:21504
	ds_read_b128 v[194:197], v155 offset:22528
	ds_read_b128 v[198:201], v155 offset:23552
	global_load_lds_dwordx4 v[150:151], off
	v_lshl_add_u64 v[202:203], v[150:151], 0, s[84:85]
	s_add_i32 m0, s78, 0x2000
	s_add_i32 s78, s81, s31
	global_load_lds_dwordx4 v[202:203], off
	v_lshl_add_u64 v[202:203], v[150:151], 0, s[4:5]
	s_mov_b32 m0, s78
	s_nop 0
	global_load_lds_dwordx4 v[202:203], off
	v_lshl_add_u64 v[202:203], v[150:151], 0, s[12:13]
	s_add_i32 m0, s78, 0x2000
	s_nop 0
	global_load_lds_dwordx4 v[202:203], off
	v_lshl_add_u64 v[202:203], s[2:3], 0, v[160:161]
	s_mov_b32 m0, s33
	v_lshl_add_u64 v[204:205], v[202:203], 0, s[84:85]
	global_load_lds_dwordx4 v[202:203], off
	s_mov_b32 m0, s48
	s_nop 0
	global_load_lds_dwordx4 v[204:205], off
	s_waitcnt vmcnt(8)
	s_waitcnt lgkmcnt(0)
	s_barrier
	s_waitcnt lgkmcnt(0)
	v_mfma_f32_16x16x32_bf16 v[60:63], v[130:133], v[170:173], v[60:63]
	v_mfma_f32_16x16x32_bf16 v[56:59], v[138:141], v[170:173], v[56:59]
	v_mfma_f32_16x16x32_bf16 v[44:47], v[130:133], v[178:181], v[44:47]
	v_mfma_f32_16x16x32_bf16 v[40:43], v[138:141], v[178:181], v[40:43]
	v_mfma_f32_16x16x32_bf16 v[28:31], v[130:133], v[186:189], v[28:31]
	v_mfma_f32_16x16x32_bf16 v[24:27], v[138:141], v[186:189], v[24:27]
	v_mfma_f32_16x16x32_bf16 v[12:15], v[130:133], v[194:197], v[12:15]
	v_mfma_f32_16x16x32_bf16 v[8:11], v[138:141], v[194:197], v[8:11]
	v_mfma_f32_16x16x32_bf16 v[60:63], v[134:137], v[174:177], v[60:63]
	v_mfma_f32_16x16x32_bf16 v[56:59], v[142:145], v[174:177], v[56:59]
	v_mfma_f32_16x16x32_bf16 v[44:47], v[134:137], v[182:185], v[44:47]
	v_mfma_f32_16x16x32_bf16 v[40:43], v[142:145], v[182:185], v[40:43]
	v_mfma_f32_16x16x32_bf16 v[28:31], v[134:137], v[190:193], v[28:31]
	v_mfma_f32_16x16x32_bf16 v[24:27], v[142:145], v[190:193], v[24:27]
	v_mfma_f32_16x16x32_bf16 v[12:15], v[134:137], v[198:201], v[12:15]
	v_mfma_f32_16x16x32_bf16 v[8:11], v[142:145], v[198:201], v[8:11]
	v_mfma_f32_16x16x32_bf16 v[52:55], v[146:149], v[170:173], v[52:55]
	v_mfma_f32_16x16x32_bf16 v[48:51], v[162:165], v[170:173], v[48:51]
	v_mfma_f32_16x16x32_bf16 v[36:39], v[146:149], v[178:181], v[36:39]
	v_mfma_f32_16x16x32_bf16 v[32:35], v[162:165], v[178:181], v[32:35]
	v_mfma_f32_16x16x32_bf16 v[20:23], v[146:149], v[186:189], v[20:23]
	v_mfma_f32_16x16x32_bf16 v[16:19], v[162:165], v[186:189], v[16:19]
	v_mfma_f32_16x16x32_bf16 v[4:7], v[146:149], v[194:197], v[4:7]
	v_mfma_f32_16x16x32_bf16 v[0:3], v[162:165], v[194:197], v[0:3]
	v_mfma_f32_16x16x32_bf16 v[52:55], v[156:159], v[174:177], v[52:55]
	v_mfma_f32_16x16x32_bf16 v[48:51], v[166:169], v[174:177], v[48:51]
	v_mfma_f32_16x16x32_bf16 v[36:39], v[156:159], v[182:185], v[36:39]
	v_mfma_f32_16x16x32_bf16 v[32:35], v[166:169], v[182:185], v[32:35]
	v_mfma_f32_16x16x32_bf16 v[20:23], v[156:159], v[190:193], v[20:23]
	v_mfma_f32_16x16x32_bf16 v[16:19], v[166:169], v[190:193], v[16:19]
	v_mfma_f32_16x16x32_bf16 v[4:7], v[156:159], v[198:201], v[4:7]
	v_mfma_f32_16x16x32_bf16 v[0:3], v[166:169], v[198:201], v[0:3]
	s_barrier
	s_add_i32 s2, 0, 0x18000
	s_add_i32 s3, 0, 0x1c000
	v_add_u32_e32 v142, s2, v153
	v_add_u32_e32 v166, s3, v153
	ds_read_b128 v[130:133], v142
	ds_read_b128 v[134:137], v142 offset:1024
	ds_read_b128 v[138:141], v142 offset:2048
	ds_read_b128 v[142:145], v142 offset:3072
	ds_read_b128 v[146:149], v166
	ds_read_b128 v[156:159], v166 offset:1024
	ds_read_b128 v[162:165], v166 offset:2048
	ds_read_b128 v[166:169], v166 offset:3072
	s_mov_b32 m0, s49
	v_lshl_add_u64 v[204:205], v[202:203], 0, s[4:5]
	ds_read_b128 v[170:173], v155 offset:32768
	ds_read_b128 v[174:177], v155 offset:33792
	ds_read_b128 v[178:181], v155 offset:34816
	ds_read_b128 v[182:185], v155 offset:35840
	ds_read_b128 v[186:189], v155 offset:36864
	ds_read_b128 v[190:193], v155 offset:37888
	ds_read_b128 v[194:197], v155 offset:38912
	ds_read_b128 v[198:201], v155 offset:39936
	global_load_lds_dwordx4 v[204:205], off
	v_lshl_add_u64 v[204:205], v[202:203], 0, s[12:13]
	s_mov_b32 m0, s50
	s_nop 0
	global_load_lds_dwordx4 v[204:205], off
	s_waitcnt vmcnt(8)
	s_waitcnt lgkmcnt(0)
	s_barrier
	s_waitcnt lgkmcnt(0)
	v_mfma_f32_16x16x32_bf16 v[124:127], v[130:133], v[170:173], v[124:127]
	v_mfma_f32_16x16x32_bf16 v[120:123], v[138:141], v[170:173], v[120:123]
	v_mfma_f32_16x16x32_bf16 v[108:111], v[130:133], v[178:181], v[108:111]
	v_mfma_f32_16x16x32_bf16 v[104:107], v[138:141], v[178:181], v[104:107]
	v_mfma_f32_16x16x32_bf16 v[92:95], v[130:133], v[186:189], v[92:95]
	v_mfma_f32_16x16x32_bf16 v[88:91], v[138:141], v[186:189], v[88:91]
	v_mfma_f32_16x16x32_bf16 v[76:79], v[130:133], v[194:197], v[76:79]
	v_mfma_f32_16x16x32_bf16 v[72:75], v[138:141], v[194:197], v[72:75]
	v_mfma_f32_16x16x32_bf16 v[124:127], v[134:137], v[174:177], v[124:127]
	v_mfma_f32_16x16x32_bf16 v[120:123], v[142:145], v[174:177], v[120:123]
	v_mfma_f32_16x16x32_bf16 v[108:111], v[134:137], v[182:185], v[108:111]
	v_mfma_f32_16x16x32_bf16 v[104:107], v[142:145], v[182:185], v[104:107]
	v_mfma_f32_16x16x32_bf16 v[92:95], v[134:137], v[190:193], v[92:95]
	v_mfma_f32_16x16x32_bf16 v[88:91], v[142:145], v[190:193], v[88:91]
	v_mfma_f32_16x16x32_bf16 v[76:79], v[134:137], v[198:201], v[76:79]
	v_mfma_f32_16x16x32_bf16 v[72:75], v[142:145], v[198:201], v[72:75]
	v_mfma_f32_16x16x32_bf16 v[116:119], v[146:149], v[170:173], v[116:119]
	v_mfma_f32_16x16x32_bf16 v[112:115], v[162:165], v[170:173], v[112:115]
	v_mfma_f32_16x16x32_bf16 v[100:103], v[146:149], v[178:181], v[100:103]
	v_mfma_f32_16x16x32_bf16 v[96:99], v[162:165], v[178:181], v[96:99]
	v_mfma_f32_16x16x32_bf16 v[84:87], v[146:149], v[186:189], v[84:87]
	v_mfma_f32_16x16x32_bf16 v[80:83], v[162:165], v[186:189], v[80:83]
	v_mfma_f32_16x16x32_bf16 v[68:71], v[146:149], v[194:197], v[68:71]
	v_mfma_f32_16x16x32_bf16 v[64:67], v[162:165], v[194:197], v[64:67]
	v_mfma_f32_16x16x32_bf16 v[116:119], v[156:159], v[174:177], v[116:119]
	v_mfma_f32_16x16x32_bf16 v[112:115], v[166:169], v[174:177], v[112:115]
	v_mfma_f32_16x16x32_bf16 v[100:103], v[156:159], v[182:185], v[100:103]
	v_mfma_f32_16x16x32_bf16 v[96:99], v[166:169], v[182:185], v[96:99]
	v_mfma_f32_16x16x32_bf16 v[84:87], v[156:159], v[190:193], v[84:87]
	v_mfma_f32_16x16x32_bf16 v[80:83], v[166:169], v[190:193], v[80:83]
	v_mfma_f32_16x16x32_bf16 v[68:71], v[156:159], v[198:201], v[68:71]
	v_mfma_f32_16x16x32_bf16 v[64:67], v[166:169], v[198:201], v[64:67]
	s_barrier
	s_add_i32 s2, s2, s31
	v_lshl_add_u64 v[204:205], v[150:151], 0, s[56:57]
	s_mov_b32 m0, s2
	ds_read_b128 v[170:173], v155 offset:49152
	ds_read_b128 v[174:177], v155 offset:50176
	ds_read_b128 v[178:181], v155 offset:51200
	ds_read_b128 v[182:185], v155 offset:52224
	ds_read_b128 v[186:189], v155 offset:53248
	ds_read_b128 v[190:193], v155 offset:54272
	ds_read_b128 v[194:197], v155 offset:55296
	ds_read_b128 v[198:201], v155 offset:56320
	global_load_lds_dwordx4 v[204:205], off
	v_lshl_add_u64 v[204:205], v[150:151], 0, s[64:65]
	s_add_i32 m0, s2, 0x2000
	s_add_i32 s2, s3, s31
	global_load_lds_dwordx4 v[204:205], off
	v_lshl_add_u64 v[204:205], v[150:151], 0, s[72:73]
	s_mov_b32 m0, s2
	v_lshl_add_u64 v[150:151], v[150:151], 0, s[86:87]
	global_load_lds_dwordx4 v[204:205], off
	s_add_i32 m0, s2, 0x2000
	s_nop 0
	global_load_lds_dwordx4 v[150:151], off
	v_lshl_add_u64 v[150:151], v[202:203], 0, s[56:57]
	s_mov_b32 m0, s51
	s_nop 0
	global_load_lds_dwordx4 v[150:151], off
	v_lshl_add_u64 v[150:151], v[202:203], 0, s[64:65]
	s_mov_b32 m0, s54
	s_nop 0
	global_load_lds_dwordx4 v[150:151], off
	s_waitcnt vmcnt(8)
	s_waitcnt lgkmcnt(0)
	s_barrier
	s_waitcnt lgkmcnt(0)
	v_mfma_f32_16x16x32_bf16 v[60:63], v[130:133], v[170:173], v[60:63]
	v_mfma_f32_16x16x32_bf16 v[56:59], v[138:141], v[170:173], v[56:59]
	v_mfma_f32_16x16x32_bf16 v[44:47], v[130:133], v[178:181], v[44:47]
	v_mfma_f32_16x16x32_bf16 v[40:43], v[138:141], v[178:181], v[40:43]
	v_mfma_f32_16x16x32_bf16 v[28:31], v[130:133], v[186:189], v[28:31]
	v_mfma_f32_16x16x32_bf16 v[24:27], v[138:141], v[186:189], v[24:27]
	v_mfma_f32_16x16x32_bf16 v[12:15], v[130:133], v[194:197], v[12:15]
	v_mfma_f32_16x16x32_bf16 v[8:11], v[138:141], v[194:197], v[8:11]
	v_mfma_f32_16x16x32_bf16 v[60:63], v[134:137], v[174:177], v[60:63]
	v_mfma_f32_16x16x32_bf16 v[56:59], v[142:145], v[174:177], v[56:59]
	v_mfma_f32_16x16x32_bf16 v[44:47], v[134:137], v[182:185], v[44:47]
	v_mfma_f32_16x16x32_bf16 v[40:43], v[142:145], v[182:185], v[40:43]
	v_mfma_f32_16x16x32_bf16 v[28:31], v[134:137], v[190:193], v[28:31]
	v_mfma_f32_16x16x32_bf16 v[24:27], v[142:145], v[190:193], v[24:27]
	v_mfma_f32_16x16x32_bf16 v[12:15], v[134:137], v[198:201], v[12:15]
	v_mfma_f32_16x16x32_bf16 v[8:11], v[142:145], v[198:201], v[8:11]
	v_mfma_f32_16x16x32_bf16 v[52:55], v[146:149], v[170:173], v[52:55]
	v_mfma_f32_16x16x32_bf16 v[48:51], v[162:165], v[170:173], v[48:51]
	v_mfma_f32_16x16x32_bf16 v[36:39], v[146:149], v[178:181], v[36:39]
	v_mfma_f32_16x16x32_bf16 v[32:35], v[162:165], v[178:181], v[32:35]
	v_mfma_f32_16x16x32_bf16 v[20:23], v[146:149], v[186:189], v[20:23]
	v_mfma_f32_16x16x32_bf16 v[16:19], v[162:165], v[186:189], v[16:19]
	v_mfma_f32_16x16x32_bf16 v[4:7], v[146:149], v[194:197], v[4:7]
	v_mfma_f32_16x16x32_bf16 v[0:3], v[162:165], v[194:197], v[0:3]
	v_mfma_f32_16x16x32_bf16 v[52:55], v[156:159], v[174:177], v[52:55]
	v_mfma_f32_16x16x32_bf16 v[48:51], v[166:169], v[174:177], v[48:51]
	v_mfma_f32_16x16x32_bf16 v[36:39], v[156:159], v[182:185], v[36:39]
	v_mfma_f32_16x16x32_bf16 v[32:35], v[166:169], v[182:185], v[32:35]
	v_mfma_f32_16x16x32_bf16 v[20:23], v[156:159], v[190:193], v[20:23]
	v_mfma_f32_16x16x32_bf16 v[16:19], v[166:169], v[190:193], v[16:19]
	v_mfma_f32_16x16x32_bf16 v[4:7], v[156:159], v[198:201], v[4:7]
	v_mfma_f32_16x16x32_bf16 v[0:3], v[166:169], v[198:201], v[0:3]
	s_barrier
	s_add_u32 s46, s46, 0x100
	s_addc_u32 s47, s47, 0
	s_add_u32 s22, s22, 0x100
	s_addc_u32 s23, s23, 0
	s_cmp_ge_i32 s77, s55
	s_mov_b32 s2, s77
	s_cbranch_scc0 .LBB0_1311

.LBB0_1536:
	ds_read_b128 v[20:23], v175
	ds_read_b128 v[24:27], v176
	ds_read_b128 v[16:19], v171
	ds_read_b128 v[0:3], v172
	ds_read_b128 v[28:31], v177
	ds_read_b128 v[4:7], v178
	ds_read_b128 v[8:11], v179
	ds_read_b128 v[12:15], v180
	s_add_i32 s34, s2, 2
	s_add_u32 s22, s38, 0xfffe0080
	s_addc_u32 s3, s39, -1
	s_cmp_eq_u32 s6, s2
	s_cselect_b32 s2, s49, s22
	s_cselect_b32 s3, s47, s3
	s_cselect_b32 s23, s51, vcc_hi
	s_cselect_b32 s22, s50, vcc_lo
	v_lshl_add_u64 v[166:167], s[38:39], 0, v[164:165]
	s_add_i32 m0, s75, 0xc000
	ds_read_b128 v[190:193], v188
	ds_read_b128 v[194:197], v188 offset:1024
	ds_read_b128 v[198:201], v188 offset:2048
	ds_read_b128 v[202:205], v188 offset:3072
	ds_read_b128 v[206:209], v188 offset:4096
	ds_read_b128 v[210:213], v188 offset:5120
	ds_read_b128 v[214:217], v188 offset:6144
	ds_read_b128 v[218:221], v188 offset:7168
	global_load_lds_dwordx4 v[166:167], off
	v_lshl_add_u64 v[166:167], v[166:167], 0, s[8:9]
	s_add_i32 m0, s75, 0xe000
	s_nop 0
	global_load_lds_dwordx4 v[166:167], off
	s_waitcnt vmcnt(8)
	s_waitcnt lgkmcnt(0)
	s_barrier
	s_waitcnt lgkmcnt(0)
	v_mfma_f32_16x16x128_f8f6f4 v[152:155], v[16:23], v[190:197], v[152:155]
	v_mfma_f32_16x16x128_f8f6f4 v[144:147], v[24:31], v[190:197], v[144:147]
	v_mfma_f32_16x16x128_f8f6f4 v[136:139], v[16:23], v[198:205], v[136:139]
	v_mfma_f32_16x16x128_f8f6f4 v[128:131], v[24:31], v[198:205], v[128:131]
	v_mfma_f32_16x16x128_f8f6f4 v[120:123], v[16:23], v[206:213], v[120:123]
	v_mfma_f32_16x16x128_f8f6f4 v[112:115], v[24:31], v[206:213], v[112:115]
	v_mfma_f32_16x16x128_f8f6f4 v[104:107], v[16:23], v[214:221], v[104:107]
	v_mfma_f32_16x16x128_f8f6f4 v[96:99], v[24:31], v[214:221], v[96:99]
	v_mfma_f32_16x16x128_f8f6f4 v[156:159], v[0:7], v[190:197], v[156:159]
	v_mfma_f32_16x16x128_f8f6f4 v[148:151], v[8:15], v[190:197], v[148:151]
	v_mfma_f32_16x16x128_f8f6f4 v[140:143], v[0:7], v[198:205], v[140:143]
	v_mfma_f32_16x16x128_f8f6f4 v[132:135], v[8:15], v[198:205], v[132:135]
	v_mfma_f32_16x16x128_f8f6f4 v[124:127], v[0:7], v[206:213], v[124:127]
	v_mfma_f32_16x16x128_f8f6f4 v[116:119], v[8:15], v[206:213], v[116:119]
	v_mfma_f32_16x16x128_f8f6f4 v[108:111], v[0:7], v[214:221], v[108:111]
	v_mfma_f32_16x16x128_f8f6f4 v[100:103], v[8:15], v[214:221], v[100:103]
	s_barrier
	s_mov_b32 m0, s78
	v_lshl_add_u64 v[166:167], s[22:23], 0, v[160:161]
	ds_read_b128 v[190:193], v188 offset:16384
	ds_read_b128 v[194:197], v188 offset:17408
	ds_read_b128 v[198:201], v188 offset:18432
	ds_read_b128 v[202:205], v188 offset:19456
	ds_read_b128 v[206:209], v188 offset:20480
	ds_read_b128 v[210:213], v188 offset:21504
	ds_read_b128 v[214:217], v188 offset:22528
	ds_read_b128 v[218:221], v188 offset:23552
	global_load_lds_dwordx4 v[166:167], off
	v_lshl_add_u64 v[168:169], v[166:167], 0, s[8:9]
	s_mov_b32 m0, s79
	s_nop 0
	global_load_lds_dwordx4 v[168:169], off
	v_lshl_add_u64 v[168:169], v[166:167], 0, s[14:15]
	s_mov_b32 m0, s80
	s_nop 0
	global_load_lds_dwordx4 v[168:169], off
	v_lshl_add_u64 v[168:169], v[166:167], 0, s[16:17]
	s_mov_b32 m0, s81
	s_nop 0
	global_load_lds_dwordx4 v[168:169], off
	v_lshl_add_u64 v[168:169], s[2:3], 0, v[162:163]
	s_mov_b32 m0, s75
	v_lshl_add_u64 v[222:223], v[168:169], 0, s[8:9]
	global_load_lds_dwordx4 v[168:169], off
	s_mov_b32 m0, s83
	s_nop 0
	global_load_lds_dwordx4 v[222:223], off
	s_waitcnt vmcnt(8)
	s_waitcnt lgkmcnt(0)
	s_barrier
	s_waitcnt lgkmcnt(0)
	v_mfma_f32_16x16x128_f8f6f4 v[88:91], v[16:23], v[190:197], v[88:91]
	v_mfma_f32_16x16x128_f8f6f4 v[80:83], v[24:31], v[190:197], v[80:83]
	v_mfma_f32_16x16x128_f8f6f4 v[72:75], v[16:23], v[198:205], v[72:75]
	v_mfma_f32_16x16x128_f8f6f4 v[64:67], v[24:31], v[198:205], v[64:67]
	v_mfma_f32_16x16x128_f8f6f4 v[56:59], v[16:23], v[206:213], v[56:59]
	v_mfma_f32_16x16x128_f8f6f4 v[48:51], v[24:31], v[206:213], v[48:51]
	v_mfma_f32_16x16x128_f8f6f4 v[36:39], v[16:23], v[214:221], v[36:39]
	v_mfma_f32_16x16x128_f8f6f4 v[32:35], v[24:31], v[214:221], v[32:35]
	v_mfma_f32_16x16x128_f8f6f4 v[92:95], v[0:7], v[190:197], v[92:95]
	v_mfma_f32_16x16x128_f8f6f4 v[84:87], v[8:15], v[190:197], v[84:87]
	v_mfma_f32_16x16x128_f8f6f4 v[76:79], v[0:7], v[198:205], v[76:79]
	v_mfma_f32_16x16x128_f8f6f4 v[68:71], v[8:15], v[198:205], v[68:71]
	v_mfma_f32_16x16x128_f8f6f4 v[60:63], v[0:7], v[206:213], v[60:63]
	v_mfma_f32_16x16x128_f8f6f4 v[52:55], v[8:15], v[206:213], v[52:55]
	v_mfma_f32_16x16x128_f8f6f4 v[40:43], v[0:7], v[214:221], v[40:43]
	v_mfma_f32_16x16x128_f8f6f4 v[44:47], v[8:15], v[214:221], v[44:47]
	s_barrier
	ds_read_b128 v[4:7], v181
	ds_read_b128 v[8:11], v182
	ds_read_b128 v[0:3], v173
	ds_read_b128 v[16:19], v174
	ds_read_b128 v[12:15], v183
	ds_read_b128 v[20:23], v184
	ds_read_b128 v[24:27], v185
	ds_read_b128 v[28:31], v186
	s_mov_b32 m0, s86
	v_lshl_add_u64 v[222:223], v[168:169], 0, s[14:15]
	ds_read_b128 v[190:193], v188 offset:32768
	ds_read_b128 v[194:197], v188 offset:33792
	ds_read_b128 v[198:201], v188 offset:34816
	ds_read_b128 v[202:205], v188 offset:35840
	ds_read_b128 v[206:209], v188 offset:36864
	ds_read_b128 v[210:213], v188 offset:37888
	ds_read_b128 v[214:217], v188 offset:38912
	ds_read_b128 v[218:221], v188 offset:39936
	global_load_lds_dwordx4 v[222:223], off
	v_lshl_add_u64 v[222:223], v[168:169], 0, s[16:17]
	s_mov_b32 m0, s87
	s_nop 0
	global_load_lds_dwordx4 v[222:223], off
	s_waitcnt vmcnt(8)
	s_waitcnt lgkmcnt(0)
	s_barrier
	s_waitcnt lgkmcnt(0)
	v_mfma_f32_16x16x128_f8f6f4 v[152:155], v[0:7], v[190:197], v[152:155]
	v_mfma_f32_16x16x128_f8f6f4 v[144:147], v[8:15], v[190:197], v[144:147]
	v_mfma_f32_16x16x128_f8f6f4 v[136:139], v[0:7], v[198:205], v[136:139]
	v_mfma_f32_16x16x128_f8f6f4 v[128:131], v[8:15], v[198:205], v[128:131]
	v_mfma_f32_16x16x128_f8f6f4 v[120:123], v[0:7], v[206:213], v[120:123]
	v_mfma_f32_16x16x128_f8f6f4 v[112:115], v[8:15], v[206:213], v[112:115]
	v_mfma_f32_16x16x128_f8f6f4 v[104:107], v[0:7], v[214:221], v[104:107]
	v_mfma_f32_16x16x128_f8f6f4 v[96:99], v[8:15], v[214:221], v[96:99]
	v_mfma_f32_16x16x128_f8f6f4 v[156:159], v[16:23], v[190:197], v[156:159]
	v_mfma_f32_16x16x128_f8f6f4 v[148:151], v[24:31], v[190:197], v[148:151]
	v_mfma_f32_16x16x128_f8f6f4 v[140:143], v[16:23], v[198:205], v[140:143]
	v_mfma_f32_16x16x128_f8f6f4 v[132:135], v[24:31], v[198:205], v[132:135]
	v_mfma_f32_16x16x128_f8f6f4 v[124:127], v[16:23], v[206:213], v[124:127]
	v_mfma_f32_16x16x128_f8f6f4 v[116:119], v[24:31], v[206:213], v[116:119]
	v_mfma_f32_16x16x128_f8f6f4 v[108:111], v[16:23], v[214:221], v[108:111]
	v_mfma_f32_16x16x128_f8f6f4 v[100:103], v[24:31], v[214:221], v[100:103]
	s_barrier
	s_mov_b32 m0, s91
	v_lshl_add_u64 v[222:223], v[166:167], 0, s[56:57]
	ds_read_b128 v[190:193], v188 offset:49152
	ds_read_b128 v[194:197], v188 offset:50176
	ds_read_b128 v[198:201], v188 offset:51200
	ds_read_b128 v[202:205], v188 offset:52224
	ds_read_b128 v[206:209], v188 offset:53248
	ds_read_b128 v[210:213], v188 offset:54272
	ds_read_b128 v[214:217], v188 offset:55296
	ds_read_b128 v[218:221], v188 offset:56320
	global_load_lds_dwordx4 v[222:223], off
	v_lshl_add_u64 v[222:223], v[166:167], 0, s[28:29]
	s_mov_b32 m0, s92
	s_nop 0
	global_load_lds_dwordx4 v[222:223], off
	v_lshl_add_u64 v[222:223], v[166:167], 0, s[0:1]
	s_mov_b32 m0, s11
	v_lshl_add_u64 v[166:167], v[166:167], 0, s[4:5]
	global_load_lds_dwordx4 v[222:223], off
	s_mov_b32 m0, s31
	s_nop 0
	global_load_lds_dwordx4 v[166:167], off
	v_lshl_add_u64 v[166:167], v[168:169], 0, s[56:57]
	s_mov_b32 m0, s93
	s_nop 0
	global_load_lds_dwordx4 v[166:167], off
	v_lshl_add_u64 v[166:167], v[168:169], 0, s[28:29]
	s_mov_b32 m0, s95
	s_nop 0
	global_load_lds_dwordx4 v[166:167], off
	s_waitcnt vmcnt(8)
	s_waitcnt lgkmcnt(0)
	s_barrier
	s_waitcnt lgkmcnt(0)
	v_mfma_f32_16x16x128_f8f6f4 v[88:91], v[0:7], v[190:197], v[88:91]
	v_mfma_f32_16x16x128_f8f6f4 v[80:83], v[8:15], v[190:197], v[80:83]
	v_mfma_f32_16x16x128_f8f6f4 v[72:75], v[0:7], v[198:205], v[72:75]
	v_mfma_f32_16x16x128_f8f6f4 v[64:67], v[8:15], v[198:205], v[64:67]
	v_mfma_f32_16x16x128_f8f6f4 v[56:59], v[0:7], v[206:213], v[56:59]
	v_mfma_f32_16x16x128_f8f6f4 v[48:51], v[8:15], v[206:213], v[48:51]
	v_mfma_f32_16x16x128_f8f6f4 v[36:39], v[0:7], v[214:221], v[36:39]
	v_mfma_f32_16x16x128_f8f6f4 v[32:35], v[8:15], v[214:221], v[32:35]
	v_mfma_f32_16x16x128_f8f6f4 v[92:95], v[16:23], v[190:197], v[92:95]
	v_mfma_f32_16x16x128_f8f6f4 v[84:87], v[24:31], v[190:197], v[84:87]
	v_mfma_f32_16x16x128_f8f6f4 v[76:79], v[16:23], v[198:205], v[76:79]
	v_mfma_f32_16x16x128_f8f6f4 v[68:71], v[24:31], v[198:205], v[68:71]
	v_mfma_f32_16x16x128_f8f6f4 v[60:63], v[16:23], v[206:213], v[60:63]
	v_mfma_f32_16x16x128_f8f6f4 v[52:55], v[24:31], v[206:213], v[52:55]
	v_mfma_f32_16x16x128_f8f6f4 v[40:43], v[16:23], v[214:221], v[40:43]
	v_mfma_f32_16x16x128_f8f6f4 v[44:47], v[24:31], v[214:221], v[44:47]
	s_barrier
	s_add_u32 vcc_lo, vcc_lo, 0x100
	s_addc_u32 vcc_hi, vcc_hi, 0
	s_add_u32 s38, s38, 0x100
	s_addc_u32 s39, s39, 0
	s_cmp_ge_i32 s34, s10
	s_mov_b32 s2, s34
	s_cbranch_scc0 .LBB0_1536

.LBB0_1619:
	ds_read_b128 v[20:23], v175
	ds_read_b128 v[24:27], v176
	ds_read_b128 v[16:19], v171
	ds_read_b128 v[0:3], v172
	ds_read_b128 v[28:31], v177
	ds_read_b128 v[4:7], v178
	ds_read_b128 v[8:11], v179
	ds_read_b128 v[12:15], v180
	s_add_i32 s6, s2, 2
	s_add_u32 s22, s48, 0xfff90080
	s_addc_u32 s3, s49, -1
	s_cmp_eq_u32 s91, s2
	s_cselect_b32 s2, s38, s22
	s_cselect_b32 s3, s39, s3
	s_cselect_b32 s23, s47, vcc_hi
	s_cselect_b32 s22, s46, vcc_lo
	v_lshl_add_u64 v[166:167], s[48:49], 0, v[164:165]
	s_add_i32 m0, s55, 0xc000
	ds_read_b128 v[190:193], v188
	ds_read_b128 v[194:197], v188 offset:1024
	ds_read_b128 v[198:201], v188 offset:2048
	ds_read_b128 v[202:205], v188 offset:3072
	ds_read_b128 v[206:209], v188 offset:4096
	ds_read_b128 v[210:213], v188 offset:5120
	ds_read_b128 v[214:217], v188 offset:6144
	ds_read_b128 v[218:221], v188 offset:7168
	global_load_lds_dwordx4 v[166:167], off
	v_lshl_add_u64 v[166:167], v[166:167], 0, s[20:21]
	s_add_i32 m0, s55, 0xe000
	s_nop 0
	global_load_lds_dwordx4 v[166:167], off
	s_waitcnt vmcnt(8)
	s_waitcnt lgkmcnt(0)
	s_barrier
	s_waitcnt lgkmcnt(0)
	v_mfma_f32_16x16x128_f8f6f4 v[156:159], v[16:23], v[190:197], v[156:159]
	v_mfma_f32_16x16x128_f8f6f4 v[152:155], v[24:31], v[190:197], v[152:155]
	v_mfma_f32_16x16x128_f8f6f4 v[148:151], v[16:23], v[198:205], v[148:151]
	v_mfma_f32_16x16x128_f8f6f4 v[144:147], v[24:31], v[198:205], v[144:147]
	v_mfma_f32_16x16x128_f8f6f4 v[136:139], v[16:23], v[206:213], v[136:139]
	v_mfma_f32_16x16x128_f8f6f4 v[128:131], v[24:31], v[206:213], v[128:131]
	v_mfma_f32_16x16x128_f8f6f4 v[120:123], v[16:23], v[214:221], v[120:123]
	v_mfma_f32_16x16x128_f8f6f4 v[112:115], v[24:31], v[214:221], v[112:115]
	v_mfma_f32_16x16x128_f8f6f4 v[140:143], v[0:7], v[190:197], v[140:143]
	v_mfma_f32_16x16x128_f8f6f4 v[132:135], v[8:15], v[190:197], v[132:135]
	v_mfma_f32_16x16x128_f8f6f4 v[124:127], v[0:7], v[198:205], v[124:127]
	v_mfma_f32_16x16x128_f8f6f4 v[116:119], v[8:15], v[198:205], v[116:119]
	v_mfma_f32_16x16x128_f8f6f4 v[108:111], v[0:7], v[206:213], v[108:111]
	v_mfma_f32_16x16x128_f8f6f4 v[104:107], v[8:15], v[206:213], v[104:107]
	v_mfma_f32_16x16x128_f8f6f4 v[100:103], v[0:7], v[214:221], v[100:103]
	v_mfma_f32_16x16x128_f8f6f4 v[96:99], v[8:15], v[214:221], v[96:99]
	s_barrier
	s_mov_b32 m0, s58
	v_lshl_add_u64 v[166:167], s[22:23], 0, v[160:161]
	ds_read_b128 v[190:193], v188 offset:16384
	ds_read_b128 v[194:197], v188 offset:17408
	ds_read_b128 v[198:201], v188 offset:18432
	ds_read_b128 v[202:205], v188 offset:19456
	ds_read_b128 v[206:209], v188 offset:20480
	ds_read_b128 v[210:213], v188 offset:21504
	ds_read_b128 v[214:217], v188 offset:22528
	ds_read_b128 v[218:221], v188 offset:23552
	global_load_lds_dwordx4 v[166:167], off
	v_lshl_add_u64 v[168:169], v[166:167], 0, s[20:21]
	s_mov_b32 m0, s59
	s_nop 0
	global_load_lds_dwordx4 v[168:169], off
	v_lshl_add_u64 v[168:169], v[166:167], 0, s[84:85]
	s_mov_b32 m0, s63
	s_nop 0
	global_load_lds_dwordx4 v[168:169], off
	v_lshl_add_u64 v[168:169], v[166:167], 0, s[12:13]
	s_mov_b32 m0, s74
	s_nop 0
	global_load_lds_dwordx4 v[168:169], off
	v_lshl_add_u64 v[168:169], s[2:3], 0, v[162:163]
	s_mov_b32 m0, s55
	v_lshl_add_u64 v[222:223], v[168:169], 0, s[20:21]
	global_load_lds_dwordx4 v[168:169], off
	s_mov_b32 m0, s75
	s_nop 0
	global_load_lds_dwordx4 v[222:223], off
	s_waitcnt vmcnt(8)
	s_waitcnt lgkmcnt(0)
	s_barrier
	s_waitcnt lgkmcnt(0)
	v_mfma_f32_16x16x128_f8f6f4 v[92:95], v[16:23], v[190:197], v[92:95]
	v_mfma_f32_16x16x128_f8f6f4 v[88:91], v[24:31], v[190:197], v[88:91]
	v_mfma_f32_16x16x128_f8f6f4 v[76:79], v[16:23], v[198:205], v[76:79]
	v_mfma_f32_16x16x128_f8f6f4 v[72:75], v[24:31], v[198:205], v[72:75]
	v_mfma_f32_16x16x128_f8f6f4 v[60:63], v[16:23], v[206:213], v[60:63]
	v_mfma_f32_16x16x128_f8f6f4 v[56:59], v[24:31], v[206:213], v[56:59]
	v_mfma_f32_16x16x128_f8f6f4 v[44:47], v[16:23], v[214:221], v[44:47]
	v_mfma_f32_16x16x128_f8f6f4 v[40:43], v[24:31], v[214:221], v[40:43]
	v_mfma_f32_16x16x128_f8f6f4 v[84:87], v[0:7], v[190:197], v[84:87]
	v_mfma_f32_16x16x128_f8f6f4 v[80:83], v[8:15], v[190:197], v[80:83]
	v_mfma_f32_16x16x128_f8f6f4 v[68:71], v[0:7], v[198:205], v[68:71]
	v_mfma_f32_16x16x128_f8f6f4 v[64:67], v[8:15], v[198:205], v[64:67]
	v_mfma_f32_16x16x128_f8f6f4 v[52:55], v[0:7], v[206:213], v[52:55]
	v_mfma_f32_16x16x128_f8f6f4 v[48:51], v[8:15], v[206:213], v[48:51]
	v_mfma_f32_16x16x128_f8f6f4 v[36:39], v[0:7], v[214:221], v[36:39]
	v_mfma_f32_16x16x128_f8f6f4 v[32:35], v[8:15], v[214:221], v[32:35]
	s_barrier
	ds_read_b128 v[4:7], v181
	ds_read_b128 v[8:11], v182
	ds_read_b128 v[0:3], v173
	ds_read_b128 v[16:19], v174
	ds_read_b128 v[12:15], v183
	ds_read_b128 v[20:23], v184
	ds_read_b128 v[24:27], v185
	ds_read_b128 v[28:31], v186
	s_mov_b32 m0, s77
	v_lshl_add_u64 v[222:223], v[168:169], 0, s[84:85]
	ds_read_b128 v[190:193], v188 offset:32768
	ds_read_b128 v[194:197], v188 offset:33792
	ds_read_b128 v[198:201], v188 offset:34816
	ds_read_b128 v[202:205], v188 offset:35840
	ds_read_b128 v[206:209], v188 offset:36864
	ds_read_b128 v[210:213], v188 offset:37888
	ds_read_b128 v[214:217], v188 offset:38912
	ds_read_b128 v[218:221], v188 offset:39936
	global_load_lds_dwordx4 v[222:223], off
	v_lshl_add_u64 v[222:223], v[168:169], 0, s[12:13]
	s_mov_b32 m0, s78
	s_nop 0
	global_load_lds_dwordx4 v[222:223], off
	s_waitcnt vmcnt(8)
	s_waitcnt lgkmcnt(0)
	s_barrier
	s_waitcnt lgkmcnt(0)
	v_mfma_f32_16x16x128_f8f6f4 v[156:159], v[0:7], v[190:197], v[156:159]
	v_mfma_f32_16x16x128_f8f6f4 v[152:155], v[8:15], v[190:197], v[152:155]
	v_mfma_f32_16x16x128_f8f6f4 v[148:151], v[0:7], v[198:205], v[148:151]
	v_mfma_f32_16x16x128_f8f6f4 v[144:147], v[8:15], v[198:205], v[144:147]
	v_mfma_f32_16x16x128_f8f6f4 v[136:139], v[0:7], v[206:213], v[136:139]
	v_mfma_f32_16x16x128_f8f6f4 v[128:131], v[8:15], v[206:213], v[128:131]
	v_mfma_f32_16x16x128_f8f6f4 v[120:123], v[0:7], v[214:221], v[120:123]
	v_mfma_f32_16x16x128_f8f6f4 v[112:115], v[8:15], v[214:221], v[112:115]
	v_mfma_f32_16x16x128_f8f6f4 v[140:143], v[16:23], v[190:197], v[140:143]
	v_mfma_f32_16x16x128_f8f6f4 v[132:135], v[24:31], v[190:197], v[132:135]
	v_mfma_f32_16x16x128_f8f6f4 v[124:127], v[16:23], v[198:205], v[124:127]
	v_mfma_f32_16x16x128_f8f6f4 v[116:119], v[24:31], v[198:205], v[116:119]
	v_mfma_f32_16x16x128_f8f6f4 v[108:111], v[16:23], v[206:213], v[108:111]
	v_mfma_f32_16x16x128_f8f6f4 v[104:107], v[24:31], v[206:213], v[104:107]
	v_mfma_f32_16x16x128_f8f6f4 v[100:103], v[16:23], v[214:221], v[100:103]
	v_mfma_f32_16x16x128_f8f6f4 v[96:99], v[24:31], v[214:221], v[96:99]
	s_barrier
	s_mov_b32 m0, s79
	v_lshl_add_u64 v[222:223], v[166:167], 0, s[56:57]
	ds_read_b128 v[190:193], v188 offset:49152
	ds_read_b128 v[194:197], v188 offset:50176
	ds_read_b128 v[198:201], v188 offset:51200
	ds_read_b128 v[202:205], v188 offset:52224
	ds_read_b128 v[206:209], v188 offset:53248
	ds_read_b128 v[210:213], v188 offset:54272
	ds_read_b128 v[214:217], v188 offset:55296
	ds_read_b128 v[218:221], v188 offset:56320
	global_load_lds_dwordx4 v[222:223], off
	v_lshl_add_u64 v[222:223], v[166:167], 0, s[64:65]
	s_mov_b32 m0, s80
	s_nop 0
	global_load_lds_dwordx4 v[222:223], off
	v_lshl_add_u64 v[222:223], v[166:167], 0, s[4:5]
	s_mov_b32 m0, s86
	v_lshl_add_u64 v[166:167], v[166:167], 0, s[72:73]
	global_load_lds_dwordx4 v[222:223], off
	s_mov_b32 m0, s87
	s_nop 0
	global_load_lds_dwordx4 v[166:167], off
	v_lshl_add_u64 v[166:167], v[168:169], 0, s[56:57]
	s_mov_b32 m0, s81
	s_nop 0
	global_load_lds_dwordx4 v[166:167], off
	v_lshl_add_u64 v[166:167], v[168:169], 0, s[64:65]
	s_mov_b32 m0, s83
	s_nop 0
	global_load_lds_dwordx4 v[166:167], off
	s_waitcnt vmcnt(8)
	s_waitcnt lgkmcnt(0)
	s_barrier
	s_waitcnt lgkmcnt(0)
	v_mfma_f32_16x16x128_f8f6f4 v[92:95], v[0:7], v[190:197], v[92:95]
	v_mfma_f32_16x16x128_f8f6f4 v[88:91], v[8:15], v[190:197], v[88:91]
	v_mfma_f32_16x16x128_f8f6f4 v[76:79], v[0:7], v[198:205], v[76:79]
	v_mfma_f32_16x16x128_f8f6f4 v[72:75], v[8:15], v[198:205], v[72:75]
	v_mfma_f32_16x16x128_f8f6f4 v[60:63], v[0:7], v[206:213], v[60:63]
	v_mfma_f32_16x16x128_f8f6f4 v[56:59], v[8:15], v[206:213], v[56:59]
	v_mfma_f32_16x16x128_f8f6f4 v[44:47], v[0:7], v[214:221], v[44:47]
	v_mfma_f32_16x16x128_f8f6f4 v[40:43], v[8:15], v[214:221], v[40:43]
	v_mfma_f32_16x16x128_f8f6f4 v[84:87], v[16:23], v[190:197], v[84:87]
	v_mfma_f32_16x16x128_f8f6f4 v[80:83], v[24:31], v[190:197], v[80:83]
	v_mfma_f32_16x16x128_f8f6f4 v[68:71], v[16:23], v[198:205], v[68:71]
	v_mfma_f32_16x16x128_f8f6f4 v[64:67], v[24:31], v[198:205], v[64:67]
	v_mfma_f32_16x16x128_f8f6f4 v[52:55], v[16:23], v[206:213], v[52:55]
	v_mfma_f32_16x16x128_f8f6f4 v[48:51], v[24:31], v[206:213], v[48:51]
	v_mfma_f32_16x16x128_f8f6f4 v[36:39], v[16:23], v[214:221], v[36:39]
	v_mfma_f32_16x16x128_f8f6f4 v[32:35], v[24:31], v[214:221], v[32:35]
	s_barrier
	s_add_u32 vcc_lo, vcc_lo, 0x100
	s_addc_u32 vcc_hi, vcc_hi, 0
	s_add_u32 s48, s48, 0x100
	s_addc_u32 s49, s49, 0
	s_cmp_ge_i32 s6, s90
	s_mov_b32 s2, s6
	s_cbranch_scc0 .LBB0_1619
	v_pk_mul_f32 v[6:7], v[158:159], s[30:31] op_sel_hi:[1,0]
	v_pk_mul_f32 v[16:17], v[156:157], s[30:31] op_sel_hi:[1,0]
	v_pk_mul_f32 v[22:23], v[154:155], s[30:31] op_sel_hi:[1,0]
	v_pk_mul_f32 v[30:31], v[152:153], s[30:31] op_sel_hi:[1,0]
	v_pk_mul_f32 v[142:143], v[142:143], s[30:31] op_sel_hi:[1,0]
	v_pk_mul_f32 v[140:141], v[140:141], s[30:31] op_sel_hi:[1,0]
	v_pk_mul_f32 v[134:135], v[134:135], s[30:31] op_sel_hi:[1,0]
	v_pk_mul_f32 v[132:133], v[132:133], s[30:31] op_sel_hi:[1,0]
	v_pk_mul_f32 v[4:5], v[150:151], s[30:31] op_sel_hi:[1,0]
	v_pk_mul_f32 v[12:13], v[148:149], s[30:31] op_sel_hi:[1,0]
	v_pk_mul_f32 v[20:21], v[146:147], s[30:31] op_sel_hi:[1,0]
	v_pk_mul_f32 v[28:29], v[144:145], s[30:31] op_sel_hi:[1,0]
	v_pk_mul_f32 v[126:127], v[126:127], s[30:31] op_sel_hi:[1,0]
	v_pk_mul_f32 v[124:125], v[124:125], s[30:31] op_sel_hi:[1,0]
	v_pk_mul_f32 v[118:119], v[118:119], s[30:31] op_sel_hi:[1,0]
	v_pk_mul_f32 v[116:117], v[116:117], s[30:31] op_sel_hi:[1,0]
	v_pk_mul_f32 v[2:3], v[138:139], s[30:31] op_sel_hi:[1,0]
	v_pk_mul_f32 v[10:11], v[136:137], s[30:31] op_sel_hi:[1,0]
	v_pk_mul_f32 v[18:19], v[130:131], s[30:31] op_sel_hi:[1,0]
	v_pk_mul_f32 v[26:27], v[128:129], s[30:31] op_sel_hi:[1,0]
	v_pk_mul_f32 v[110:111], v[110:111], s[30:31] op_sel_hi:[1,0]
	v_pk_mul_f32 v[108:109], v[108:109], s[30:31] op_sel_hi:[1,0]
	v_pk_mul_f32 v[106:107], v[106:107], s[30:31] op_sel_hi:[1,0]
	v_pk_mul_f32 v[104:105], v[104:105], s[30:31] op_sel_hi:[1,0]
	v_pk_mul_f32 v[0:1], v[122:123], s[30:31] op_sel_hi:[1,0]
	v_pk_mul_f32 v[8:9], v[120:121], s[30:31] op_sel_hi:[1,0]
	v_pk_mul_f32 v[14:15], v[114:115], s[30:31] op_sel_hi:[1,0]
	v_pk_mul_f32 v[24:25], v[112:113], s[30:31] op_sel_hi:[1,0]
	v_pk_mul_f32 v[102:103], v[102:103], s[30:31] op_sel_hi:[1,0]
	v_pk_mul_f32 v[100:101], v[100:101], s[30:31] op_sel_hi:[1,0]
	v_pk_mul_f32 v[98:99], v[98:99], s[30:31] op_sel_hi:[1,0]
	v_pk_mul_f32 v[96:97], v[96:97], s[30:31] op_sel_hi:[1,0]

.LBB0_1705:
	ds_read_b128 v[20:23], v175
	ds_read_b128 v[24:27], v176
	ds_read_b128 v[16:19], v171
	ds_read_b128 v[0:3], v172
	ds_read_b128 v[28:31], v177
	ds_read_b128 v[4:7], v178
	ds_read_b128 v[8:11], v179
	ds_read_b128 v[12:15], v180
	s_add_i32 s18, s2, 2
	s_add_u32 s19, s38, 0xfffe0080
	s_addc_u32 s3, s39, -1
	s_cmp_eq_u32 s7, s2
	s_cselect_b32 s2, s51, s19
	s_cselect_b32 s3, s49, s3
	s_cselect_b32 s23, s55, vcc_hi
	s_cselect_b32 s22, s54, vcc_lo
	v_lshl_add_u64 v[166:167], s[38:39], 0, v[164:165]
	s_add_i32 m0, s77, 0xc000
	ds_read_b128 v[190:193], v188
	ds_read_b128 v[194:197], v188 offset:1024
	ds_read_b128 v[198:201], v188 offset:2048
	ds_read_b128 v[202:205], v188 offset:3072
	ds_read_b128 v[206:209], v188 offset:4096
	ds_read_b128 v[210:213], v188 offset:5120
	ds_read_b128 v[214:217], v188 offset:6144
	ds_read_b128 v[218:221], v188 offset:7168
	global_load_lds_dwordx4 v[166:167], off
	v_lshl_add_u64 v[166:167], v[166:167], 0, s[8:9]
	s_add_i32 m0, s77, 0xe000
	s_nop 0
	global_load_lds_dwordx4 v[166:167], off
	s_waitcnt vmcnt(8)
	s_waitcnt lgkmcnt(0)
	s_barrier
	s_waitcnt lgkmcnt(0)
	v_mfma_f32_16x16x128_f8f6f4 v[152:155], v[16:23], v[190:197], v[152:155]
	v_mfma_f32_16x16x128_f8f6f4 v[144:147], v[24:31], v[190:197], v[144:147]
	v_mfma_f32_16x16x128_f8f6f4 v[136:139], v[16:23], v[198:205], v[136:139]
	v_mfma_f32_16x16x128_f8f6f4 v[128:131], v[24:31], v[198:205], v[128:131]
	v_mfma_f32_16x16x128_f8f6f4 v[120:123], v[16:23], v[206:213], v[120:123]
	v_mfma_f32_16x16x128_f8f6f4 v[112:115], v[24:31], v[206:213], v[112:115]
	v_mfma_f32_16x16x128_f8f6f4 v[104:107], v[16:23], v[214:221], v[104:107]
	v_mfma_f32_16x16x128_f8f6f4 v[96:99], v[24:31], v[214:221], v[96:99]
	v_mfma_f32_16x16x128_f8f6f4 v[156:159], v[0:7], v[190:197], v[156:159]
	v_mfma_f32_16x16x128_f8f6f4 v[148:151], v[8:15], v[190:197], v[148:151]
	v_mfma_f32_16x16x128_f8f6f4 v[140:143], v[0:7], v[198:205], v[140:143]
	v_mfma_f32_16x16x128_f8f6f4 v[132:135], v[8:15], v[198:205], v[132:135]
	v_mfma_f32_16x16x128_f8f6f4 v[124:127], v[0:7], v[206:213], v[124:127]
	v_mfma_f32_16x16x128_f8f6f4 v[116:119], v[8:15], v[206:213], v[116:119]
	v_mfma_f32_16x16x128_f8f6f4 v[108:111], v[0:7], v[214:221], v[108:111]
	v_mfma_f32_16x16x128_f8f6f4 v[100:103], v[8:15], v[214:221], v[100:103]
	s_barrier
	s_mov_b32 m0, s78
	v_lshl_add_u64 v[166:167], s[22:23], 0, v[160:161]
	ds_read_b128 v[190:193], v188 offset:16384
	ds_read_b128 v[194:197], v188 offset:17408
	ds_read_b128 v[198:201], v188 offset:18432
	ds_read_b128 v[202:205], v188 offset:19456
	ds_read_b128 v[206:209], v188 offset:20480
	ds_read_b128 v[210:213], v188 offset:21504
	ds_read_b128 v[214:217], v188 offset:22528
	ds_read_b128 v[218:221], v188 offset:23552
	global_load_lds_dwordx4 v[166:167], off
	v_lshl_add_u64 v[168:169], v[166:167], 0, s[8:9]
	s_mov_b32 m0, s79
	s_nop 0
	global_load_lds_dwordx4 v[168:169], off
	v_lshl_add_u64 v[168:169], v[166:167], 0, s[14:15]
	s_mov_b32 m0, s80
	s_nop 0
	global_load_lds_dwordx4 v[168:169], off
	v_lshl_add_u64 v[168:169], v[166:167], 0, s[16:17]
	s_mov_b32 m0, s81
	s_nop 0
	global_load_lds_dwordx4 v[168:169], off
	v_lshl_add_u64 v[168:169], s[2:3], 0, v[162:163]
	s_mov_b32 m0, s77
	v_lshl_add_u64 v[222:223], v[168:169], 0, s[8:9]
	global_load_lds_dwordx4 v[168:169], off
	s_mov_b32 m0, s83
	s_nop 0
	global_load_lds_dwordx4 v[222:223], off
	s_waitcnt vmcnt(8)
	s_waitcnt lgkmcnt(0)
	s_barrier
	s_waitcnt lgkmcnt(0)
	v_mfma_f32_16x16x128_f8f6f4 v[88:91], v[16:23], v[190:197], v[88:91]
	v_mfma_f32_16x16x128_f8f6f4 v[80:83], v[24:31], v[190:197], v[80:83]
	v_mfma_f32_16x16x128_f8f6f4 v[72:75], v[16:23], v[198:205], v[72:75]
	v_mfma_f32_16x16x128_f8f6f4 v[64:67], v[24:31], v[198:205], v[64:67]
	v_mfma_f32_16x16x128_f8f6f4 v[56:59], v[16:23], v[206:213], v[56:59]
	v_mfma_f32_16x16x128_f8f6f4 v[48:51], v[24:31], v[206:213], v[48:51]
	v_mfma_f32_16x16x128_f8f6f4 v[36:39], v[16:23], v[214:221], v[36:39]
	v_mfma_f32_16x16x128_f8f6f4 v[32:35], v[24:31], v[214:221], v[32:35]
	v_mfma_f32_16x16x128_f8f6f4 v[92:95], v[0:7], v[190:197], v[92:95]
	v_mfma_f32_16x16x128_f8f6f4 v[84:87], v[8:15], v[190:197], v[84:87]
	v_mfma_f32_16x16x128_f8f6f4 v[76:79], v[0:7], v[198:205], v[76:79]
	v_mfma_f32_16x16x128_f8f6f4 v[68:71], v[8:15], v[198:205], v[68:71]
	v_mfma_f32_16x16x128_f8f6f4 v[60:63], v[0:7], v[206:213], v[60:63]
	v_mfma_f32_16x16x128_f8f6f4 v[52:55], v[8:15], v[206:213], v[52:55]
	v_mfma_f32_16x16x128_f8f6f4 v[40:43], v[0:7], v[214:221], v[40:43]
	v_mfma_f32_16x16x128_f8f6f4 v[44:47], v[8:15], v[214:221], v[44:47]
	s_barrier
	ds_read_b128 v[4:7], v181
	ds_read_b128 v[8:11], v182
	ds_read_b128 v[0:3], v173
	ds_read_b128 v[16:19], v174
	ds_read_b128 v[12:15], v183
	ds_read_b128 v[20:23], v184
	ds_read_b128 v[24:27], v185
	ds_read_b128 v[28:31], v186
	s_mov_b32 m0, s86
	v_lshl_add_u64 v[222:223], v[168:169], 0, s[14:15]
	ds_read_b128 v[190:193], v188 offset:32768
	ds_read_b128 v[194:197], v188 offset:33792
	ds_read_b128 v[198:201], v188 offset:34816
	ds_read_b128 v[202:205], v188 offset:35840
	ds_read_b128 v[206:209], v188 offset:36864
	ds_read_b128 v[210:213], v188 offset:37888
	ds_read_b128 v[214:217], v188 offset:38912
	ds_read_b128 v[218:221], v188 offset:39936
	global_load_lds_dwordx4 v[222:223], off
	v_lshl_add_u64 v[222:223], v[168:169], 0, s[16:17]
	s_mov_b32 m0, s87
	s_nop 0
	global_load_lds_dwordx4 v[222:223], off
	s_waitcnt vmcnt(8)
	s_waitcnt lgkmcnt(0)
	s_barrier
	s_waitcnt lgkmcnt(0)
	v_mfma_f32_16x16x128_f8f6f4 v[152:155], v[0:7], v[190:197], v[152:155]
	v_mfma_f32_16x16x128_f8f6f4 v[144:147], v[8:15], v[190:197], v[144:147]
	v_mfma_f32_16x16x128_f8f6f4 v[136:139], v[0:7], v[198:205], v[136:139]
	v_mfma_f32_16x16x128_f8f6f4 v[128:131], v[8:15], v[198:205], v[128:131]
	v_mfma_f32_16x16x128_f8f6f4 v[120:123], v[0:7], v[206:213], v[120:123]
	v_mfma_f32_16x16x128_f8f6f4 v[112:115], v[8:15], v[206:213], v[112:115]
	v_mfma_f32_16x16x128_f8f6f4 v[104:107], v[0:7], v[214:221], v[104:107]
	v_mfma_f32_16x16x128_f8f6f4 v[96:99], v[8:15], v[214:221], v[96:99]
	v_mfma_f32_16x16x128_f8f6f4 v[156:159], v[16:23], v[190:197], v[156:159]
	v_mfma_f32_16x16x128_f8f6f4 v[148:151], v[24:31], v[190:197], v[148:151]
	v_mfma_f32_16x16x128_f8f6f4 v[140:143], v[16:23], v[198:205], v[140:143]
	v_mfma_f32_16x16x128_f8f6f4 v[132:135], v[24:31], v[198:205], v[132:135]
	v_mfma_f32_16x16x128_f8f6f4 v[124:127], v[16:23], v[206:213], v[124:127]
	v_mfma_f32_16x16x128_f8f6f4 v[116:119], v[24:31], v[206:213], v[116:119]
	v_mfma_f32_16x16x128_f8f6f4 v[108:111], v[16:23], v[214:221], v[108:111]
	v_mfma_f32_16x16x128_f8f6f4 v[100:103], v[24:31], v[214:221], v[100:103]
	s_barrier
	s_mov_b32 m0, s91
	v_lshl_add_u64 v[222:223], v[166:167], 0, s[56:57]
	ds_read_b128 v[190:193], v188 offset:49152
	ds_read_b128 v[194:197], v188 offset:50176
	ds_read_b128 v[198:201], v188 offset:51200
	ds_read_b128 v[202:205], v188 offset:52224
	ds_read_b128 v[206:209], v188 offset:53248
	ds_read_b128 v[210:213], v188 offset:54272
	ds_read_b128 v[214:217], v188 offset:55296
	ds_read_b128 v[218:221], v188 offset:56320
	global_load_lds_dwordx4 v[222:223], off
	v_lshl_add_u64 v[222:223], v[166:167], 0, s[28:29]
	s_mov_b32 m0, s93
	s_nop 0
	global_load_lds_dwordx4 v[222:223], off
	v_lshl_add_u64 v[222:223], v[166:167], 0, s[0:1]
	s_mov_b32 m0, s41
	v_lshl_add_u64 v[166:167], v[166:167], 0, s[4:5]
	global_load_lds_dwordx4 v[222:223], off
	s_mov_b32 m0, s31
	s_nop 0
	global_load_lds_dwordx4 v[166:167], off
	v_lshl_add_u64 v[166:167], v[168:169], 0, s[56:57]
	s_mov_b32 m0, s95
	s_nop 0
	global_load_lds_dwordx4 v[166:167], off
	v_lshl_add_u64 v[166:167], v[168:169], 0, s[28:29]
	s_mov_b32 m0, s40
	s_nop 0
	global_load_lds_dwordx4 v[166:167], off
	s_waitcnt vmcnt(8)
	s_waitcnt lgkmcnt(0)
	s_barrier
	s_waitcnt lgkmcnt(0)
	v_mfma_f32_16x16x128_f8f6f4 v[88:91], v[0:7], v[190:197], v[88:91]
	v_mfma_f32_16x16x128_f8f6f4 v[80:83], v[8:15], v[190:197], v[80:83]
	v_mfma_f32_16x16x128_f8f6f4 v[72:75], v[0:7], v[198:205], v[72:75]
	v_mfma_f32_16x16x128_f8f6f4 v[64:67], v[8:15], v[198:205], v[64:67]
	v_mfma_f32_16x16x128_f8f6f4 v[56:59], v[0:7], v[206:213], v[56:59]
	v_mfma_f32_16x16x128_f8f6f4 v[48:51], v[8:15], v[206:213], v[48:51]
	v_mfma_f32_16x16x128_f8f6f4 v[36:39], v[0:7], v[214:221], v[36:39]
	v_mfma_f32_16x16x128_f8f6f4 v[32:35], v[8:15], v[214:221], v[32:35]
	v_mfma_f32_16x16x128_f8f6f4 v[92:95], v[16:23], v[190:197], v[92:95]
	v_mfma_f32_16x16x128_f8f6f4 v[84:87], v[24:31], v[190:197], v[84:87]
	v_mfma_f32_16x16x128_f8f6f4 v[76:79], v[16:23], v[198:205], v[76:79]
	v_mfma_f32_16x16x128_f8f6f4 v[68:71], v[24:31], v[198:205], v[68:71]
	v_mfma_f32_16x16x128_f8f6f4 v[60:63], v[16:23], v[206:213], v[60:63]
	v_mfma_f32_16x16x128_f8f6f4 v[52:55], v[24:31], v[206:213], v[52:55]
	v_mfma_f32_16x16x128_f8f6f4 v[40:43], v[16:23], v[214:221], v[40:43]
	v_mfma_f32_16x16x128_f8f6f4 v[44:47], v[24:31], v[214:221], v[44:47]
	s_barrier
	s_add_u32 vcc_lo, vcc_lo, 0x100
	s_addc_u32 vcc_hi, vcc_hi, 0
	s_add_u32 s38, s38, 0x100
	s_addc_u32 s39, s39, 0
	s_cmp_ge_i32 s18, s11
	s_mov_b32 s2, s18
	s_cbranch_scc0 .LBB0_1705

.LBB0_1780:
	ds_read_b128 v[20:23], v173
	ds_read_b128 v[24:27], v174
	ds_read_b128 v[16:19], v169
	ds_read_b128 v[0:3], v170
	ds_read_b128 v[28:31], v175
	ds_read_b128 v[4:7], v176
	ds_read_b128 v[8:11], v177
	ds_read_b128 v[12:15], v178
	s_add_i32 vcc_lo, s2, 2
	s_add_u32 s22, s54, 0xfff90080
	s_addc_u32 s3, s55, -1
	s_cmp_eq_u32 s86, s2
	s_cselect_b32 s2, s48, s22
	s_cselect_b32 s3, s49, s3
	s_cselect_b32 s23, s51, s96
	s_cselect_b32 s22, s50, s47
	v_lshl_add_u64 v[164:165], s[54:55], 0, v[162:163]
	s_add_i32 m0, s31, 0xc000
	ds_read_b128 v[188:191], v186
	ds_read_b128 v[192:195], v186 offset:1024
	ds_read_b128 v[196:199], v186 offset:2048
	ds_read_b128 v[200:203], v186 offset:3072
	ds_read_b128 v[204:207], v186 offset:4096
	ds_read_b128 v[208:211], v186 offset:5120
	ds_read_b128 v[212:215], v186 offset:6144
	ds_read_b128 v[216:219], v186 offset:7168
	global_load_lds_dwordx4 v[164:165], off
	v_lshl_add_u64 v[164:165], v[164:165], 0, s[20:21]
	s_add_i32 m0, s31, 0xe000
	s_nop 0
	global_load_lds_dwordx4 v[164:165], off
	s_waitcnt vmcnt(8)
	s_waitcnt lgkmcnt(0)
	s_barrier
	s_waitcnt lgkmcnt(0)
	v_mfma_f32_16x16x128_f8f6f4 v[156:159], v[16:23], v[188:195], v[156:159]
	v_mfma_f32_16x16x128_f8f6f4 v[152:155], v[24:31], v[188:195], v[152:155]
	v_mfma_f32_16x16x128_f8f6f4 v[140:143], v[16:23], v[196:203], v[140:143]
	v_mfma_f32_16x16x128_f8f6f4 v[136:139], v[24:31], v[196:203], v[136:139]
	v_mfma_f32_16x16x128_f8f6f4 v[124:127], v[16:23], v[204:211], v[124:127]
	v_mfma_f32_16x16x128_f8f6f4 v[120:123], v[24:31], v[204:211], v[120:123]
	v_mfma_f32_16x16x128_f8f6f4 v[108:111], v[16:23], v[212:219], v[108:111]
	v_mfma_f32_16x16x128_f8f6f4 v[104:107], v[24:31], v[212:219], v[104:107]
	v_mfma_f32_16x16x128_f8f6f4 v[148:151], v[0:7], v[188:195], v[148:151]
	v_mfma_f32_16x16x128_f8f6f4 v[144:147], v[8:15], v[188:195], v[144:147]
	v_mfma_f32_16x16x128_f8f6f4 v[132:135], v[0:7], v[196:203], v[132:135]
	v_mfma_f32_16x16x128_f8f6f4 v[128:131], v[8:15], v[196:203], v[128:131]
	v_mfma_f32_16x16x128_f8f6f4 v[116:119], v[0:7], v[204:211], v[116:119]
	v_mfma_f32_16x16x128_f8f6f4 v[112:115], v[8:15], v[204:211], v[112:115]
	v_mfma_f32_16x16x128_f8f6f4 v[100:103], v[0:7], v[212:219], v[100:103]
	v_mfma_f32_16x16x128_f8f6f4 v[96:99], v[8:15], v[212:219], v[96:99]
	s_barrier
	s_mov_b32 m0, s33
	v_lshl_add_u64 v[164:165], s[22:23], 0, v[160:161]
	ds_read_b128 v[188:191], v186 offset:16384
	ds_read_b128 v[192:195], v186 offset:17408
	ds_read_b128 v[196:199], v186 offset:18432
	ds_read_b128 v[200:203], v186 offset:19456
	ds_read_b128 v[204:207], v186 offset:20480
	ds_read_b128 v[208:211], v186 offset:21504
	ds_read_b128 v[212:215], v186 offset:22528
	ds_read_b128 v[216:219], v186 offset:23552
	global_load_lds_dwordx4 v[164:165], off
	v_lshl_add_u64 v[166:167], v[164:165], 0, s[20:21]
	s_mov_b32 m0, s35
	s_nop 0
	global_load_lds_dwordx4 v[166:167], off
	v_lshl_add_u64 v[166:167], v[164:165], 0, s[84:85]
	s_mov_b32 m0, s39
	s_nop 0
	global_load_lds_dwordx4 v[166:167], off
	v_lshl_add_u64 v[166:167], v[164:165], 0, s[12:13]
	s_mov_b32 m0, s58
	s_nop 0
	global_load_lds_dwordx4 v[166:167], off
	v_lshl_add_u64 v[166:167], s[2:3], 0, v[160:161]
	s_mov_b32 m0, s31
	v_lshl_add_u64 v[220:221], v[166:167], 0, s[20:21]
	global_load_lds_dwordx4 v[166:167], off
	s_mov_b32 m0, s59
	s_nop 0
	global_load_lds_dwordx4 v[220:221], off
	s_waitcnt vmcnt(8)
	s_waitcnt lgkmcnt(0)
	s_barrier
	s_waitcnt lgkmcnt(0)
	v_mfma_f32_16x16x128_f8f6f4 v[92:95], v[16:23], v[188:195], v[92:95]
	v_mfma_f32_16x16x128_f8f6f4 v[88:91], v[24:31], v[188:195], v[88:91]
	v_mfma_f32_16x16x128_f8f6f4 v[76:79], v[16:23], v[196:203], v[76:79]
	v_mfma_f32_16x16x128_f8f6f4 v[72:75], v[24:31], v[196:203], v[72:75]
	v_mfma_f32_16x16x128_f8f6f4 v[60:63], v[16:23], v[204:211], v[60:63]
	v_mfma_f32_16x16x128_f8f6f4 v[56:59], v[24:31], v[204:211], v[56:59]
	v_mfma_f32_16x16x128_f8f6f4 v[44:47], v[16:23], v[212:219], v[44:47]
	v_mfma_f32_16x16x128_f8f6f4 v[40:43], v[24:31], v[212:219], v[40:43]
	v_mfma_f32_16x16x128_f8f6f4 v[84:87], v[0:7], v[188:195], v[84:87]
	v_mfma_f32_16x16x128_f8f6f4 v[80:83], v[8:15], v[188:195], v[80:83]
	v_mfma_f32_16x16x128_f8f6f4 v[68:71], v[0:7], v[196:203], v[68:71]
	v_mfma_f32_16x16x128_f8f6f4 v[64:67], v[8:15], v[196:203], v[64:67]
	v_mfma_f32_16x16x128_f8f6f4 v[52:55], v[0:7], v[204:211], v[52:55]
	v_mfma_f32_16x16x128_f8f6f4 v[48:51], v[8:15], v[204:211], v[48:51]
	v_mfma_f32_16x16x128_f8f6f4 v[36:39], v[0:7], v[212:219], v[36:39]
	v_mfma_f32_16x16x128_f8f6f4 v[32:35], v[8:15], v[212:219], v[32:35]
	s_barrier
	ds_read_b128 v[4:7], v179
	ds_read_b128 v[8:11], v180
	ds_read_b128 v[0:3], v171
	ds_read_b128 v[16:19], v172
	ds_read_b128 v[12:15], v181
	ds_read_b128 v[20:23], v182
	ds_read_b128 v[24:27], v183
	ds_read_b128 v[28:31], v184
	s_mov_b32 m0, s63
	v_lshl_add_u64 v[220:221], v[166:167], 0, s[84:85]
	ds_read_b128 v[188:191], v186 offset:32768
	ds_read_b128 v[192:195], v186 offset:33792
	ds_read_b128 v[196:199], v186 offset:34816
	ds_read_b128 v[200:203], v186 offset:35840
	ds_read_b128 v[204:207], v186 offset:36864
	ds_read_b128 v[208:211], v186 offset:37888
	ds_read_b128 v[212:215], v186 offset:38912
	ds_read_b128 v[216:219], v186 offset:39936
	global_load_lds_dwordx4 v[220:221], off
	v_lshl_add_u64 v[220:221], v[166:167], 0, s[12:13]
	s_mov_b32 m0, s74
	s_nop 0
	global_load_lds_dwordx4 v[220:221], off
	s_waitcnt vmcnt(8)
	s_waitcnt lgkmcnt(0)
	s_barrier
	s_waitcnt lgkmcnt(0)
	v_mfma_f32_16x16x128_f8f6f4 v[156:159], v[0:7], v[188:195], v[156:159]
	v_mfma_f32_16x16x128_f8f6f4 v[152:155], v[8:15], v[188:195], v[152:155]
	v_mfma_f32_16x16x128_f8f6f4 v[140:143], v[0:7], v[196:203], v[140:143]
	v_mfma_f32_16x16x128_f8f6f4 v[136:139], v[8:15], v[196:203], v[136:139]
	v_mfma_f32_16x16x128_f8f6f4 v[124:127], v[0:7], v[204:211], v[124:127]
	v_mfma_f32_16x16x128_f8f6f4 v[120:123], v[8:15], v[204:211], v[120:123]
	v_mfma_f32_16x16x128_f8f6f4 v[108:111], v[0:7], v[212:219], v[108:111]
	v_mfma_f32_16x16x128_f8f6f4 v[104:107], v[8:15], v[212:219], v[104:107]
	v_mfma_f32_16x16x128_f8f6f4 v[148:151], v[16:23], v[188:195], v[148:151]
	v_mfma_f32_16x16x128_f8f6f4 v[144:147], v[24:31], v[188:195], v[144:147]
	v_mfma_f32_16x16x128_f8f6f4 v[132:135], v[16:23], v[196:203], v[132:135]
	v_mfma_f32_16x16x128_f8f6f4 v[128:131], v[24:31], v[196:203], v[128:131]
	v_mfma_f32_16x16x128_f8f6f4 v[116:119], v[16:23], v[204:211], v[116:119]
	v_mfma_f32_16x16x128_f8f6f4 v[112:115], v[24:31], v[204:211], v[112:115]
	v_mfma_f32_16x16x128_f8f6f4 v[100:103], v[16:23], v[212:219], v[100:103]
	v_mfma_f32_16x16x128_f8f6f4 v[96:99], v[24:31], v[212:219], v[96:99]
	s_barrier
	s_mov_b32 m0, s75
	v_lshl_add_u64 v[220:221], v[164:165], 0, s[56:57]
	ds_read_b128 v[188:191], v186 offset:49152
	ds_read_b128 v[192:195], v186 offset:50176
	ds_read_b128 v[196:199], v186 offset:51200
	ds_read_b128 v[200:203], v186 offset:52224
	ds_read_b128 v[204:207], v186 offset:53248
	ds_read_b128 v[208:211], v186 offset:54272
	ds_read_b128 v[212:215], v186 offset:55296
	ds_read_b128 v[216:219], v186 offset:56320
	global_load_lds_dwordx4 v[220:221], off
	v_lshl_add_u64 v[220:221], v[164:165], 0, s[64:65]
	s_mov_b32 m0, s77
	s_nop 0
	global_load_lds_dwordx4 v[220:221], off
	v_lshl_add_u64 v[220:221], v[164:165], 0, s[4:5]
	s_mov_b32 m0, s80
	v_lshl_add_u64 v[164:165], v[164:165], 0, s[72:73]
	global_load_lds_dwordx4 v[220:221], off
	s_mov_b32 m0, s81
	s_nop 0
	global_load_lds_dwordx4 v[164:165], off
	v_lshl_add_u64 v[164:165], v[166:167], 0, s[56:57]
	s_mov_b32 m0, s78
	s_nop 0
	global_load_lds_dwordx4 v[164:165], off
	v_lshl_add_u64 v[164:165], v[166:167], 0, s[64:65]
	s_mov_b32 m0, s79
	s_nop 0
	global_load_lds_dwordx4 v[164:165], off
	s_waitcnt vmcnt(8)
	s_waitcnt lgkmcnt(0)
	s_barrier
	s_waitcnt lgkmcnt(0)
	v_mfma_f32_16x16x128_f8f6f4 v[92:95], v[0:7], v[188:195], v[92:95]
	v_mfma_f32_16x16x128_f8f6f4 v[88:91], v[8:15], v[188:195], v[88:91]
	v_mfma_f32_16x16x128_f8f6f4 v[76:79], v[0:7], v[196:203], v[76:79]
	v_mfma_f32_16x16x128_f8f6f4 v[72:75], v[8:15], v[196:203], v[72:75]
	v_mfma_f32_16x16x128_f8f6f4 v[60:63], v[0:7], v[204:211], v[60:63]
	v_mfma_f32_16x16x128_f8f6f4 v[56:59], v[8:15], v[204:211], v[56:59]
	v_mfma_f32_16x16x128_f8f6f4 v[44:47], v[0:7], v[212:219], v[44:47]
	v_mfma_f32_16x16x128_f8f6f4 v[40:43], v[8:15], v[212:219], v[40:43]
	v_mfma_f32_16x16x128_f8f6f4 v[84:87], v[16:23], v[188:195], v[84:87]
	v_mfma_f32_16x16x128_f8f6f4 v[80:83], v[24:31], v[188:195], v[80:83]
	v_mfma_f32_16x16x128_f8f6f4 v[68:71], v[16:23], v[196:203], v[68:71]
	v_mfma_f32_16x16x128_f8f6f4 v[64:67], v[24:31], v[196:203], v[64:67]
	v_mfma_f32_16x16x128_f8f6f4 v[52:55], v[16:23], v[204:211], v[52:55]
	v_mfma_f32_16x16x128_f8f6f4 v[48:51], v[24:31], v[204:211], v[48:51]
	v_mfma_f32_16x16x128_f8f6f4 v[36:39], v[16:23], v[212:219], v[36:39]
	v_mfma_f32_16x16x128_f8f6f4 v[32:35], v[24:31], v[212:219], v[32:35]
	s_barrier
	s_add_u32 s47, s47, 0x100
	s_addc_u32 s96, s96, 0
	s_add_u32 s54, s54, 0x100
	s_addc_u32 s55, s55, 0
	s_cmp_ge_i32 vcc_lo, s83
	s_mov_b32 s2, vcc_lo
	s_cbranch_scc0 .LBB0_1780
